# expert-weight conversion work queue dealt in chunks of 32 items (4 per wave) instead of 128: same conversion work, finer load balance at the end of the attention phase; on top of previous stack
# speedup vs baseline: 1.0091x; 1.0007x over previous
; __device__ __forceinline__ unsigned xb_add(gbar_t p, unsigned v) { return __hip_atomic_fetch_add(p, v, __ATOMIC_RELAXED, __HIP_MEMORY_SCOPE_AGENT); }
; __device__ __forceinline__ ConvItem moe_conv_desc(const Args& a, ARGAS unsigned char* ws, int it, int lane) {
;     const int m = it / MOE_CONV_PER_M, r = it % MOE_CONV_PER_M, nl = lane & 15, kg = lane >> 4; ConvItem d;
;     if (r < 256) { const int kb = r / 32, nb = r % 32; d.N = 2048; d.ldk = DM; d.gu = 64 * nb + 1; d.src = a.moe_w_gu + (size_t)m * DM * 2048 + (size_t)(128 * kb + 4 * kg) * 2048 + 64 * nb + 4 * nl; d.dst = (unsigned char*)(ws + WS_WGU) + (size_t)m * 2048 * DM + 128 * kb; }
;     else { const int r2 = r - 256, kb = r2 / 16, nb = r2 % 16; d.N = DM; d.ldk = EFF; d.gu = -(64 * nb) - 1; d.src = a.moe_w_down + (size_t)m * EFF * DM + (size_t)(128 * kb + 4 * kg) * DM + 64 * nb + 4 * nl; d.dst = (unsigned char*)(ws + WS_WDN) + (size_t)m * DM * EFF + 128 * kb; }
;     return d;
; __device__ __forceinline__ void moe_conv_drain(const Frame& F, const Args& a, ARGAS unsigned char* ws, gbar_t head, LAS unsigned* qslot, const int first_chunk, const int nchunks) {
;     ...
;         __syncthreads();
;         if (F.tid == 0) *qslot = xb_add(head, 1u);
;         __syncthreads();
;         const unsigned ch = *qslot;
;         if (ch >= (unsigned)nchunks) break;
;         moe_conv_stream(a, ws, scr, (first_chunk + (int)ch) * MOE_CONV_CHUNK + F.wave, MOE_CONV_CHUNK / 8, F.lane);
.LBB0_580:
	s_or_b64 exec, exec, s[8:9]
	s_waitcnt lgkmcnt(0)
	s_barrier
	s_waitcnt vmcnt(27)
	ds_read_b32 v0, v144
	s_mov_b64 s[8:9], -1
	s_waitcnt lgkmcnt(0)
	s_movk_i32 s98, 0x2ff
	v_cmp_lt_u32_e32 vcc, s98, v0
	v_readfirstlane_b32 s6, v0
	s_cbranch_vccnz .LBB0_575
	s_lshl_b32 s38, s6, 5
	s_add_i32 s38, s38, s45
	s_mul_hi_i32 s6, s38, 0x2aaaaaab
	s_lshr_b32 s8, s6, 31
	s_ashr_i32 s6, s6, 6
	s_add_i32 s10, s6, s8
	s_mul_i32 s6, s10, 0x180
	s_sub_i32 s14, s38, s6
	s_cmpk_gt_i32 s14, 0xff
	s_cbranch_scc0 .LBB0_583
	s_load_dwordx2 s[8:9], s[20:21], 0xe0
	s_lshl_b32 s6, s14, 6
	s_and_b32 s6, s6, 0x3c0
	s_ashr_i32 s11, s10, 31
	s_not_b32 s39, s6
	s_lshl_b64 s[12:13], s[10:11], 20
	s_lshl_b64 s[40:41], s[10:11], 22
	s_waitcnt lgkmcnt(0)
	s_add_u32 s8, s8, s40
	s_addc_u32 s9, s9, s41
	s_lshl_b32 s11, s14, 3
	s_and_b32 s11, s11, 0x7fffff80
	s_addk_i32 s11, 0xf800
	v_or_b32_e32 v0, s11, v136
	v_mov_b32_e32 v1, v129
	v_lshlrev_b64 v[0:1], 12, v[0:1]
	v_lshl_add_u64 v[0:1], s[8:9], 0, v[0:1]
	s_lshl_b32 s6, s6, 2
	v_lshl_add_u64 v[0:1], v[0:1], 0, s[6:7]
	s_add_u32 s6, s16, s12
	s_addc_u32 s9, s17, s13
	s_add_u32 s8, s6, s11
	s_addc_u32 s9, s9, 0
	s_movk_i32 s11, 0x400
	s_cbranch_execz .LBB0_584
	s_branch .LBB0_585

; #define CV_LOAD(qi, Q, D) do { _Pragma("unroll") for (int s_ = 0; s_ < 2; ++s_) _Pragma("unroll") for (int r_ = 0; r_ < 4; ++r_) Q.v[s_][r_] = *(const f32x4*)(D.src + (size_t)(16 * (2 * (qi) + s_) + r_) * D.N); asm volatile("" ::: "memory"); } while (0)
; #define CV_PROC(qi, Q) do { _Pragma("unroll") for (int s_ = 0; s_ < 2; ++s_) _Pragma("unroll") for (int c_ = 0; c_ < 4; ++c_) \
;         *(LAS unsigned*)(scr + (4 * nl + c_) * 132 + 16 * (2 * (qi) + s_) + 4 * kg) = pg8::pk4_fp8c(Q.v[s_][0][c_] * FP8_WSC, Q.v[s_][1][c_] * FP8_WSC, Q.v[s_][2][c_] * FP8_WSC, Q.v[s_][3][c_] * FP8_WSC); asm volatile("" ::: "memory"); } while (0)
; __device__ __forceinline__ void moe_conv_stream(const Args& a, ARGAS unsigned char* ws, LAS unsigned char* scr, int first, int cnt, int lane) {
;     ...
;     Qt A, B, C, D4;
;     ConvItem cur = moe_conv_desc(a, ws, first, lane);
;     CV_LOAD(0, A, cur); CV_LOAD(1, B, cur); CV_LOAD(2, C, cur);
; #pragma unroll 1
;     for (int i = 0; i < cnt; ++i) {
;         const ConvItem nxt = moe_conv_desc(a, ws, first + 8 * ((i + 1 < cnt) ? i + 1 : i), lane);
;         CV_LOAD(3, D4, cur); CV_PROC(0, A);
;         CV_LOAD(0, A, nxt);  CV_PROC(1, B);
;         CV_LOAD(1, B, nxt);  CV_PROC(2, C);
;         CV_LOAD(2, C, nxt);  CV_PROC(3, D4);
.LBB0_586:
	s_waitcnt vmcnt(17)
	v_mul_f32_e32 v28, 0x43000000, v28
	v_mul_f32_e32 v16, 0x43000000, v16
	v_med3_f32 v28, v28, s36, v149
	v_med3_f32 v16, v16, s36, v149
	v_mov_b32_e32 v150, v129
	v_cvt_pk_fp8_f32 v150, v28, v16
	v_mul_f32_e32 v20, 0x43000000, v20
	v_mul_f32_e32 v16, 0x43000000, v24
	v_med3_f32 v20, v20, s36, v149
	v_med3_f32 v16, v16, s36, v149
	v_cvt_pk_fp8_f32 v150, v20, v16 op_sel:[0,0,1]
	v_mul_f32_e32 v16, 0x43000000, v29
	v_mul_f32_e32 v17, 0x43000000, v17
	v_mul_f32_e32 v20, 0x43000000, v21
	v_med3_f32 v16, v16, s36, v149
	v_med3_f32 v17, v17, s36, v149
	v_mov_b32_e32 v21, v129
	v_cvt_pk_fp8_f32 v21, v16, v17
	v_mul_f32_e32 v16, 0x43000000, v25
	v_med3_f32 v17, v20, s36, v149
	v_med3_f32 v16, v16, s36, v149
	v_cvt_pk_fp8_f32 v21, v17, v16 op_sel:[0,0,1]
	v_mul_f32_e32 v16, 0x43000000, v30
	v_mul_f32_e32 v17, 0x43000000, v18
	v_med3_f32 v16, v16, s36, v149
	v_med3_f32 v17, v17, s36, v149
	v_mov_b32_e32 v20, v129
	v_cvt_pk_fp8_f32 v20, v16, v17
	v_mul_f32_e32 v18, 0x43000000, v22
	v_mul_f32_e32 v16, 0x43000000, v26
	v_med3_f32 v17, v18, s36, v149
	v_med3_f32 v16, v16, s36, v149
	v_cvt_pk_fp8_f32 v20, v17, v16 op_sel:[0,0,1]
	v_mul_f32_e32 v16, 0x43000000, v31
	v_mul_f32_e32 v17, 0x43000000, v19
	v_med3_f32 v16, v16, s36, v149
	v_med3_f32 v17, v17, s36, v149
	v_mov_b32_e32 v19, v129
	v_cvt_pk_fp8_f32 v19, v16, v17
	v_mul_f32_e32 v18, 0x43000000, v23
	v_mul_f32_e32 v16, 0x43000000, v27
	v_med3_f32 v17, v18, s36, v149
	v_med3_f32 v16, v16, s36, v149
	v_mul_f32_e32 v0, 0x43000000, v0
	v_mul_f32_e32 v4, 0x43000000, v4
	v_cvt_pk_fp8_f32 v19, v17, v16 op_sel:[0,0,1]
	v_med3_f32 v0, v0, s36, v149
	v_med3_f32 v4, v4, s36, v149
	v_mov_b32_e32 v16, v129
	v_cvt_pk_fp8_f32 v16, v0, v4
	v_mul_f32_e32 v8, 0x43000000, v8
	s_waitcnt vmcnt(16)
	v_mul_f32_e32 v0, 0x43000000, v12
	v_med3_f32 v4, v8, s36, v149
	v_med3_f32 v0, v0, s36, v149
	v_cvt_pk_fp8_f32 v16, v4, v0 op_sel:[0,0,1]
	v_mul_f32_e32 v0, 0x43000000, v1
	v_mul_f32_e32 v1, 0x43000000, v5
	v_med3_f32 v0, v0, s36, v149
	v_med3_f32 v1, v1, s36, v149
	v_mov_b32_e32 v5, v129
	v_cvt_pk_fp8_f32 v5, v0, v1
	v_mul_f32_e32 v4, 0x43000000, v9
	v_mul_f32_e32 v0, 0x43000000, v13
	v_med3_f32 v1, v4, s36, v149
	v_med3_f32 v0, v0, s36, v149
	v_cvt_pk_fp8_f32 v5, v1, v0 op_sel:[0,0,1]
	v_mul_f32_e32 v0, 0x43000000, v2
	v_mul_f32_e32 v1, 0x43000000, v6
	v_med3_f32 v0, v0, s36, v149
	v_med3_f32 v1, v1, s36, v149
	v_mov_b32_e32 v4, v129
	v_cvt_pk_fp8_f32 v4, v0, v1
	v_mad_u64_u32 v[96:97], s[14:15], s6, v148, v[96:97]
	v_mul_f32_e32 v2, 0x43000000, v10
	v_mul_f32_e32 v0, 0x43000000, v14
	s_lshl_b64 s[14:15], s[6:7], 2
	v_med3_f32 v1, v2, s36, v149
	v_med3_f32 v0, v0, s36, v149
	v_lshl_add_u64 v[132:133], v[98:99], 0, v[128:129]
	v_lshl_add_u64 v[98:99], v[96:97], 0, s[14:15]
	v_cvt_pk_fp8_f32 v4, v1, v0 op_sel:[0,0,1]
	v_mul_f32_e32 v0, 0x43000000, v3
	v_mul_f32_e32 v1, 0x43000000, v7
	global_load_dwordx4 v[116:119], v[96:97], off
	global_load_dwordx4 v[120:123], v[98:99], off
	v_lshl_add_u64 v[96:97], v[98:99], 0, s[14:15]
	v_med3_f32 v0, v0, s36, v149
	v_med3_f32 v1, v1, s36, v149
	v_mov_b32_e32 v3, v129
	v_lshl_add_u64 v[98:99], v[96:97], 0, s[14:15]
	v_cvt_pk_fp8_f32 v3, v0, v1
	global_load_dwordx4 v[124:127], v[96:97], off
	global_load_dwordx4 v[112:115], v[98:99], off
	v_mad_u64_u32 v[96:97], s[42:43], s6, 52, v[98:99]
	v_lshl_add_u64 v[98:99], v[96:97], 0, s[14:15]
	v_mul_f32_e32 v2, 0x43000000, v11
	v_mul_f32_e32 v0, 0x43000000, v15
	global_load_dwordx4 v[100:103], v[96:97], off
	global_load_dwordx4 v[104:107], v[98:99], off
	v_lshl_add_u64 v[96:97], v[98:99], 0, s[14:15]
	v_med3_f32 v1, v2, s36, v149
	v_med3_f32 v0, v0, s36, v149
	v_lshl_add_u64 v[98:99], v[96:97], 0, s[14:15]
	v_cvt_pk_fp8_f32 v3, v1, v0 op_sel:[0,0,1]
	s_waitcnt vmcnt(21)
	v_mul_f32_e32 v40, 0x43000000, v40
	s_waitcnt vmcnt(20)
	v_mul_f32_e32 v48, 0x43000000, v48
	global_load_dwordx4 v[108:111], v[96:97], off
	s_nop 0
	global_load_dwordx4 v[96:99], v[98:99], off
	ds_write2_b32 v145, v150, v16 offset1:4
	ds_write2_b32 v145, v21, v5 offset0:33 offset1:37
	ds_write2_b32 v145, v20, v4 offset0:66 offset1:70
	ds_write2_b32 v145, v19, v3 offset0:99 offset1:103
	v_med3_f32 v40, v40, s36, v149
	v_med3_f32 v48, v48, s36, v149
	v_mov_b32_e32 v150, v129
	v_cvt_pk_fp8_f32 v150, v40, v48
	s_waitcnt vmcnt(21)
	v_mul_f32_e32 v60, 0x43000000, v60
	s_waitcnt vmcnt(20)
	v_mul_f32_e32 v40, 0x43000000, v56
	v_med3_f32 v48, v60, s36, v149
	v_med3_f32 v40, v40, s36, v149
	v_cvt_pk_fp8_f32 v150, v48, v40 op_sel:[0,0,1]
	v_mul_f32_e32 v40, 0x43000000, v41
	v_mul_f32_e32 v41, 0x43000000, v49
	v_med3_f32 v40, v40, s36, v149
	v_med3_f32 v41, v41, s36, v149
	v_mov_b32_e32 v49, v129
	v_cvt_pk_fp8_f32 v49, v40, v41
	v_mul_f32_e32 v48, 0x43000000, v61
	v_mul_f32_e32 v40, 0x43000000, v57
	v_med3_f32 v41, v48, s36, v149
	v_med3_f32 v40, v40, s36, v149
	v_cvt_pk_fp8_f32 v49, v41, v40 op_sel:[0,0,1]
	v_mul_f32_e32 v40, 0x43000000, v42
	v_mul_f32_e32 v41, 0x43000000, v50
	v_med3_f32 v40, v40, s36, v149
	v_med3_f32 v41, v41, s36, v149
	v_mov_b32_e32 v48, v129
	v_cvt_pk_fp8_f32 v48, v40, v41
	v_mul_f32_e32 v42, 0x43000000, v62
	v_mul_f32_e32 v40, 0x43000000, v58
	v_med3_f32 v41, v42, s36, v149
	v_med3_f32 v40, v40, s36, v149
	v_cvt_pk_fp8_f32 v48, v41, v40 op_sel:[0,0,1]
	v_mul_f32_e32 v40, 0x43000000, v43
	v_mul_f32_e32 v41, 0x43000000, v51
	v_med3_f32 v40, v40, s36, v149
	v_med3_f32 v41, v41, s36, v149
	v_mov_b32_e32 v43, v129
	v_cvt_pk_fp8_f32 v43, v40, v41
	v_mul_f32_e32 v42, 0x43000000, v63
	v_mul_f32_e32 v40, 0x43000000, v59
	v_med3_f32 v41, v42, s36, v149
	v_med3_f32 v40, v40, s36, v149
	s_waitcnt vmcnt(19)
	v_mul_f32_e32 v32, 0x43000000, v32
	s_waitcnt vmcnt(18)
; #define CV_LOAD(qi, Q, D) do { _Pragma("unroll") for (int s_ = 0; s_ < 2; ++s_) _Pragma("unroll") for (int r_ = 0; r_ < 4; ++r_) Q.v[s_][r_] = *(const f32x4*)(D.src + (size_t)(16 * (2 * (qi) + s_) + r_) * D.N); asm volatile("" ::: "memory"); } while (0)
; #define CV_PROC(qi, Q) do { _Pragma("unroll") for (int s_ = 0; s_ < 2; ++s_) _Pragma("unroll") for (int c_ = 0; c_ < 4; ++c_) \
;         *(LAS unsigned*)(scr + (4 * nl + c_) * 132 + 16 * (2 * (qi) + s_) + 4 * kg) = pg8::pk4_fp8c(Q.v[s_][0][c_] * FP8_WSC, Q.v[s_][1][c_] * FP8_WSC, Q.v[s_][2][c_] * FP8_WSC, Q.v[s_][3][c_] * FP8_WSC); asm volatile("" ::: "memory"); } while (0)
; __device__ __forceinline__ void moe_conv_stream(const Args& a, ARGAS unsigned char* ws, LAS unsigned char* scr, int first, int cnt, int lane) {
;     ...
;     Qt A, B, C, D4;
;     ConvItem cur = moe_conv_desc(a, ws, first, lane);
;     CV_LOAD(0, A, cur); CV_LOAD(1, B, cur); CV_LOAD(2, C, cur);
; #pragma unroll 1
;     for (int i = 0; i < cnt; ++i) {
;         const ConvItem nxt = moe_conv_desc(a, ws, first + 8 * ((i + 1 < cnt) ? i + 1 : i), lane);
;         CV_LOAD(3, D4, cur); CV_PROC(0, A);
;         CV_LOAD(0, A, nxt);  CV_PROC(1, B);
;         CV_LOAD(1, B, nxt);  CV_PROC(2, C);
;         CV_LOAD(2, C, nxt);  CV_PROC(3, D4);
	v_mul_f32_e32 v36, 0x43000000, v36
	v_cvt_pk_fp8_f32 v43, v41, v40 op_sel:[0,0,1]
	v_med3_f32 v32, v32, s36, v149
	v_med3_f32 v36, v36, s36, v149
	v_mov_b32_e32 v41, v129
	v_cvt_pk_fp8_f32 v41, v32, v36
	s_waitcnt vmcnt(17)
	v_mul_f32_e32 v40, 0x43000000, v52
	s_waitcnt vmcnt(16)
	v_mul_f32_e32 v32, 0x43000000, v44
	v_med3_f32 v36, v40, s36, v149
	v_med3_f32 v32, v32, s36, v149
	v_cvt_pk_fp8_f32 v41, v36, v32 op_sel:[0,0,1]
	v_mul_f32_e32 v32, 0x43000000, v33
	v_mul_f32_e32 v33, 0x43000000, v37
	v_med3_f32 v32, v32, s36, v149
	v_med3_f32 v33, v33, s36, v149
	v_mov_b32_e32 v37, v129
	v_cvt_pk_fp8_f32 v37, v32, v33
	v_mul_f32_e32 v36, 0x43000000, v53
	v_mul_f32_e32 v32, 0x43000000, v45
	v_med3_f32 v33, v36, s36, v149
	v_med3_f32 v32, v32, s36, v149
	v_cvt_pk_fp8_f32 v37, v33, v32 op_sel:[0,0,1]
	v_mul_f32_e32 v32, 0x43000000, v34
	v_mul_f32_e32 v33, 0x43000000, v38
	v_med3_f32 v32, v32, s36, v149
	v_med3_f32 v33, v33, s36, v149
	v_mov_b32_e32 v36, v129
	v_cvt_pk_fp8_f32 v36, v32, v33
	v_mul_f32_e32 v34, 0x43000000, v54
	v_mul_f32_e32 v32, 0x43000000, v46
	s_lshl_b32 s6, s13, 2
	v_med3_f32 v33, v34, s36, v149
	v_med3_f32 v32, v32, s36, v149
	v_lshl_add_u64 v[0:1], v[132:133], 0, s[6:7]
	s_lshl_b32 s6, s13, 3
	v_cvt_pk_fp8_f32 v36, v33, v32 op_sel:[0,0,1]
	v_mul_f32_e32 v32, 0x43000000, v35
	v_mul_f32_e32 v33, 0x43000000, v39
	global_load_dwordx4 v[28:31], v[132:133], off
	global_load_dwordx4 v[16:19], v[0:1], off
	v_lshl_add_u64 v[0:1], v[132:133], 0, s[6:7]
	s_mul_i32 s6, s13, 12
	v_med3_f32 v32, v32, s36, v149
	v_med3_f32 v33, v33, s36, v149
	v_mov_b32_e32 v35, v129
	v_lshl_add_u64 v[2:3], v[132:133], 0, s[6:7]
	s_lshl_b32 s6, s13, 6
	v_cvt_pk_fp8_f32 v35, v32, v33
	global_load_dwordx4 v[20:23], v[0:1], off
	global_load_dwordx4 v[24:27], v[2:3], off
	v_lshl_add_u64 v[0:1], v[132:133], 0, s[6:7]
	s_mul_i32 s6, s13, 0x44
	v_lshl_add_u64 v[4:5], v[132:133], 0, s[6:7]
	s_mul_i32 s6, s13, 0x48
	v_mul_f32_e32 v34, 0x43000000, v55
	v_mul_f32_e32 v32, 0x43000000, v47
	v_lshl_add_u64 v[8:9], v[132:133], 0, s[6:7]
	s_mul_i32 s6, s13, 0x4c
	v_med3_f32 v33, v34, s36, v149
	v_med3_f32 v32, v32, s36, v149
	v_lshl_add_u64 v[12:13], v[132:133], 0, s[6:7]
	v_cvt_pk_fp8_f32 v35, v33, v32 op_sel:[0,0,1]
	s_waitcnt vmcnt(19)
	v_mul_f32_e32 v72, 0x43000000, v72
	s_waitcnt vmcnt(18)
	v_mul_f32_e32 v80, 0x43000000, v80
	global_load_dwordx4 v[0:3], v[0:1], off
	s_nop 0
	global_load_dwordx4 v[4:7], v[4:5], off
	s_nop 0
	global_load_dwordx4 v[8:11], v[8:9], off
	s_nop 0
	global_load_dwordx4 v[12:15], v[12:13], off
	ds_write2_b32 v146, v150, v41 offset0:8 offset1:12
	ds_write2_b32 v146, v49, v37 offset0:41 offset1:45
	ds_write2_b32 v146, v48, v36 offset0:74 offset1:78
	ds_write2_b32 v146, v43, v35 offset0:107 offset1:111
	v_med3_f32 v72, v72, s36, v149
	v_med3_f32 v80, v80, s36, v149
	v_mov_b32_e32 v150, v129
	v_cvt_pk_fp8_f32 v150, v72, v80
	s_waitcnt vmcnt(21)
	v_mul_f32_e32 v92, 0x43000000, v92
	s_waitcnt vmcnt(20)
	v_mul_f32_e32 v72, 0x43000000, v88
	v_med3_f32 v80, v92, s36, v149
	v_med3_f32 v72, v72, s36, v149
	v_cvt_pk_fp8_f32 v150, v80, v72 op_sel:[0,0,1]
	v_mul_f32_e32 v72, 0x43000000, v73
	v_mul_f32_e32 v73, 0x43000000, v81
	v_med3_f32 v72, v72, s36, v149
	v_med3_f32 v73, v73, s36, v149
	v_mov_b32_e32 v81, v129
	v_cvt_pk_fp8_f32 v81, v72, v73
	v_mul_f32_e32 v80, 0x43000000, v93
	v_mul_f32_e32 v72, 0x43000000, v89
	v_med3_f32 v73, v80, s36, v149
	v_med3_f32 v72, v72, s36, v149
	v_cvt_pk_fp8_f32 v81, v73, v72 op_sel:[0,0,1]
	v_mul_f32_e32 v72, 0x43000000, v74
	v_mul_f32_e32 v73, 0x43000000, v82
	v_med3_f32 v72, v72, s36, v149
	v_med3_f32 v73, v73, s36, v149
	v_mov_b32_e32 v80, v129
	v_cvt_pk_fp8_f32 v80, v72, v73
	v_mul_f32_e32 v74, 0x43000000, v94
	v_mul_f32_e32 v72, 0x43000000, v90
	v_med3_f32 v73, v74, s36, v149
	v_med3_f32 v72, v72, s36, v149
	v_cvt_pk_fp8_f32 v80, v73, v72 op_sel:[0,0,1]
	v_mul_f32_e32 v72, 0x43000000, v75
	v_mul_f32_e32 v73, 0x43000000, v83
	v_med3_f32 v72, v72, s36, v149
	v_med3_f32 v73, v73, s36, v149
	v_mov_b32_e32 v75, v129
	v_cvt_pk_fp8_f32 v75, v72, v73
	v_mul_f32_e32 v74, 0x43000000, v95
	v_mul_f32_e32 v72, 0x43000000, v91
	v_med3_f32 v73, v74, s36, v149
	v_med3_f32 v72, v72, s36, v149
	s_waitcnt vmcnt(19)
	v_mul_f32_e32 v64, 0x43000000, v64
	s_waitcnt vmcnt(18)
	v_mul_f32_e32 v68, 0x43000000, v68
	v_cvt_pk_fp8_f32 v75, v73, v72 op_sel:[0,0,1]
	v_med3_f32 v64, v64, s36, v149
	v_med3_f32 v68, v68, s36, v149
	v_mov_b32_e32 v73, v129
	v_cvt_pk_fp8_f32 v73, v64, v68
	s_waitcnt vmcnt(17)
	v_mul_f32_e32 v72, 0x43000000, v84
	s_waitcnt vmcnt(16)
	v_mul_f32_e32 v64, 0x43000000, v76
	v_med3_f32 v68, v72, s36, v149
	v_med3_f32 v64, v64, s36, v149
	v_cvt_pk_fp8_f32 v73, v68, v64 op_sel:[0,0,1]
	v_mul_f32_e32 v64, 0x43000000, v65
	v_mul_f32_e32 v65, 0x43000000, v69
	v_med3_f32 v64, v64, s36, v149
	v_med3_f32 v65, v65, s36, v149
	v_mov_b32_e32 v69, v129
	v_cvt_pk_fp8_f32 v69, v64, v65
	v_mul_f32_e32 v68, 0x43000000, v85
	v_mul_f32_e32 v64, 0x43000000, v77
	v_med3_f32 v65, v68, s36, v149
	v_med3_f32 v64, v64, s36, v149
	v_cvt_pk_fp8_f32 v69, v65, v64 op_sel:[0,0,1]
	v_mul_f32_e32 v64, 0x43000000, v66
	v_mul_f32_e32 v65, 0x43000000, v70
	v_med3_f32 v64, v64, s36, v149
	v_med3_f32 v65, v65, s36, v149
	v_mov_b32_e32 v68, v129
	v_cvt_pk_fp8_f32 v68, v64, v65
	s_lshl_b32 s6, s13, 7
	v_mul_f32_e32 v66, 0x43000000, v86
	v_mul_f32_e32 v64, 0x43000000, v78
	v_lshl_add_u64 v[32:33], v[132:133], 0, s[6:7]
	s_mul_i32 s6, s13, 0x84
	v_med3_f32 v65, v66, s36, v149
	v_med3_f32 v64, v64, s36, v149
	v_lshl_add_u64 v[34:35], v[132:133], 0, s[6:7]
	s_mul_i32 s6, s13, 0x88
	v_cvt_pk_fp8_f32 v68, v65, v64 op_sel:[0,0,1]
	v_mul_f32_e32 v64, 0x43000000, v67
	v_mul_f32_e32 v65, 0x43000000, v71
	global_load_dwordx4 v[40:43], v[32:33], off
	global_load_dwordx4 v[48:51], v[34:35], off
	v_lshl_add_u64 v[32:33], v[132:133], 0, s[6:7]
	s_mul_i32 s6, s13, 0x8c
	v_med3_f32 v64, v64, s36, v149
	v_med3_f32 v65, v65, s36, v149
	v_mov_b32_e32 v67, v129
	v_lshl_add_u64 v[34:35], v[132:133], 0, s[6:7]
	s_mul_i32 s6, s13, 0xc0
	v_cvt_pk_fp8_f32 v67, v64, v65
	global_load_dwordx4 v[60:63], v[32:33], off
	global_load_dwordx4 v[56:59], v[34:35], off
	v_lshl_add_u64 v[32:33], v[132:133], 0, s[6:7]
	s_mul_i32 s6, s13, 0xc4
	v_lshl_add_u64 v[36:37], v[132:133], 0, s[6:7]
	s_mul_i32 s6, s13, 0xc8
	v_mul_f32_e32 v66, 0x43000000, v87
	v_mul_f32_e32 v64, 0x43000000, v79
	v_lshl_add_u64 v[44:45], v[132:133], 0, s[6:7]
	s_mul_i32 s6, s13, 0xcc
	v_med3_f32 v65, v66, s36, v149
	v_med3_f32 v64, v64, s36, v149
	v_lshl_add_u64 v[46:47], v[132:133], 0, s[6:7]
	v_cvt_pk_fp8_f32 v67, v65, v64 op_sel:[0,0,1]
	s_waitcnt vmcnt(19)
; #define LAS __attribute__((address_space(3)))
; #define LDS_WAIT() asm volatile("s_waitcnt lgkmcnt(0)" ::: "memory")
; #define CV_LOAD(qi, Q, D) do { _Pragma("unroll") for (int s_ = 0; s_ < 2; ++s_) _Pragma("unroll") for (int r_ = 0; r_ < 4; ++r_) Q.v[s_][r_] = *(const f32x4*)(D.src + (size_t)(16 * (2 * (qi) + s_) + r_) * D.N); asm volatile("" ::: "memory"); } while (0)
; #define CV_PROC(qi, Q) do { _Pragma("unroll") for (int s_ = 0; s_ < 2; ++s_) _Pragma("unroll") for (int c_ = 0; c_ < 4; ++c_) \
;         *(LAS unsigned*)(scr + (4 * nl + c_) * 132 + 16 * (2 * (qi) + s_) + 4 * kg) = pg8::pk4_fp8c(Q.v[s_][0][c_] * FP8_WSC, Q.v[s_][1][c_] * FP8_WSC, Q.v[s_][2][c_] * FP8_WSC, Q.v[s_][3][c_] * FP8_WSC); asm volatile("" ::: "memory"); } while (0)
; __device__ __forceinline__ void moe_conv_stream(const Args& a, ARGAS unsigned char* ws, LAS unsigned char* scr, int first, int cnt, int lane) {
;     ...
;     Qt A, B, C, D4;
;     ConvItem cur = moe_conv_desc(a, ws, first, lane);
;     CV_LOAD(0, A, cur); CV_LOAD(1, B, cur); CV_LOAD(2, C, cur);
; #pragma unroll 1
;     for (int i = 0; i < cnt; ++i) {
;         const ConvItem nxt = moe_conv_desc(a, ws, first + 8 * ((i + 1 < cnt) ? i + 1 : i), lane);
;         CV_LOAD(3, D4, cur); CV_PROC(0, A);
;         CV_LOAD(0, A, nxt);  CV_PROC(1, B);
;         CV_LOAD(1, B, nxt);  CV_PROC(2, C);
;         CV_LOAD(2, C, nxt);  CV_PROC(3, D4);
;         LDS_WAIT(); asm volatile("" ::: "memory");
;         const int n0 = cur.gu > 0 ? cur.gu - 1 : -cur.gu - 1;
; #pragma unroll
;         for (int j = 0; j < 8; ++j) { const int row = (lane >> 3) + 8 * j; const LAS unsigned* s = (const LAS unsigned*)(scr + row * 132 + 16 * c8);
;             u32x4 o; o.x = s[0]; o.y = s[1]; o.z = s[2]; o.w = s[3];
;             const int n = n0 + row, wr_ = cur.gu > 0 ? RmGu()(n) : n;
;             *(u32x4*)(cur.dst + (size_t)wr_ * cur.ldk + 16 * c8) = o; }
	v_mul_f32_e32 v116, 0x43000000, v116
	s_waitcnt vmcnt(18)
	v_mul_f32_e32 v120, 0x43000000, v120
	global_load_dwordx4 v[32:35], v[32:33], off
	s_nop 0
	global_load_dwordx4 v[36:39], v[36:37], off
	s_nop 0
	global_load_dwordx4 v[52:55], v[44:45], off
	s_nop 0
	global_load_dwordx4 v[44:47], v[46:47], off
	ds_write2_b32 v146, v150, v73 offset0:16 offset1:20
	ds_write2_b32 v146, v81, v69 offset0:49 offset1:53
	ds_write2_b32 v146, v80, v68 offset0:82 offset1:86
	ds_write2_b32 v146, v75, v67 offset0:115 offset1:119
	v_med3_f32 v116, v116, s36, v149
	v_med3_f32 v120, v120, s36, v149
	v_mov_b32_e32 v150, v129
	v_cvt_pk_fp8_f32 v150, v116, v120
	s_waitcnt vmcnt(21)
	v_mul_f32_e32 v124, 0x43000000, v124
	s_waitcnt vmcnt(20)
	v_mul_f32_e32 v112, 0x43000000, v112
	v_med3_f32 v116, v124, s36, v149
	v_med3_f32 v112, v112, s36, v149
	v_cvt_pk_fp8_f32 v150, v116, v112 op_sel:[0,0,1]
	v_mul_f32_e32 v112, 0x43000000, v117
	v_mul_f32_e32 v116, 0x43000000, v121
	v_med3_f32 v112, v112, s36, v149
	v_med3_f32 v116, v116, s36, v149
	v_mov_b32_e32 v120, v129
	v_cvt_pk_fp8_f32 v120, v112, v116
	v_mul_f32_e32 v117, 0x43000000, v125
	v_mul_f32_e32 v112, 0x43000000, v113
	v_med3_f32 v113, v117, s36, v149
	v_med3_f32 v112, v112, s36, v149
	v_cvt_pk_fp8_f32 v120, v113, v112 op_sel:[0,0,1]
	v_mul_f32_e32 v112, 0x43000000, v118
	v_mul_f32_e32 v113, 0x43000000, v122
	v_med3_f32 v112, v112, s36, v149
	v_med3_f32 v113, v113, s36, v149
	v_mov_b32_e32 v117, v129
	v_cvt_pk_fp8_f32 v117, v112, v113
	v_mul_f32_e32 v116, 0x43000000, v126
	v_mul_f32_e32 v112, 0x43000000, v114
	v_med3_f32 v113, v116, s36, v149
	v_med3_f32 v112, v112, s36, v149
	v_cvt_pk_fp8_f32 v117, v113, v112 op_sel:[0,0,1]
	v_mul_f32_e32 v112, 0x43000000, v119
	v_mul_f32_e32 v113, 0x43000000, v123
	v_med3_f32 v112, v112, s36, v149
	v_med3_f32 v113, v113, s36, v149
	v_mov_b32_e32 v116, v129
	v_cvt_pk_fp8_f32 v116, v112, v113
	v_mul_f32_e32 v114, 0x43000000, v127
	v_mul_f32_e32 v112, 0x43000000, v115
	v_med3_f32 v113, v114, s36, v149
	v_med3_f32 v112, v112, s36, v149
	s_waitcnt vmcnt(19)
	v_mul_f32_e32 v100, 0x43000000, v100
	s_waitcnt vmcnt(18)
	v_mul_f32_e32 v104, 0x43000000, v104
	v_cvt_pk_fp8_f32 v116, v113, v112 op_sel:[0,0,1]
	v_med3_f32 v100, v100, s36, v149
	v_med3_f32 v104, v104, s36, v149
	v_mov_b32_e32 v112, v129
	v_cvt_pk_fp8_f32 v112, v100, v104
	s_waitcnt vmcnt(17)
	v_mul_f32_e32 v108, 0x43000000, v108
	s_waitcnt vmcnt(16)
	v_mul_f32_e32 v96, 0x43000000, v96
	v_med3_f32 v100, v108, s36, v149
	v_med3_f32 v96, v96, s36, v149
	v_cvt_pk_fp8_f32 v112, v100, v96 op_sel:[0,0,1]
	v_mul_f32_e32 v96, 0x43000000, v101
	v_mul_f32_e32 v100, 0x43000000, v105
	v_med3_f32 v96, v96, s36, v149
	v_med3_f32 v100, v100, s36, v149
	v_mov_b32_e32 v104, v129
	v_cvt_pk_fp8_f32 v104, v96, v100
	v_mul_f32_e32 v101, 0x43000000, v109
	v_mul_f32_e32 v96, 0x43000000, v97
	v_med3_f32 v97, v101, s36, v149
	v_med3_f32 v96, v96, s36, v149
	s_lshl_b32 s6, s13, 8
	v_cvt_pk_fp8_f32 v104, v97, v96 op_sel:[0,0,1]
	v_mul_f32_e32 v96, 0x43000000, v102
	v_mul_f32_e32 v97, 0x43000000, v106
	v_lshl_add_u64 v[64:65], v[132:133], 0, s[6:7]
	s_mul_i32 s6, s13, 0x104
	v_med3_f32 v96, v96, s36, v149
	v_med3_f32 v97, v97, s36, v149
	v_mov_b32_e32 v101, v129
	v_lshl_add_u64 v[66:67], v[132:133], 0, s[6:7]
	s_mul_i32 s6, s13, 0x108
	v_cvt_pk_fp8_f32 v101, v96, v97
	global_load_dwordx4 v[72:75], v[64:65], off
	global_load_dwordx4 v[80:83], v[66:67], off
	v_lshl_add_u64 v[64:65], v[132:133], 0, s[6:7]
	s_mul_i32 s6, s13, 0x10c
	v_lshl_add_u64 v[66:67], v[132:133], 0, s[6:7]
	s_mul_i32 s6, s13, 0x140
	v_mul_f32_e32 v100, 0x43000000, v110
	v_mul_f32_e32 v96, 0x43000000, v98
	global_load_dwordx4 v[92:95], v[64:65], off
	global_load_dwordx4 v[88:91], v[66:67], off
	v_lshl_add_u64 v[64:65], v[132:133], 0, s[6:7]
	s_mul_i32 s6, s13, 0x144
	v_med3_f32 v97, v100, s36, v149
	v_med3_f32 v96, v96, s36, v149
	v_lshl_add_u64 v[68:69], v[132:133], 0, s[6:7]
	s_mul_i32 s6, s13, 0x148
	v_cvt_pk_fp8_f32 v101, v97, v96 op_sel:[0,0,1]
	v_mul_f32_e32 v96, 0x43000000, v103
	v_mul_f32_e32 v97, 0x43000000, v107
	v_lshl_add_u64 v[76:77], v[132:133], 0, s[6:7]
	s_mul_i32 s6, s13, 0x14c
	v_med3_f32 v96, v96, s36, v149
	v_med3_f32 v97, v97, s36, v149
	v_mov_b32_e32 v100, v129
	v_lshl_add_u64 v[78:79], v[132:133], 0, s[6:7]
	v_cvt_pk_fp8_f32 v100, v96, v97
	s_add_i32 s6, s39, -1
	s_not_b32 s12, s39
	s_cmp_gt_i32 s39, 0
	global_load_dwordx4 v[64:67], v[64:65], off
	s_nop 0
	global_load_dwordx4 v[68:71], v[68:69], off
	s_nop 0
	global_load_dwordx4 v[84:87], v[76:77], off
	s_nop 0
	global_load_dwordx4 v[76:79], v[78:79], off
	v_mul_f32_e32 v98, 0x43000000, v111
	v_mul_f32_e32 v96, 0x43000000, v99
	s_cselect_b64 vcc, -1, 0
	v_med3_f32 v97, v98, s36, v149
	v_med3_f32 v96, v96, s36, v149
	s_and_b64 s[14:15], vcc, exec
	v_cvt_pk_fp8_f32 v100, v97, v96 op_sel:[0,0,1]
	s_cselect_b32 s6, s6, s12
	ds_write2_b32 v146, v150, v112 offset0:24 offset1:28
	ds_write2_b32 v146, v120, v104 offset0:57 offset1:61
	ds_write2_b32 v146, v117, v101 offset0:90 offset1:94
	ds_write2_b32 v146, v116, v100 offset0:123 offset1:127
	v_add_u32_e32 v100, s6, v194
	v_lshlrev_b32_e32 v101, 1, v100
	v_ashrrev_i32_e32 v102, 3, v100
	s_waitcnt lgkmcnt(0)
	v_and_b32_e32 v101, 0x700, v101
	v_and_b32_e32 v102, 0xffffff80, v102
	v_add_u32_e32 v101, v101, v102
	ds_read2_b32 v[96:97], v147 offset1:1
	ds_read2_b32 v[98:99], v147 offset0:2 offset1:3
	v_and_or_b32 v101, v100, s37, v101
	v_cndmask_b32_e32 v100, v100, v101, vcc
	v_ashrrev_i32_e32 v101, 31, v100
	v_lshl_add_u64 v[104:105], s[8:9], 0, v[130:131]
	v_lshlrev_b64 v[100:101], 10, v[100:101]
	v_lshl_add_u64 v[106:107], v[104:105], 0, v[100:101]
	v_add_u32_e32 v100, 0x420, v147
	v_add_u32_e32 v102, 0x428, v147
	ds_read2_b32 v[100:101], v100 offset1:1
	ds_read2_b32 v[102:103], v102 offset1:1
	s_waitcnt lgkmcnt(2)
; #define LAS __attribute__((address_space(3)))
; #define LDS_WAIT() asm volatile("s_waitcnt lgkmcnt(0)" ::: "memory")
; #define CV_LOAD(qi, Q, D) do { _Pragma("unroll") for (int s_ = 0; s_ < 2; ++s_) _Pragma("unroll") for (int r_ = 0; r_ < 4; ++r_) Q.v[s_][r_] = *(const f32x4*)(D.src + (size_t)(16 * (2 * (qi) + s_) + r_) * D.N); asm volatile("" ::: "memory"); } while (0)
; __device__ __forceinline__ ConvItem moe_conv_desc(const Args& a, ARGAS unsigned char* ws, int it, int lane) {
;     const int m = it / MOE_CONV_PER_M, r = it % MOE_CONV_PER_M, nl = lane & 15, kg = lane >> 4; ConvItem d;
;     if (r < 256) { const int kb = r / 32, nb = r % 32; d.N = 2048; d.ldk = DM; d.gu = 64 * nb + 1; d.src = a.moe_w_gu + (size_t)m * DM * 2048 + (size_t)(128 * kb + 4 * kg) * 2048 + 64 * nb + 4 * nl; d.dst = (unsigned char*)(ws + WS_WGU) + (size_t)m * 2048 * DM + 128 * kb; }
;     else { const int r2 = r - 256, kb = r2 / 16, nb = r2 % 16; d.N = DM; d.ldk = EFF; d.gu = -(64 * nb) - 1; d.src = a.moe_w_down + (size_t)m * EFF * DM + (size_t)(128 * kb + 4 * kg) * DM + 64 * nb + 4 * nl; d.dst = (unsigned char*)(ws + WS_WDN) + (size_t)m * DM * EFF + 128 * kb; }
;     return d;
; __device__ __forceinline__ void moe_conv_stream(const Args& a, ARGAS unsigned char* ws, LAS unsigned char* scr, int first, int cnt, int lane) {
;     ...
;     for (int i = 0; i < cnt; ++i) {
;         const ConvItem nxt = moe_conv_desc(a, ws, first + 8 * ((i + 1 < cnt) ? i + 1 : i), lane);
;         CV_LOAD(3, D4, cur); CV_PROC(0, A);
;         CV_LOAD(0, A, nxt);  CV_PROC(1, B);
;         CV_LOAD(1, B, nxt);  CV_PROC(2, C);
;         CV_LOAD(2, C, nxt);  CV_PROC(3, D4);
;         LDS_WAIT(); asm volatile("" ::: "memory");
;         const int n0 = cur.gu > 0 ? cur.gu - 1 : -cur.gu - 1;
; #pragma unroll
;         for (int j = 0; j < 8; ++j) { const int row = (lane >> 3) + 8 * j; const LAS unsigned* s = (const LAS unsigned*)(scr + row * 132 + 16 * c8);
;             u32x4 o; o.x = s[0]; o.y = s[1]; o.z = s[2]; o.w = s[3];
;             const int n = n0 + row, wr_ = cur.gu > 0 ? RmGu()(n) : n;
;             *(u32x4*)(cur.dst + (size_t)wr_ * cur.ldk + 16 * c8) = o; }
;         LDS_WAIT(); asm volatile("" ::: "memory");
;         cur = nxt;
	global_store_dwordx4 v[106:107], v[96:99], off
	s_add_i32 s40, s40, 8
	s_cmpk_eq_i32 s40, 0x28
	v_add_u32_e32 v96, s6, v137
	v_lshlrev_b32_e32 v97, 1, v96
	v_ashrrev_i32_e32 v98, 3, v96
	v_and_b32_e32 v97, 0x700, v97
	v_and_b32_e32 v98, 0xffffff80, v98
	v_add_u32_e32 v97, v97, v98
	v_and_or_b32 v97, v96, s37, v97
	v_cndmask_b32_e32 v96, v96, v97, vcc
	v_ashrrev_i32_e32 v97, 31, v96
	v_lshlrev_b64 v[96:97], 10, v[96:97]
	v_lshl_add_u64 v[96:97], v[104:105], 0, v[96:97]
	s_waitcnt lgkmcnt(0)
	global_store_dwordx4 v[96:97], v[100:103], off
	v_add_u32_e32 v96, 0x840, v147
	v_add_u32_e32 v98, 0x848, v147
	v_add_u32_e32 v100, s6, v138
	v_lshlrev_b32_e32 v101, 1, v100
	v_ashrrev_i32_e32 v102, 3, v100
	v_and_b32_e32 v101, 0x700, v101
	v_and_b32_e32 v102, 0xffffff80, v102
	v_add_u32_e32 v101, v101, v102
	ds_read2_b32 v[96:97], v96 offset1:1
	ds_read2_b32 v[98:99], v98 offset1:1
	v_and_or_b32 v101, v100, s37, v101
	v_cndmask_b32_e32 v100, v100, v101, vcc
	v_ashrrev_i32_e32 v101, 31, v100
	v_lshlrev_b64 v[100:101], 10, v[100:101]
	v_lshl_add_u64 v[106:107], v[104:105], 0, v[100:101]
	v_add_u32_e32 v100, 0xc60, v147
	v_add_u32_e32 v102, 0xc68, v147
	ds_read2_b32 v[100:101], v100 offset1:1
	ds_read2_b32 v[102:103], v102 offset1:1
	s_waitcnt lgkmcnt(2)
	global_store_dwordx4 v[106:107], v[96:99], off
	s_mov_b32 s39, s41
	s_mov_b64 s[8:9], s[10:11]
	v_add_u32_e32 v96, s6, v139
	v_lshlrev_b32_e32 v97, 1, v96
	v_ashrrev_i32_e32 v98, 3, v96
	v_and_b32_e32 v97, 0x700, v97
	v_and_b32_e32 v98, 0xffffff80, v98
	v_add_u32_e32 v97, v97, v98
	v_and_or_b32 v97, v96, s37, v97
	v_cndmask_b32_e32 v96, v96, v97, vcc
	v_ashrrev_i32_e32 v97, 31, v96
	v_lshlrev_b64 v[96:97], 10, v[96:97]
	v_lshl_add_u64 v[96:97], v[104:105], 0, v[96:97]
	s_waitcnt lgkmcnt(0)
	global_store_dwordx4 v[96:97], v[100:103], off
	v_add_u32_e32 v96, 0x1080, v147
	v_add_u32_e32 v98, 0x1088, v147
	v_add_u32_e32 v100, s6, v140
	v_lshlrev_b32_e32 v101, 1, v100
	v_ashrrev_i32_e32 v102, 3, v100
	v_and_b32_e32 v101, 0x700, v101
	v_and_b32_e32 v102, 0xffffff80, v102
	v_add_u32_e32 v101, v101, v102
	ds_read2_b32 v[96:97], v96 offset1:1
	ds_read2_b32 v[98:99], v98 offset1:1
	v_and_or_b32 v101, v100, s37, v101
	v_cndmask_b32_e32 v100, v100, v101, vcc
	v_ashrrev_i32_e32 v101, 31, v100
	v_lshlrev_b64 v[100:101], 10, v[100:101]
	v_lshl_add_u64 v[106:107], v[104:105], 0, v[100:101]
	v_add_u32_e32 v100, 0x14a0, v147
	v_add_u32_e32 v102, 0x14a8, v147
	ds_read2_b32 v[100:101], v100 offset1:1
	ds_read2_b32 v[102:103], v102 offset1:1
	s_waitcnt lgkmcnt(2)
	global_store_dwordx4 v[106:107], v[96:99], off
	s_nop 1
	v_add_u32_e32 v96, s6, v141
	v_lshlrev_b32_e32 v97, 1, v96
	v_ashrrev_i32_e32 v98, 3, v96
	v_and_b32_e32 v97, 0x700, v97
	v_and_b32_e32 v98, 0xffffff80, v98
	v_add_u32_e32 v97, v97, v98
	v_and_or_b32 v97, v96, s37, v97
	v_cndmask_b32_e32 v96, v96, v97, vcc
	v_ashrrev_i32_e32 v97, 31, v96
	v_lshlrev_b64 v[96:97], 10, v[96:97]
	v_lshl_add_u64 v[96:97], v[104:105], 0, v[96:97]
	s_waitcnt lgkmcnt(0)
	global_store_dwordx4 v[96:97], v[100:103], off
	v_add_u32_e32 v96, 0x18c0, v147
	v_add_u32_e32 v98, 0x18c8, v147
	v_add_u32_e32 v100, s6, v142
	v_lshlrev_b32_e32 v101, 1, v100
	v_ashrrev_i32_e32 v102, 3, v100
	v_and_b32_e32 v101, 0x700, v101
	v_and_b32_e32 v102, 0xffffff80, v102
	v_add_u32_e32 v101, v101, v102
	ds_read2_b32 v[96:97], v96 offset1:1
	ds_read2_b32 v[98:99], v98 offset1:1
	v_and_or_b32 v101, v100, s37, v101
	v_cndmask_b32_e32 v100, v100, v101, vcc
	v_ashrrev_i32_e32 v101, 31, v100
	v_lshlrev_b64 v[100:101], 10, v[100:101]
	v_lshl_add_u64 v[106:107], v[104:105], 0, v[100:101]
	v_add_u32_e32 v100, 0x1ce0, v147
	v_add_u32_e32 v102, 0x1ce8, v147
	ds_read2_b32 v[100:101], v100 offset1:1
	ds_read2_b32 v[102:103], v102 offset1:1
	s_waitcnt lgkmcnt(2)
	global_store_dwordx4 v[106:107], v[96:99], off
	s_nop 1
	v_add_u32_e32 v96, s6, v143
	v_lshlrev_b32_e32 v97, 1, v96
	v_ashrrev_i32_e32 v98, 3, v96
	v_and_b32_e32 v97, 0x700, v97
	v_and_b32_e32 v98, 0xffffff80, v98
	v_add_u32_e32 v97, v97, v98
	v_and_or_b32 v97, v96, s37, v97
	v_cndmask_b32_e32 v96, v96, v97, vcc
	v_ashrrev_i32_e32 v97, 31, v96
	v_lshlrev_b64 v[96:97], 10, v[96:97]
	v_lshl_add_u64 v[96:97], v[104:105], 0, v[96:97]
	s_waitcnt lgkmcnt(0)
	global_store_dwordx4 v[96:97], v[100:103], off
	s_waitcnt lgkmcnt(0)
	s_mov_b32 s6, s13
	v_mov_b64_e32 v[96:97], v[132:133]
	s_cbranch_scc1 .LBB0_574
.LBB0_587:
	s_cmpk_lg_i32 s40, 0x20
	s_cselect_b32 s10, s40, 0x18
	s_add_i32 s10, s10, s38
	s_mul_hi_i32 s11, s10, 0x2aaaaaab
	s_lshr_b32 s12, s11, 31
	s_ashr_i32 s11, s11, 6
	s_add_i32 s12, s11, s12
	s_mul_i32 s11, s12, 0x180
	s_sub_i32 s42, s10, s11
	s_cmpk_gt_i32 s42, 0xff
	s_cbranch_scc0 .LBB0_589
	s_load_dwordx2 s[10:11], s[20:21], 0xe0
	s_lshl_b32 s13, s42, 6
	s_and_b32 s43, s13, 0x3c0
	s_ashr_i32 s13, s12, 31
	s_not_b32 s41, s43
	s_lshl_b64 s[14:15], s[12:13], 20
	s_lshl_b64 s[48:49], s[12:13], 22
	s_waitcnt lgkmcnt(0)
	s_add_u32 s10, s10, s48
	s_addc_u32 s11, s11, s49
	s_lshl_b32 s13, s42, 3
	s_and_b32 s13, s13, 0x7fffff80
	s_addk_i32 s13, 0xf800
	v_or_b32_e32 v98, s13, v136
	v_mov_b32_e32 v99, v129
	v_lshlrev_b64 v[98:99], 12, v[98:99]
	v_lshl_add_u64 v[98:99], s[10:11], 0, v[98:99]
	s_lshl_b32 s10, s43, 2
	s_mov_b32 s11, s7
	v_lshl_add_u64 v[98:99], v[98:99], 0, s[10:11]
	s_add_u32 s10, s16, s14
	s_addc_u32 s11, s17, s15
	s_add_u32 s10, s10, s13
	s_addc_u32 s11, s11, 0
	s_movk_i32 s13, 0x400
	s_cbranch_execnz .LBB0_586
	s_branch .LBB0_590

; __device__ __forceinline__ unsigned xb_add(gbar_t p, unsigned v) { return __hip_atomic_fetch_add(p, v, __ATOMIC_RELAXED, __HIP_MEMORY_SCOPE_AGENT); }
; __device__ __forceinline__ ConvItem moe_conv_desc(const Args& a, ARGAS unsigned char* ws, int it, int lane) {
;     const int m = it / MOE_CONV_PER_M, r = it % MOE_CONV_PER_M, nl = lane & 15, kg = lane >> 4; ConvItem d;
;     if (r < 256) { const int kb = r / 32, nb = r % 32; d.N = 2048; d.ldk = DM; d.gu = 64 * nb + 1; d.src = a.moe_w_gu + (size_t)m * DM * 2048 + (size_t)(128 * kb + 4 * kg) * 2048 + 64 * nb + 4 * nl; d.dst = (unsigned char*)(ws + WS_WGU) + (size_t)m * 2048 * DM + 128 * kb; }
;     else { const int r2 = r - 256, kb = r2 / 16, nb = r2 % 16; d.N = DM; d.ldk = EFF; d.gu = -(64 * nb) - 1; d.src = a.moe_w_down + (size_t)m * EFF * DM + (size_t)(128 * kb + 4 * kg) * DM + 64 * nb + 4 * nl; d.dst = (unsigned char*)(ws + WS_WDN) + (size_t)m * DM * EFF + 128 * kb; }
;     return d;
; __device__ __forceinline__ void moe_conv_drain(const Frame& F, const Args& a, ARGAS unsigned char* ws, gbar_t head, LAS unsigned* qslot, const int first_chunk, const int nchunks) {
;     ...
;         __syncthreads();
;         if (F.tid == 0) *qslot = xb_add(head, 1u);
;         __syncthreads();
;         const unsigned ch = *qslot;
;         if (ch >= (unsigned)nchunks) break;
;         moe_conv_stream(a, ws, scr, (first_chunk + (int)ch) * MOE_CONV_CHUNK + F.wave, MOE_CONV_CHUNK / 8, F.lane);
.LBB0_660:
	s_or_b64 exec, exec, s[8:9]
	s_waitcnt lgkmcnt(0)
	s_barrier
	s_waitcnt vmcnt(27)
	ds_read_b32 v0, v142
	s_mov_b64 s[8:9], -1
	s_waitcnt lgkmcnt(0)
	s_movk_i32 s98, 0x2ff
	v_cmp_lt_u32_e32 vcc, s98, v0
	v_readfirstlane_b32 s6, v0
	s_cbranch_vccnz .LBB0_655
	s_lshl_b32 s36, s6, 5
	s_add_i32 s36, s36, s45
	s_mul_hi_i32 s6, s36, 0x2aaaaaab
	s_lshr_b32 s8, s6, 31
	s_ashr_i32 s6, s6, 6
	s_add_i32 s10, s6, s8
	s_mul_i32 s6, s10, 0x180
	s_sub_i32 s14, s36, s6
	s_cmpk_gt_i32 s14, 0xff
	s_cbranch_scc0 .LBB0_663
	s_load_dwordx2 s[8:9], s[20:21], 0xe0
	s_lshl_b32 s6, s14, 6
	s_and_b32 s6, s6, 0x3c0
	s_ashr_i32 s11, s10, 31
	s_not_b32 s37, s6
	s_lshl_b64 s[12:13], s[10:11], 20
	s_lshl_b64 s[38:39], s[10:11], 22
	s_waitcnt lgkmcnt(0)
	s_add_u32 s8, s8, s38
	s_addc_u32 s9, s9, s39
	s_lshl_b32 s11, s14, 3
	s_and_b32 s11, s11, 0x7fffff80
	s_addk_i32 s11, 0xf800
	v_or_b32_e32 v0, s11, v134
	v_mov_b32_e32 v1, v129
	v_lshlrev_b64 v[0:1], 12, v[0:1]
	v_lshl_add_u64 v[0:1], s[8:9], 0, v[0:1]
	s_lshl_b32 s6, s6, 2
	v_lshl_add_u64 v[0:1], v[0:1], 0, s[6:7]
	s_add_u32 s6, s16, s12
	s_addc_u32 s9, s17, s13
	s_add_u32 s8, s6, s11
	s_addc_u32 s9, s9, 0
	s_movk_i32 s11, 0x400
	s_cbranch_execz .LBB0_664
	s_branch .LBB0_665

; #define CV_LOAD(qi, Q, D) do { _Pragma("unroll") for (int s_ = 0; s_ < 2; ++s_) _Pragma("unroll") for (int r_ = 0; r_ < 4; ++r_) Q.v[s_][r_] = *(const f32x4*)(D.src + (size_t)(16 * (2 * (qi) + s_) + r_) * D.N); asm volatile("" ::: "memory"); } while (0)
; #define CV_PROC(qi, Q) do { _Pragma("unroll") for (int s_ = 0; s_ < 2; ++s_) _Pragma("unroll") for (int c_ = 0; c_ < 4; ++c_) \
;         *(LAS unsigned*)(scr + (4 * nl + c_) * 132 + 16 * (2 * (qi) + s_) + 4 * kg) = pg8::pk4_fp8c(Q.v[s_][0][c_] * FP8_WSC, Q.v[s_][1][c_] * FP8_WSC, Q.v[s_][2][c_] * FP8_WSC, Q.v[s_][3][c_] * FP8_WSC); asm volatile("" ::: "memory"); } while (0)
; __device__ __forceinline__ void moe_conv_stream(const Args& a, ARGAS unsigned char* ws, LAS unsigned char* scr, int first, int cnt, int lane) {
;     ...
;     Qt A, B, C, D4;
;     ConvItem cur = moe_conv_desc(a, ws, first, lane);
;     CV_LOAD(0, A, cur); CV_LOAD(1, B, cur); CV_LOAD(2, C, cur);
; #pragma unroll 1
;     for (int i = 0; i < cnt; ++i) {
;         const ConvItem nxt = moe_conv_desc(a, ws, first + 8 * ((i + 1 < cnt) ? i + 1 : i), lane);
;         CV_LOAD(3, D4, cur); CV_PROC(0, A);
;         CV_LOAD(0, A, nxt);  CV_PROC(1, B);
;         CV_LOAD(1, B, nxt);  CV_PROC(2, C);
;         CV_LOAD(2, C, nxt);  CV_PROC(3, D4);
.LBB0_666:
	s_waitcnt vmcnt(17)
	v_mul_f32_e32 v28, 0x43000000, v28
	v_mul_f32_e32 v16, 0x43000000, v16
	v_med3_f32 v28, v28, s26, v147
	v_med3_f32 v16, v16, s26, v147
	v_mov_b32_e32 v148, v129
	v_cvt_pk_fp8_f32 v148, v28, v16
	v_mul_f32_e32 v20, 0x43000000, v20
	v_mul_f32_e32 v16, 0x43000000, v24
	v_med3_f32 v20, v20, s26, v147
	v_med3_f32 v16, v16, s26, v147
	v_cvt_pk_fp8_f32 v148, v20, v16 op_sel:[0,0,1]
	v_mul_f32_e32 v16, 0x43000000, v29
	v_mul_f32_e32 v17, 0x43000000, v17
	v_mul_f32_e32 v20, 0x43000000, v21
	v_med3_f32 v16, v16, s26, v147
	v_med3_f32 v17, v17, s26, v147
	v_mov_b32_e32 v21, v129
	v_cvt_pk_fp8_f32 v21, v16, v17
	v_mul_f32_e32 v16, 0x43000000, v25
	v_med3_f32 v17, v20, s26, v147
	v_med3_f32 v16, v16, s26, v147
	v_cvt_pk_fp8_f32 v21, v17, v16 op_sel:[0,0,1]
	v_mul_f32_e32 v16, 0x43000000, v30
	v_mul_f32_e32 v17, 0x43000000, v18
	v_med3_f32 v16, v16, s26, v147
	v_med3_f32 v17, v17, s26, v147
	v_mov_b32_e32 v20, v129
	v_cvt_pk_fp8_f32 v20, v16, v17
	v_mul_f32_e32 v18, 0x43000000, v22
	v_mul_f32_e32 v16, 0x43000000, v26
	v_med3_f32 v17, v18, s26, v147
	v_med3_f32 v16, v16, s26, v147
	v_cvt_pk_fp8_f32 v20, v17, v16 op_sel:[0,0,1]
	v_mul_f32_e32 v16, 0x43000000, v31
	v_mul_f32_e32 v17, 0x43000000, v19
	v_med3_f32 v16, v16, s26, v147
	v_med3_f32 v17, v17, s26, v147
	v_mov_b32_e32 v19, v129
	v_cvt_pk_fp8_f32 v19, v16, v17
	v_mul_f32_e32 v18, 0x43000000, v23
	v_mul_f32_e32 v16, 0x43000000, v27
	v_med3_f32 v17, v18, s26, v147
	v_med3_f32 v16, v16, s26, v147
	v_mul_f32_e32 v0, 0x43000000, v0
	v_mul_f32_e32 v4, 0x43000000, v4
	v_cvt_pk_fp8_f32 v19, v17, v16 op_sel:[0,0,1]
	v_med3_f32 v0, v0, s26, v147
	v_med3_f32 v4, v4, s26, v147
	v_mov_b32_e32 v16, v129
	v_cvt_pk_fp8_f32 v16, v0, v4
	v_mul_f32_e32 v8, 0x43000000, v8
	s_waitcnt vmcnt(16)
	v_mul_f32_e32 v0, 0x43000000, v12
	v_med3_f32 v4, v8, s26, v147
	v_med3_f32 v0, v0, s26, v147
	v_cvt_pk_fp8_f32 v16, v4, v0 op_sel:[0,0,1]
	v_mul_f32_e32 v0, 0x43000000, v1
	v_mul_f32_e32 v1, 0x43000000, v5
	v_med3_f32 v0, v0, s26, v147
	v_med3_f32 v1, v1, s26, v147
	v_mov_b32_e32 v5, v129
	v_cvt_pk_fp8_f32 v5, v0, v1
	v_mul_f32_e32 v4, 0x43000000, v9
	v_mul_f32_e32 v0, 0x43000000, v13
	v_med3_f32 v1, v4, s26, v147
	v_med3_f32 v0, v0, s26, v147
	v_cvt_pk_fp8_f32 v5, v1, v0 op_sel:[0,0,1]
	v_mul_f32_e32 v0, 0x43000000, v2
	v_mul_f32_e32 v1, 0x43000000, v6
	v_med3_f32 v0, v0, s26, v147
	v_med3_f32 v1, v1, s26, v147
	v_mov_b32_e32 v4, v129
	v_cvt_pk_fp8_f32 v4, v0, v1
	v_mad_u64_u32 v[96:97], s[14:15], s6, v146, v[96:97]
	v_mul_f32_e32 v2, 0x43000000, v10
	v_mul_f32_e32 v0, 0x43000000, v14
	s_lshl_b64 s[14:15], s[6:7], 2
	v_med3_f32 v1, v2, s26, v147
	v_med3_f32 v0, v0, s26, v147
	v_lshl_add_u64 v[132:133], v[98:99], 0, v[128:129]
	v_lshl_add_u64 v[98:99], v[96:97], 0, s[14:15]
	v_cvt_pk_fp8_f32 v4, v1, v0 op_sel:[0,0,1]
	v_mul_f32_e32 v0, 0x43000000, v3
	v_mul_f32_e32 v1, 0x43000000, v7
	global_load_dwordx4 v[116:119], v[96:97], off
	global_load_dwordx4 v[120:123], v[98:99], off
	v_lshl_add_u64 v[96:97], v[98:99], 0, s[14:15]
	v_med3_f32 v0, v0, s26, v147
	v_med3_f32 v1, v1, s26, v147
	v_mov_b32_e32 v3, v129
	v_lshl_add_u64 v[98:99], v[96:97], 0, s[14:15]
	v_cvt_pk_fp8_f32 v3, v0, v1
	global_load_dwordx4 v[124:127], v[96:97], off
	global_load_dwordx4 v[112:115], v[98:99], off
	v_mad_u64_u32 v[96:97], s[40:41], s6, 52, v[98:99]
	v_lshl_add_u64 v[98:99], v[96:97], 0, s[14:15]
	v_mul_f32_e32 v2, 0x43000000, v11
	v_mul_f32_e32 v0, 0x43000000, v15
	global_load_dwordx4 v[100:103], v[96:97], off
	global_load_dwordx4 v[104:107], v[98:99], off
	v_lshl_add_u64 v[96:97], v[98:99], 0, s[14:15]
	v_med3_f32 v1, v2, s26, v147
	v_med3_f32 v0, v0, s26, v147
	v_lshl_add_u64 v[98:99], v[96:97], 0, s[14:15]
	v_cvt_pk_fp8_f32 v3, v1, v0 op_sel:[0,0,1]
	s_waitcnt vmcnt(21)
	v_mul_f32_e32 v40, 0x43000000, v40
	s_waitcnt vmcnt(20)
	v_mul_f32_e32 v48, 0x43000000, v48
	global_load_dwordx4 v[108:111], v[96:97], off
	s_nop 0
	global_load_dwordx4 v[96:99], v[98:99], off
	ds_write2_b32 v143, v148, v16 offset1:4
	ds_write2_b32 v143, v21, v5 offset0:33 offset1:37
	ds_write2_b32 v143, v20, v4 offset0:66 offset1:70
	ds_write2_b32 v143, v19, v3 offset0:99 offset1:103
	v_med3_f32 v40, v40, s26, v147
	v_med3_f32 v48, v48, s26, v147
	v_mov_b32_e32 v148, v129
	v_cvt_pk_fp8_f32 v148, v40, v48
	s_waitcnt vmcnt(21)
	v_mul_f32_e32 v60, 0x43000000, v60
	s_waitcnt vmcnt(20)
	v_mul_f32_e32 v40, 0x43000000, v56
	v_med3_f32 v48, v60, s26, v147
	v_med3_f32 v40, v40, s26, v147
	v_cvt_pk_fp8_f32 v148, v48, v40 op_sel:[0,0,1]
	v_mul_f32_e32 v40, 0x43000000, v41
	v_mul_f32_e32 v41, 0x43000000, v49
	v_med3_f32 v40, v40, s26, v147
	v_med3_f32 v41, v41, s26, v147
	v_mov_b32_e32 v49, v129
	v_cvt_pk_fp8_f32 v49, v40, v41
	v_mul_f32_e32 v48, 0x43000000, v61
	v_mul_f32_e32 v40, 0x43000000, v57
	v_med3_f32 v41, v48, s26, v147
	v_med3_f32 v40, v40, s26, v147
	v_cvt_pk_fp8_f32 v49, v41, v40 op_sel:[0,0,1]
	v_mul_f32_e32 v40, 0x43000000, v42
	v_mul_f32_e32 v41, 0x43000000, v50
	v_med3_f32 v40, v40, s26, v147
	v_med3_f32 v41, v41, s26, v147
	v_mov_b32_e32 v48, v129
	v_cvt_pk_fp8_f32 v48, v40, v41
	v_mul_f32_e32 v42, 0x43000000, v62
	v_mul_f32_e32 v40, 0x43000000, v58
	v_med3_f32 v41, v42, s26, v147
	v_med3_f32 v40, v40, s26, v147
	v_cvt_pk_fp8_f32 v48, v41, v40 op_sel:[0,0,1]
	v_mul_f32_e32 v40, 0x43000000, v43
	v_mul_f32_e32 v41, 0x43000000, v51
	v_med3_f32 v40, v40, s26, v147
	v_med3_f32 v41, v41, s26, v147
	v_mov_b32_e32 v43, v129
	v_cvt_pk_fp8_f32 v43, v40, v41
	v_mul_f32_e32 v42, 0x43000000, v63
	v_mul_f32_e32 v40, 0x43000000, v59
	v_med3_f32 v41, v42, s26, v147
	v_med3_f32 v40, v40, s26, v147
	s_waitcnt vmcnt(19)
	v_mul_f32_e32 v32, 0x43000000, v32
	s_waitcnt vmcnt(18)
; #define CV_LOAD(qi, Q, D) do { _Pragma("unroll") for (int s_ = 0; s_ < 2; ++s_) _Pragma("unroll") for (int r_ = 0; r_ < 4; ++r_) Q.v[s_][r_] = *(const f32x4*)(D.src + (size_t)(16 * (2 * (qi) + s_) + r_) * D.N); asm volatile("" ::: "memory"); } while (0)
; #define CV_PROC(qi, Q) do { _Pragma("unroll") for (int s_ = 0; s_ < 2; ++s_) _Pragma("unroll") for (int c_ = 0; c_ < 4; ++c_) \
;         *(LAS unsigned*)(scr + (4 * nl + c_) * 132 + 16 * (2 * (qi) + s_) + 4 * kg) = pg8::pk4_fp8c(Q.v[s_][0][c_] * FP8_WSC, Q.v[s_][1][c_] * FP8_WSC, Q.v[s_][2][c_] * FP8_WSC, Q.v[s_][3][c_] * FP8_WSC); asm volatile("" ::: "memory"); } while (0)
; __device__ __forceinline__ void moe_conv_stream(const Args& a, ARGAS unsigned char* ws, LAS unsigned char* scr, int first, int cnt, int lane) {
;     ...
;     Qt A, B, C, D4;
;     ConvItem cur = moe_conv_desc(a, ws, first, lane);
;     CV_LOAD(0, A, cur); CV_LOAD(1, B, cur); CV_LOAD(2, C, cur);
; #pragma unroll 1
;     for (int i = 0; i < cnt; ++i) {
;         const ConvItem nxt = moe_conv_desc(a, ws, first + 8 * ((i + 1 < cnt) ? i + 1 : i), lane);
;         CV_LOAD(3, D4, cur); CV_PROC(0, A);
;         CV_LOAD(0, A, nxt);  CV_PROC(1, B);
;         CV_LOAD(1, B, nxt);  CV_PROC(2, C);
;         CV_LOAD(2, C, nxt);  CV_PROC(3, D4);
	v_mul_f32_e32 v36, 0x43000000, v36
	v_cvt_pk_fp8_f32 v43, v41, v40 op_sel:[0,0,1]
	v_med3_f32 v32, v32, s26, v147
	v_med3_f32 v36, v36, s26, v147
	v_mov_b32_e32 v41, v129
	v_cvt_pk_fp8_f32 v41, v32, v36
	s_waitcnt vmcnt(17)
	v_mul_f32_e32 v40, 0x43000000, v52
	s_waitcnt vmcnt(16)
	v_mul_f32_e32 v32, 0x43000000, v44
	v_med3_f32 v36, v40, s26, v147
	v_med3_f32 v32, v32, s26, v147
	v_cvt_pk_fp8_f32 v41, v36, v32 op_sel:[0,0,1]
	v_mul_f32_e32 v32, 0x43000000, v33
	v_mul_f32_e32 v33, 0x43000000, v37
	v_med3_f32 v32, v32, s26, v147
	v_med3_f32 v33, v33, s26, v147
	v_mov_b32_e32 v37, v129
	v_cvt_pk_fp8_f32 v37, v32, v33
	v_mul_f32_e32 v36, 0x43000000, v53
	v_mul_f32_e32 v32, 0x43000000, v45
	v_med3_f32 v33, v36, s26, v147
	v_med3_f32 v32, v32, s26, v147
	v_cvt_pk_fp8_f32 v37, v33, v32 op_sel:[0,0,1]
	v_mul_f32_e32 v32, 0x43000000, v34
	v_mul_f32_e32 v33, 0x43000000, v38
	v_med3_f32 v32, v32, s26, v147
	v_med3_f32 v33, v33, s26, v147
	v_mov_b32_e32 v36, v129
	v_cvt_pk_fp8_f32 v36, v32, v33
	v_mul_f32_e32 v34, 0x43000000, v54
	v_mul_f32_e32 v32, 0x43000000, v46
	s_lshl_b32 s6, s13, 2
	v_med3_f32 v33, v34, s26, v147
	v_med3_f32 v32, v32, s26, v147
	v_lshl_add_u64 v[0:1], v[132:133], 0, s[6:7]
	s_lshl_b32 s6, s13, 3
	v_cvt_pk_fp8_f32 v36, v33, v32 op_sel:[0,0,1]
	v_mul_f32_e32 v32, 0x43000000, v35
	v_mul_f32_e32 v33, 0x43000000, v39
	global_load_dwordx4 v[28:31], v[132:133], off
	global_load_dwordx4 v[16:19], v[0:1], off
	v_lshl_add_u64 v[0:1], v[132:133], 0, s[6:7]
	s_mul_i32 s6, s13, 12
	v_med3_f32 v32, v32, s26, v147
	v_med3_f32 v33, v33, s26, v147
	v_mov_b32_e32 v35, v129
	v_lshl_add_u64 v[2:3], v[132:133], 0, s[6:7]
	s_lshl_b32 s6, s13, 6
	v_cvt_pk_fp8_f32 v35, v32, v33
	global_load_dwordx4 v[20:23], v[0:1], off
	global_load_dwordx4 v[24:27], v[2:3], off
	v_lshl_add_u64 v[0:1], v[132:133], 0, s[6:7]
	s_mul_i32 s6, s13, 0x44
	v_lshl_add_u64 v[4:5], v[132:133], 0, s[6:7]
	s_mul_i32 s6, s13, 0x48
	v_mul_f32_e32 v34, 0x43000000, v55
	v_mul_f32_e32 v32, 0x43000000, v47
	v_lshl_add_u64 v[8:9], v[132:133], 0, s[6:7]
	s_mul_i32 s6, s13, 0x4c
	v_med3_f32 v33, v34, s26, v147
	v_med3_f32 v32, v32, s26, v147
	v_lshl_add_u64 v[12:13], v[132:133], 0, s[6:7]
	v_cvt_pk_fp8_f32 v35, v33, v32 op_sel:[0,0,1]
	s_waitcnt vmcnt(19)
	v_mul_f32_e32 v72, 0x43000000, v72
	s_waitcnt vmcnt(18)
	v_mul_f32_e32 v80, 0x43000000, v80
	global_load_dwordx4 v[0:3], v[0:1], off
	s_nop 0
	global_load_dwordx4 v[4:7], v[4:5], off
	s_nop 0
	global_load_dwordx4 v[8:11], v[8:9], off
	s_nop 0
	global_load_dwordx4 v[12:15], v[12:13], off
	ds_write2_b32 v144, v148, v41 offset0:8 offset1:12
	ds_write2_b32 v144, v49, v37 offset0:41 offset1:45
	ds_write2_b32 v144, v48, v36 offset0:74 offset1:78
	ds_write2_b32 v144, v43, v35 offset0:107 offset1:111
	v_med3_f32 v72, v72, s26, v147
	v_med3_f32 v80, v80, s26, v147
	v_mov_b32_e32 v148, v129
	v_cvt_pk_fp8_f32 v148, v72, v80
	s_waitcnt vmcnt(21)
	v_mul_f32_e32 v92, 0x43000000, v92
	s_waitcnt vmcnt(20)
	v_mul_f32_e32 v72, 0x43000000, v88
	v_med3_f32 v80, v92, s26, v147
	v_med3_f32 v72, v72, s26, v147
	v_cvt_pk_fp8_f32 v148, v80, v72 op_sel:[0,0,1]
	v_mul_f32_e32 v72, 0x43000000, v73
	v_mul_f32_e32 v73, 0x43000000, v81
	v_med3_f32 v72, v72, s26, v147
	v_med3_f32 v73, v73, s26, v147
	v_mov_b32_e32 v81, v129
	v_cvt_pk_fp8_f32 v81, v72, v73
	v_mul_f32_e32 v80, 0x43000000, v93
	v_mul_f32_e32 v72, 0x43000000, v89
	v_med3_f32 v73, v80, s26, v147
	v_med3_f32 v72, v72, s26, v147
	v_cvt_pk_fp8_f32 v81, v73, v72 op_sel:[0,0,1]
	v_mul_f32_e32 v72, 0x43000000, v74
	v_mul_f32_e32 v73, 0x43000000, v82
	v_med3_f32 v72, v72, s26, v147
	v_med3_f32 v73, v73, s26, v147
	v_mov_b32_e32 v80, v129
	v_cvt_pk_fp8_f32 v80, v72, v73
	v_mul_f32_e32 v74, 0x43000000, v94
	v_mul_f32_e32 v72, 0x43000000, v90
	v_med3_f32 v73, v74, s26, v147
	v_med3_f32 v72, v72, s26, v147
	v_cvt_pk_fp8_f32 v80, v73, v72 op_sel:[0,0,1]
	v_mul_f32_e32 v72, 0x43000000, v75
	v_mul_f32_e32 v73, 0x43000000, v83
	v_med3_f32 v72, v72, s26, v147
	v_med3_f32 v73, v73, s26, v147
	v_mov_b32_e32 v75, v129
	v_cvt_pk_fp8_f32 v75, v72, v73
	v_mul_f32_e32 v74, 0x43000000, v95
	v_mul_f32_e32 v72, 0x43000000, v91
	v_med3_f32 v73, v74, s26, v147
	v_med3_f32 v72, v72, s26, v147
	s_waitcnt vmcnt(19)
	v_mul_f32_e32 v64, 0x43000000, v64
	s_waitcnt vmcnt(18)
	v_mul_f32_e32 v68, 0x43000000, v68
	v_cvt_pk_fp8_f32 v75, v73, v72 op_sel:[0,0,1]
	v_med3_f32 v64, v64, s26, v147
	v_med3_f32 v68, v68, s26, v147
	v_mov_b32_e32 v73, v129
	v_cvt_pk_fp8_f32 v73, v64, v68
	s_waitcnt vmcnt(17)
	v_mul_f32_e32 v72, 0x43000000, v84
	s_waitcnt vmcnt(16)
	v_mul_f32_e32 v64, 0x43000000, v76
	v_med3_f32 v68, v72, s26, v147
	v_med3_f32 v64, v64, s26, v147
	v_cvt_pk_fp8_f32 v73, v68, v64 op_sel:[0,0,1]
	v_mul_f32_e32 v64, 0x43000000, v65
	v_mul_f32_e32 v65, 0x43000000, v69
	v_med3_f32 v64, v64, s26, v147
	v_med3_f32 v65, v65, s26, v147
	v_mov_b32_e32 v69, v129
	v_cvt_pk_fp8_f32 v69, v64, v65
	v_mul_f32_e32 v68, 0x43000000, v85
	v_mul_f32_e32 v64, 0x43000000, v77
	v_med3_f32 v65, v68, s26, v147
	v_med3_f32 v64, v64, s26, v147
	v_cvt_pk_fp8_f32 v69, v65, v64 op_sel:[0,0,1]
	v_mul_f32_e32 v64, 0x43000000, v66
	v_mul_f32_e32 v65, 0x43000000, v70
	v_med3_f32 v64, v64, s26, v147
	v_med3_f32 v65, v65, s26, v147
	v_mov_b32_e32 v68, v129
	v_cvt_pk_fp8_f32 v68, v64, v65
	s_lshl_b32 s6, s13, 7
	v_mul_f32_e32 v66, 0x43000000, v86
	v_mul_f32_e32 v64, 0x43000000, v78
	v_lshl_add_u64 v[32:33], v[132:133], 0, s[6:7]
	s_mul_i32 s6, s13, 0x84
	v_med3_f32 v65, v66, s26, v147
	v_med3_f32 v64, v64, s26, v147
	v_lshl_add_u64 v[34:35], v[132:133], 0, s[6:7]
	s_mul_i32 s6, s13, 0x88
	v_cvt_pk_fp8_f32 v68, v65, v64 op_sel:[0,0,1]
	v_mul_f32_e32 v64, 0x43000000, v67
	v_mul_f32_e32 v65, 0x43000000, v71
	global_load_dwordx4 v[40:43], v[32:33], off
	global_load_dwordx4 v[48:51], v[34:35], off
	v_lshl_add_u64 v[32:33], v[132:133], 0, s[6:7]
	s_mul_i32 s6, s13, 0x8c
	v_med3_f32 v64, v64, s26, v147
	v_med3_f32 v65, v65, s26, v147
	v_mov_b32_e32 v67, v129
	v_lshl_add_u64 v[34:35], v[132:133], 0, s[6:7]
	s_mul_i32 s6, s13, 0xc0
	v_cvt_pk_fp8_f32 v67, v64, v65
	global_load_dwordx4 v[60:63], v[32:33], off
	global_load_dwordx4 v[56:59], v[34:35], off
	v_lshl_add_u64 v[32:33], v[132:133], 0, s[6:7]
	s_mul_i32 s6, s13, 0xc4
	v_lshl_add_u64 v[36:37], v[132:133], 0, s[6:7]
	s_mul_i32 s6, s13, 0xc8
	v_mul_f32_e32 v66, 0x43000000, v87
	v_mul_f32_e32 v64, 0x43000000, v79
	v_lshl_add_u64 v[44:45], v[132:133], 0, s[6:7]
	s_mul_i32 s6, s13, 0xcc
	v_med3_f32 v65, v66, s26, v147
	v_med3_f32 v64, v64, s26, v147
	v_lshl_add_u64 v[46:47], v[132:133], 0, s[6:7]
	v_cvt_pk_fp8_f32 v67, v65, v64 op_sel:[0,0,1]
	s_waitcnt vmcnt(19)
; #define LAS __attribute__((address_space(3)))
; #define LDS_WAIT() asm volatile("s_waitcnt lgkmcnt(0)" ::: "memory")
; #define CV_LOAD(qi, Q, D) do { _Pragma("unroll") for (int s_ = 0; s_ < 2; ++s_) _Pragma("unroll") for (int r_ = 0; r_ < 4; ++r_) Q.v[s_][r_] = *(const f32x4*)(D.src + (size_t)(16 * (2 * (qi) + s_) + r_) * D.N); asm volatile("" ::: "memory"); } while (0)
; #define CV_PROC(qi, Q) do { _Pragma("unroll") for (int s_ = 0; s_ < 2; ++s_) _Pragma("unroll") for (int c_ = 0; c_ < 4; ++c_) \
;         *(LAS unsigned*)(scr + (4 * nl + c_) * 132 + 16 * (2 * (qi) + s_) + 4 * kg) = pg8::pk4_fp8c(Q.v[s_][0][c_] * FP8_WSC, Q.v[s_][1][c_] * FP8_WSC, Q.v[s_][2][c_] * FP8_WSC, Q.v[s_][3][c_] * FP8_WSC); asm volatile("" ::: "memory"); } while (0)
; __device__ __forceinline__ void moe_conv_stream(const Args& a, ARGAS unsigned char* ws, LAS unsigned char* scr, int first, int cnt, int lane) {
;     ...
;     Qt A, B, C, D4;
;     ConvItem cur = moe_conv_desc(a, ws, first, lane);
;     CV_LOAD(0, A, cur); CV_LOAD(1, B, cur); CV_LOAD(2, C, cur);
; #pragma unroll 1
;     for (int i = 0; i < cnt; ++i) {
;         const ConvItem nxt = moe_conv_desc(a, ws, first + 8 * ((i + 1 < cnt) ? i + 1 : i), lane);
;         CV_LOAD(3, D4, cur); CV_PROC(0, A);
;         CV_LOAD(0, A, nxt);  CV_PROC(1, B);
;         CV_LOAD(1, B, nxt);  CV_PROC(2, C);
;         CV_LOAD(2, C, nxt);  CV_PROC(3, D4);
;         LDS_WAIT(); asm volatile("" ::: "memory");
;         const int n0 = cur.gu > 0 ? cur.gu - 1 : -cur.gu - 1;
; #pragma unroll
;         for (int j = 0; j < 8; ++j) { const int row = (lane >> 3) + 8 * j; const LAS unsigned* s = (const LAS unsigned*)(scr + row * 132 + 16 * c8);
;             u32x4 o; o.x = s[0]; o.y = s[1]; o.z = s[2]; o.w = s[3];
;             const int n = n0 + row, wr_ = cur.gu > 0 ? RmGu()(n) : n;
;             *(u32x4*)(cur.dst + (size_t)wr_ * cur.ldk + 16 * c8) = o; }
	v_mul_f32_e32 v116, 0x43000000, v116
	s_waitcnt vmcnt(18)
	v_mul_f32_e32 v120, 0x43000000, v120
	global_load_dwordx4 v[32:35], v[32:33], off
	s_nop 0
	global_load_dwordx4 v[36:39], v[36:37], off
	s_nop 0
	global_load_dwordx4 v[52:55], v[44:45], off
	s_nop 0
	global_load_dwordx4 v[44:47], v[46:47], off
	ds_write2_b32 v144, v148, v73 offset0:16 offset1:20
	ds_write2_b32 v144, v81, v69 offset0:49 offset1:53
	ds_write2_b32 v144, v80, v68 offset0:82 offset1:86
	ds_write2_b32 v144, v75, v67 offset0:115 offset1:119
	v_med3_f32 v116, v116, s26, v147
	v_med3_f32 v120, v120, s26, v147
	v_mov_b32_e32 v148, v129
	v_cvt_pk_fp8_f32 v148, v116, v120
	s_waitcnt vmcnt(21)
	v_mul_f32_e32 v124, 0x43000000, v124
	s_waitcnt vmcnt(20)
	v_mul_f32_e32 v112, 0x43000000, v112
	v_med3_f32 v116, v124, s26, v147
	v_med3_f32 v112, v112, s26, v147
	v_cvt_pk_fp8_f32 v148, v116, v112 op_sel:[0,0,1]
	v_mul_f32_e32 v112, 0x43000000, v117
	v_mul_f32_e32 v116, 0x43000000, v121
	v_med3_f32 v112, v112, s26, v147
	v_med3_f32 v116, v116, s26, v147
	v_mov_b32_e32 v120, v129
	v_cvt_pk_fp8_f32 v120, v112, v116
	v_mul_f32_e32 v117, 0x43000000, v125
	v_mul_f32_e32 v112, 0x43000000, v113
	v_med3_f32 v113, v117, s26, v147
	v_med3_f32 v112, v112, s26, v147
	v_cvt_pk_fp8_f32 v120, v113, v112 op_sel:[0,0,1]
	v_mul_f32_e32 v112, 0x43000000, v118
	v_mul_f32_e32 v113, 0x43000000, v122
	v_med3_f32 v112, v112, s26, v147
	v_med3_f32 v113, v113, s26, v147
	v_mov_b32_e32 v117, v129
	v_cvt_pk_fp8_f32 v117, v112, v113
	v_mul_f32_e32 v116, 0x43000000, v126
	v_mul_f32_e32 v112, 0x43000000, v114
	v_med3_f32 v113, v116, s26, v147
	v_med3_f32 v112, v112, s26, v147
	v_cvt_pk_fp8_f32 v117, v113, v112 op_sel:[0,0,1]
	v_mul_f32_e32 v112, 0x43000000, v119
	v_mul_f32_e32 v113, 0x43000000, v123
	v_med3_f32 v112, v112, s26, v147
	v_med3_f32 v113, v113, s26, v147
	v_mov_b32_e32 v116, v129
	v_cvt_pk_fp8_f32 v116, v112, v113
	v_mul_f32_e32 v114, 0x43000000, v127
	v_mul_f32_e32 v112, 0x43000000, v115
	v_med3_f32 v113, v114, s26, v147
	v_med3_f32 v112, v112, s26, v147
	s_waitcnt vmcnt(19)
	v_mul_f32_e32 v100, 0x43000000, v100
	s_waitcnt vmcnt(18)
	v_mul_f32_e32 v104, 0x43000000, v104
	v_cvt_pk_fp8_f32 v116, v113, v112 op_sel:[0,0,1]
	v_med3_f32 v100, v100, s26, v147
	v_med3_f32 v104, v104, s26, v147
	v_mov_b32_e32 v112, v129
	v_cvt_pk_fp8_f32 v112, v100, v104
	s_waitcnt vmcnt(17)
	v_mul_f32_e32 v108, 0x43000000, v108
	s_waitcnt vmcnt(16)
	v_mul_f32_e32 v96, 0x43000000, v96
	v_med3_f32 v100, v108, s26, v147
	v_med3_f32 v96, v96, s26, v147
	v_cvt_pk_fp8_f32 v112, v100, v96 op_sel:[0,0,1]
	v_mul_f32_e32 v96, 0x43000000, v101
	v_mul_f32_e32 v100, 0x43000000, v105
	v_med3_f32 v96, v96, s26, v147
	v_med3_f32 v100, v100, s26, v147
	v_mov_b32_e32 v104, v129
	v_cvt_pk_fp8_f32 v104, v96, v100
	v_mul_f32_e32 v101, 0x43000000, v109
	v_mul_f32_e32 v96, 0x43000000, v97
	v_med3_f32 v97, v101, s26, v147
	v_med3_f32 v96, v96, s26, v147
	s_lshl_b32 s6, s13, 8
	v_cvt_pk_fp8_f32 v104, v97, v96 op_sel:[0,0,1]
	v_mul_f32_e32 v96, 0x43000000, v102
	v_mul_f32_e32 v97, 0x43000000, v106
	v_lshl_add_u64 v[64:65], v[132:133], 0, s[6:7]
	s_mul_i32 s6, s13, 0x104
	v_med3_f32 v96, v96, s26, v147
	v_med3_f32 v97, v97, s26, v147
	v_mov_b32_e32 v101, v129
	v_lshl_add_u64 v[66:67], v[132:133], 0, s[6:7]
	s_mul_i32 s6, s13, 0x108
	v_cvt_pk_fp8_f32 v101, v96, v97
	global_load_dwordx4 v[72:75], v[64:65], off
	global_load_dwordx4 v[80:83], v[66:67], off
	v_lshl_add_u64 v[64:65], v[132:133], 0, s[6:7]
	s_mul_i32 s6, s13, 0x10c
	v_lshl_add_u64 v[66:67], v[132:133], 0, s[6:7]
	s_mul_i32 s6, s13, 0x140
	v_mul_f32_e32 v100, 0x43000000, v110
	v_mul_f32_e32 v96, 0x43000000, v98
	global_load_dwordx4 v[92:95], v[64:65], off
	global_load_dwordx4 v[88:91], v[66:67], off
	v_lshl_add_u64 v[64:65], v[132:133], 0, s[6:7]
	s_mul_i32 s6, s13, 0x144
	v_med3_f32 v97, v100, s26, v147
	v_med3_f32 v96, v96, s26, v147
	v_lshl_add_u64 v[68:69], v[132:133], 0, s[6:7]
	s_mul_i32 s6, s13, 0x148
	v_cvt_pk_fp8_f32 v101, v97, v96 op_sel:[0,0,1]
	v_mul_f32_e32 v96, 0x43000000, v103
	v_mul_f32_e32 v97, 0x43000000, v107
	v_lshl_add_u64 v[76:77], v[132:133], 0, s[6:7]
	s_mul_i32 s6, s13, 0x14c
	v_med3_f32 v96, v96, s26, v147
	v_med3_f32 v97, v97, s26, v147
	v_mov_b32_e32 v100, v129
	v_lshl_add_u64 v[78:79], v[132:133], 0, s[6:7]
	v_cvt_pk_fp8_f32 v100, v96, v97
	s_add_i32 s6, s37, -1
	s_not_b32 s12, s37
	s_cmp_gt_i32 s37, 0
	global_load_dwordx4 v[64:67], v[64:65], off
	s_nop 0
	global_load_dwordx4 v[68:71], v[68:69], off
	s_nop 0
	global_load_dwordx4 v[84:87], v[76:77], off
	s_nop 0
	global_load_dwordx4 v[76:79], v[78:79], off
	v_mul_f32_e32 v98, 0x43000000, v111
	v_mul_f32_e32 v96, 0x43000000, v99
	s_cselect_b64 vcc, -1, 0
	v_med3_f32 v97, v98, s26, v147
	v_med3_f32 v96, v96, s26, v147
	s_and_b64 s[14:15], vcc, exec
	v_cvt_pk_fp8_f32 v100, v97, v96 op_sel:[0,0,1]
	s_cselect_b32 s6, s6, s12
	ds_write2_b32 v144, v148, v112 offset0:24 offset1:28
	ds_write2_b32 v144, v120, v104 offset0:57 offset1:61
	ds_write2_b32 v144, v117, v101 offset0:90 offset1:94
	ds_write2_b32 v144, v116, v100 offset0:123 offset1:127
	v_add_u32_e32 v100, s6, v194
	v_lshlrev_b32_e32 v101, 1, v100
	v_ashrrev_i32_e32 v102, 3, v100
	s_waitcnt lgkmcnt(0)
	v_and_b32_e32 v101, 0x700, v101
	v_and_b32_e32 v102, 0xffffff80, v102
	v_add_u32_e32 v101, v101, v102
	ds_read2_b32 v[96:97], v145 offset1:1
	ds_read2_b32 v[98:99], v145 offset0:2 offset1:3
	v_and_or_b32 v101, v100, s27, v101
	v_cndmask_b32_e32 v100, v100, v101, vcc
	v_ashrrev_i32_e32 v101, 31, v100
	v_lshl_add_u64 v[104:105], s[8:9], 0, v[130:131]
	v_lshlrev_b64 v[100:101], 10, v[100:101]
	v_lshl_add_u64 v[106:107], v[104:105], 0, v[100:101]
	v_add_u32_e32 v100, 0x420, v145
	v_add_u32_e32 v102, 0x428, v145
	ds_read2_b32 v[100:101], v100 offset1:1
	ds_read2_b32 v[102:103], v102 offset1:1
	s_waitcnt lgkmcnt(2)
; #define LAS __attribute__((address_space(3)))
; #define LDS_WAIT() asm volatile("s_waitcnt lgkmcnt(0)" ::: "memory")
; #define CV_LOAD(qi, Q, D) do { _Pragma("unroll") for (int s_ = 0; s_ < 2; ++s_) _Pragma("unroll") for (int r_ = 0; r_ < 4; ++r_) Q.v[s_][r_] = *(const f32x4*)(D.src + (size_t)(16 * (2 * (qi) + s_) + r_) * D.N); asm volatile("" ::: "memory"); } while (0)
; __device__ __forceinline__ ConvItem moe_conv_desc(const Args& a, ARGAS unsigned char* ws, int it, int lane) {
;     const int m = it / MOE_CONV_PER_M, r = it % MOE_CONV_PER_M, nl = lane & 15, kg = lane >> 4; ConvItem d;
;     if (r < 256) { const int kb = r / 32, nb = r % 32; d.N = 2048; d.ldk = DM; d.gu = 64 * nb + 1; d.src = a.moe_w_gu + (size_t)m * DM * 2048 + (size_t)(128 * kb + 4 * kg) * 2048 + 64 * nb + 4 * nl; d.dst = (unsigned char*)(ws + WS_WGU) + (size_t)m * 2048 * DM + 128 * kb; }
;     else { const int r2 = r - 256, kb = r2 / 16, nb = r2 % 16; d.N = DM; d.ldk = EFF; d.gu = -(64 * nb) - 1; d.src = a.moe_w_down + (size_t)m * EFF * DM + (size_t)(128 * kb + 4 * kg) * DM + 64 * nb + 4 * nl; d.dst = (unsigned char*)(ws + WS_WDN) + (size_t)m * DM * EFF + 128 * kb; }
;     return d;
; __device__ __forceinline__ void moe_conv_stream(const Args& a, ARGAS unsigned char* ws, LAS unsigned char* scr, int first, int cnt, int lane) {
;     ...
;     for (int i = 0; i < cnt; ++i) {
;         const ConvItem nxt = moe_conv_desc(a, ws, first + 8 * ((i + 1 < cnt) ? i + 1 : i), lane);
;         CV_LOAD(3, D4, cur); CV_PROC(0, A);
;         CV_LOAD(0, A, nxt);  CV_PROC(1, B);
;         CV_LOAD(1, B, nxt);  CV_PROC(2, C);
;         CV_LOAD(2, C, nxt);  CV_PROC(3, D4);
;         LDS_WAIT(); asm volatile("" ::: "memory");
;         const int n0 = cur.gu > 0 ? cur.gu - 1 : -cur.gu - 1;
; #pragma unroll
;         for (int j = 0; j < 8; ++j) { const int row = (lane >> 3) + 8 * j; const LAS unsigned* s = (const LAS unsigned*)(scr + row * 132 + 16 * c8);
;             u32x4 o; o.x = s[0]; o.y = s[1]; o.z = s[2]; o.w = s[3];
;             const int n = n0 + row, wr_ = cur.gu > 0 ? RmGu()(n) : n;
;             *(u32x4*)(cur.dst + (size_t)wr_ * cur.ldk + 16 * c8) = o; }
;         LDS_WAIT(); asm volatile("" ::: "memory");
;         cur = nxt;
	global_store_dwordx4 v[106:107], v[96:99], off
	s_add_i32 s38, s38, 8
	s_cmpk_eq_i32 s38, 0x28
	v_add_u32_e32 v96, s6, v135
	v_lshlrev_b32_e32 v97, 1, v96
	v_ashrrev_i32_e32 v98, 3, v96
	v_and_b32_e32 v97, 0x700, v97
	v_and_b32_e32 v98, 0xffffff80, v98
	v_add_u32_e32 v97, v97, v98
	v_and_or_b32 v97, v96, s27, v97
	v_cndmask_b32_e32 v96, v96, v97, vcc
	v_ashrrev_i32_e32 v97, 31, v96
	v_lshlrev_b64 v[96:97], 10, v[96:97]
	v_lshl_add_u64 v[96:97], v[104:105], 0, v[96:97]
	s_waitcnt lgkmcnt(0)
	global_store_dwordx4 v[96:97], v[100:103], off
	v_add_u32_e32 v96, 0x840, v145
	v_add_u32_e32 v98, 0x848, v145
	v_add_u32_e32 v100, s6, v136
	v_lshlrev_b32_e32 v101, 1, v100
	v_ashrrev_i32_e32 v102, 3, v100
	v_and_b32_e32 v101, 0x700, v101
	v_and_b32_e32 v102, 0xffffff80, v102
	v_add_u32_e32 v101, v101, v102
	ds_read2_b32 v[96:97], v96 offset1:1
	ds_read2_b32 v[98:99], v98 offset1:1
	v_and_or_b32 v101, v100, s27, v101
	v_cndmask_b32_e32 v100, v100, v101, vcc
	v_ashrrev_i32_e32 v101, 31, v100
	v_lshlrev_b64 v[100:101], 10, v[100:101]
	v_lshl_add_u64 v[106:107], v[104:105], 0, v[100:101]
	v_add_u32_e32 v100, 0xc60, v145
	v_add_u32_e32 v102, 0xc68, v145
	ds_read2_b32 v[100:101], v100 offset1:1
	ds_read2_b32 v[102:103], v102 offset1:1
	s_waitcnt lgkmcnt(2)
	global_store_dwordx4 v[106:107], v[96:99], off
	s_mov_b32 s37, s39
	s_mov_b64 s[8:9], s[10:11]
	v_add_u32_e32 v96, s6, v137
	v_lshlrev_b32_e32 v97, 1, v96
	v_ashrrev_i32_e32 v98, 3, v96
	v_and_b32_e32 v97, 0x700, v97
	v_and_b32_e32 v98, 0xffffff80, v98
	v_add_u32_e32 v97, v97, v98
	v_and_or_b32 v97, v96, s27, v97
	v_cndmask_b32_e32 v96, v96, v97, vcc
	v_ashrrev_i32_e32 v97, 31, v96
	v_lshlrev_b64 v[96:97], 10, v[96:97]
	v_lshl_add_u64 v[96:97], v[104:105], 0, v[96:97]
	s_waitcnt lgkmcnt(0)
	global_store_dwordx4 v[96:97], v[100:103], off
	v_add_u32_e32 v96, 0x1080, v145
	v_add_u32_e32 v98, 0x1088, v145
	v_add_u32_e32 v100, s6, v138
	v_lshlrev_b32_e32 v101, 1, v100
	v_ashrrev_i32_e32 v102, 3, v100
	v_and_b32_e32 v101, 0x700, v101
	v_and_b32_e32 v102, 0xffffff80, v102
	v_add_u32_e32 v101, v101, v102
	ds_read2_b32 v[96:97], v96 offset1:1
	ds_read2_b32 v[98:99], v98 offset1:1
	v_and_or_b32 v101, v100, s27, v101
	v_cndmask_b32_e32 v100, v100, v101, vcc
	v_ashrrev_i32_e32 v101, 31, v100
	v_lshlrev_b64 v[100:101], 10, v[100:101]
	v_lshl_add_u64 v[106:107], v[104:105], 0, v[100:101]
	v_add_u32_e32 v100, 0x14a0, v145
	v_add_u32_e32 v102, 0x14a8, v145
	ds_read2_b32 v[100:101], v100 offset1:1
	ds_read2_b32 v[102:103], v102 offset1:1
	s_waitcnt lgkmcnt(2)
	global_store_dwordx4 v[106:107], v[96:99], off
	s_nop 1
	v_add_u32_e32 v96, s6, v139
	v_lshlrev_b32_e32 v97, 1, v96
	v_ashrrev_i32_e32 v98, 3, v96
	v_and_b32_e32 v97, 0x700, v97
	v_and_b32_e32 v98, 0xffffff80, v98
	v_add_u32_e32 v97, v97, v98
	v_and_or_b32 v97, v96, s27, v97
	v_cndmask_b32_e32 v96, v96, v97, vcc
	v_ashrrev_i32_e32 v97, 31, v96
	v_lshlrev_b64 v[96:97], 10, v[96:97]
	v_lshl_add_u64 v[96:97], v[104:105], 0, v[96:97]
	s_waitcnt lgkmcnt(0)
	global_store_dwordx4 v[96:97], v[100:103], off
	v_add_u32_e32 v96, 0x18c0, v145
	v_add_u32_e32 v98, 0x18c8, v145
	v_add_u32_e32 v100, s6, v140
	v_lshlrev_b32_e32 v101, 1, v100
	v_ashrrev_i32_e32 v102, 3, v100
	v_and_b32_e32 v101, 0x700, v101
	v_and_b32_e32 v102, 0xffffff80, v102
	v_add_u32_e32 v101, v101, v102
	ds_read2_b32 v[96:97], v96 offset1:1
	ds_read2_b32 v[98:99], v98 offset1:1
	v_and_or_b32 v101, v100, s27, v101
	v_cndmask_b32_e32 v100, v100, v101, vcc
	v_ashrrev_i32_e32 v101, 31, v100
	v_lshlrev_b64 v[100:101], 10, v[100:101]
	v_lshl_add_u64 v[106:107], v[104:105], 0, v[100:101]
	v_add_u32_e32 v100, 0x1ce0, v145
	v_add_u32_e32 v102, 0x1ce8, v145
	ds_read2_b32 v[100:101], v100 offset1:1
	ds_read2_b32 v[102:103], v102 offset1:1
	s_waitcnt lgkmcnt(2)
	global_store_dwordx4 v[106:107], v[96:99], off
	s_nop 1
	v_add_u32_e32 v96, s6, v141
	v_lshlrev_b32_e32 v97, 1, v96
	v_ashrrev_i32_e32 v98, 3, v96
	v_and_b32_e32 v97, 0x700, v97
	v_and_b32_e32 v98, 0xffffff80, v98
	v_add_u32_e32 v97, v97, v98
	v_and_or_b32 v97, v96, s27, v97
	v_cndmask_b32_e32 v96, v96, v97, vcc
	v_ashrrev_i32_e32 v97, 31, v96
	v_lshlrev_b64 v[96:97], 10, v[96:97]
	v_lshl_add_u64 v[96:97], v[104:105], 0, v[96:97]
	s_waitcnt lgkmcnt(0)
	global_store_dwordx4 v[96:97], v[100:103], off
	s_waitcnt lgkmcnt(0)
	s_mov_b32 s6, s13
	v_mov_b64_e32 v[96:97], v[132:133]
	s_cbranch_scc1 .LBB0_654
.LBB0_667:
	s_cmpk_lg_i32 s38, 0x20
	s_cselect_b32 s10, s38, 0x18
	s_add_i32 s10, s10, s36
	s_mul_hi_i32 s11, s10, 0x2aaaaaab
	s_lshr_b32 s12, s11, 31
	s_ashr_i32 s11, s11, 6
	s_add_i32 s12, s11, s12
	s_mul_i32 s11, s12, 0x180
	s_sub_i32 s40, s10, s11
	s_cmpk_gt_i32 s40, 0xff
	s_cbranch_scc0 .LBB0_669
	s_load_dwordx2 s[10:11], s[20:21], 0xe0
	s_lshl_b32 s13, s40, 6
	s_and_b32 s41, s13, 0x3c0
	s_ashr_i32 s13, s12, 31
	s_not_b32 s39, s41
	s_lshl_b64 s[14:15], s[12:13], 20
	s_lshl_b64 s[42:43], s[12:13], 22
	s_waitcnt lgkmcnt(0)
	s_add_u32 s10, s10, s42
	s_addc_u32 s11, s11, s43
	s_lshl_b32 s13, s40, 3
	s_and_b32 s13, s13, 0x7fffff80
	s_addk_i32 s13, 0xf800
	v_or_b32_e32 v98, s13, v134
	v_mov_b32_e32 v99, v129
	v_lshlrev_b64 v[98:99], 12, v[98:99]
	v_lshl_add_u64 v[98:99], s[10:11], 0, v[98:99]
	s_lshl_b32 s10, s41, 2
	s_mov_b32 s11, s7
	v_lshl_add_u64 v[98:99], v[98:99], 0, s[10:11]
	s_add_u32 s10, s16, s14
	s_addc_u32 s11, s17, s15
	s_add_u32 s10, s10, s13
	s_addc_u32 s11, s11, 0
	s_movk_i32 s13, 0x400
	s_cbranch_execnz .LBB0_666
	s_branch .LBB0_670

; __device__ __forceinline__ unsigned xb_add(gbar_t p, unsigned v) { return __hip_atomic_fetch_add(p, v, __ATOMIC_RELAXED, __HIP_MEMORY_SCOPE_AGENT); }
; __device__ __forceinline__ ConvItem moe_conv_desc(const Args& a, ARGAS unsigned char* ws, int it, int lane) {
;     const int m = it / MOE_CONV_PER_M, r = it % MOE_CONV_PER_M, nl = lane & 15, kg = lane >> 4; ConvItem d;
;     if (r < 256) { const int kb = r / 32, nb = r % 32; d.N = 2048; d.ldk = DM; d.gu = 64 * nb + 1; d.src = a.moe_w_gu + (size_t)m * DM * 2048 + (size_t)(128 * kb + 4 * kg) * 2048 + 64 * nb + 4 * nl; d.dst = (unsigned char*)(ws + WS_WGU) + (size_t)m * 2048 * DM + 128 * kb; }
;     else { const int r2 = r - 256, kb = r2 / 16, nb = r2 % 16; d.N = DM; d.ldk = EFF; d.gu = -(64 * nb) - 1; d.src = a.moe_w_down + (size_t)m * EFF * DM + (size_t)(128 * kb + 4 * kg) * DM + 64 * nb + 4 * nl; d.dst = (unsigned char*)(ws + WS_WDN) + (size_t)m * DM * EFF + 128 * kb; }
;     return d;
; __device__ __forceinline__ void moe_conv_drain(const Frame& F, const Args& a, ARGAS unsigned char* ws, gbar_t head, LAS unsigned* qslot, const int first_chunk, const int nchunks) {
;     ...
;         __syncthreads();
;         if (F.tid == 0) *qslot = xb_add(head, 1u);
;         __syncthreads();
;         const unsigned ch = *qslot;
;         if (ch >= (unsigned)nchunks) break;
;         moe_conv_stream(a, ws, scr, (first_chunk + (int)ch) * MOE_CONV_CHUNK + F.wave, MOE_CONV_CHUNK / 8, F.lane);
.LBB0_3121:
	s_or_b64 exec, exec, s[8:9]
	s_waitcnt lgkmcnt(0)
	s_barrier
	s_waitcnt vmcnt(27)
	ds_read_b32 v0, v144
	s_mov_b64 s[8:9], -1
	s_waitcnt lgkmcnt(0)
	s_movk_i32 s98, 0x2ff
	v_cmp_lt_u32_e32 vcc, s98, v0
	v_readfirstlane_b32 s6, v0
	s_cbranch_vccnz .LBB0_3116
	s_lshl_b32 s6, s6, 5
	s_add_i32 s39, s26, s6
	s_mul_hi_i32 s6, s39, 0x2aaaaaab
	s_lshr_b32 s8, s6, 31
	s_ashr_i32 s6, s6, 6
	s_add_i32 s10, s6, s8
	s_mul_i32 s6, s10, 0x180
	s_sub_i32 s14, s39, s6
	s_cmpk_gt_i32 s14, 0xff
	s_cbranch_scc0 .LBB0_3124
	s_load_dwordx2 s[8:9], s[20:21], 0xe0
	s_lshl_b32 s6, s14, 6
	s_and_b32 s6, s6, 0x3c0
	s_ashr_i32 s11, s10, 31
	s_not_b32 s40, s6
	s_lshl_b64 s[12:13], s[10:11], 20
	s_lshl_b64 s[42:43], s[10:11], 22
	s_waitcnt lgkmcnt(0)
	s_add_u32 s8, s8, s42
	s_addc_u32 s9, s9, s43
	s_lshl_b32 s11, s14, 3
	s_and_b32 s11, s11, 0x7fffff80
	s_addk_i32 s11, 0xf800
	v_or_b32_e32 v0, s11, v136
	v_mov_b32_e32 v1, v129
	v_lshlrev_b64 v[0:1], 12, v[0:1]
	v_lshl_add_u64 v[0:1], s[8:9], 0, v[0:1]
	s_lshl_b32 s6, s6, 2
	v_lshl_add_u64 v[0:1], v[0:1], 0, s[6:7]
	s_add_u32 s6, s16, s12
	s_addc_u32 s9, s17, s13
	s_add_u32 s8, s6, s11
	s_addc_u32 s9, s9, 0
	s_movk_i32 s11, 0x400
	s_cbranch_execz .LBB0_3125
	s_branch .LBB0_3126

; #define CV_LOAD(qi, Q, D) do { _Pragma("unroll") for (int s_ = 0; s_ < 2; ++s_) _Pragma("unroll") for (int r_ = 0; r_ < 4; ++r_) Q.v[s_][r_] = *(const f32x4*)(D.src + (size_t)(16 * (2 * (qi) + s_) + r_) * D.N); asm volatile("" ::: "memory"); } while (0)
; #define CV_PROC(qi, Q) do { _Pragma("unroll") for (int s_ = 0; s_ < 2; ++s_) _Pragma("unroll") for (int c_ = 0; c_ < 4; ++c_) \
;         *(LAS unsigned*)(scr + (4 * nl + c_) * 132 + 16 * (2 * (qi) + s_) + 4 * kg) = pg8::pk4_fp8c(Q.v[s_][0][c_] * FP8_WSC, Q.v[s_][1][c_] * FP8_WSC, Q.v[s_][2][c_] * FP8_WSC, Q.v[s_][3][c_] * FP8_WSC); asm volatile("" ::: "memory"); } while (0)
; __device__ __forceinline__ void moe_conv_stream(const Args& a, ARGAS unsigned char* ws, LAS unsigned char* scr, int first, int cnt, int lane) {
;     ...
;     Qt A, B, C, D4;
;     ConvItem cur = moe_conv_desc(a, ws, first, lane);
;     CV_LOAD(0, A, cur); CV_LOAD(1, B, cur); CV_LOAD(2, C, cur);
; #pragma unroll 1
;     for (int i = 0; i < cnt; ++i) {
;         const ConvItem nxt = moe_conv_desc(a, ws, first + 8 * ((i + 1 < cnt) ? i + 1 : i), lane);
;         CV_LOAD(3, D4, cur); CV_PROC(0, A);
;         CV_LOAD(0, A, nxt);  CV_PROC(1, B);
;         CV_LOAD(1, B, nxt);  CV_PROC(2, C);
;         CV_LOAD(2, C, nxt);  CV_PROC(3, D4);
.LBB0_3127:
	s_waitcnt vmcnt(17)
	v_mul_f32_e32 v28, 0x43000000, v28
	v_mul_f32_e32 v16, 0x43000000, v16
	v_med3_f32 v28, v28, s37, v149
	v_med3_f32 v16, v16, s37, v149
	v_mov_b32_e32 v150, v129
	v_cvt_pk_fp8_f32 v150, v28, v16
	v_mul_f32_e32 v20, 0x43000000, v20
	v_mul_f32_e32 v16, 0x43000000, v24
	v_med3_f32 v20, v20, s37, v149
	v_med3_f32 v16, v16, s37, v149
	v_cvt_pk_fp8_f32 v150, v20, v16 op_sel:[0,0,1]
	v_mul_f32_e32 v16, 0x43000000, v29
	v_mul_f32_e32 v17, 0x43000000, v17
	v_mul_f32_e32 v20, 0x43000000, v21
	v_med3_f32 v16, v16, s37, v149
	v_med3_f32 v17, v17, s37, v149
	v_mov_b32_e32 v21, v129
	v_cvt_pk_fp8_f32 v21, v16, v17
	v_mul_f32_e32 v16, 0x43000000, v25
	v_med3_f32 v17, v20, s37, v149
	v_med3_f32 v16, v16, s37, v149
	v_cvt_pk_fp8_f32 v21, v17, v16 op_sel:[0,0,1]
	v_mul_f32_e32 v16, 0x43000000, v30
	v_mul_f32_e32 v17, 0x43000000, v18
	v_med3_f32 v16, v16, s37, v149
	v_med3_f32 v17, v17, s37, v149
	v_mov_b32_e32 v20, v129
	v_cvt_pk_fp8_f32 v20, v16, v17
	v_mul_f32_e32 v18, 0x43000000, v22
	v_mul_f32_e32 v16, 0x43000000, v26
	v_med3_f32 v17, v18, s37, v149
	v_med3_f32 v16, v16, s37, v149
	v_cvt_pk_fp8_f32 v20, v17, v16 op_sel:[0,0,1]
	v_mul_f32_e32 v16, 0x43000000, v31
	v_mul_f32_e32 v17, 0x43000000, v19
	v_med3_f32 v16, v16, s37, v149
	v_med3_f32 v17, v17, s37, v149
	v_mov_b32_e32 v19, v129
	v_cvt_pk_fp8_f32 v19, v16, v17
	v_mul_f32_e32 v18, 0x43000000, v23
	v_mul_f32_e32 v16, 0x43000000, v27
	v_med3_f32 v17, v18, s37, v149
	v_med3_f32 v16, v16, s37, v149
	v_mul_f32_e32 v0, 0x43000000, v0
	v_mul_f32_e32 v4, 0x43000000, v4
	v_cvt_pk_fp8_f32 v19, v17, v16 op_sel:[0,0,1]
	v_med3_f32 v0, v0, s37, v149
	v_med3_f32 v4, v4, s37, v149
	v_mov_b32_e32 v16, v129
	v_cvt_pk_fp8_f32 v16, v0, v4
	v_mul_f32_e32 v8, 0x43000000, v8
	s_waitcnt vmcnt(16)
	v_mul_f32_e32 v0, 0x43000000, v12
	v_med3_f32 v4, v8, s37, v149
	v_med3_f32 v0, v0, s37, v149
	v_cvt_pk_fp8_f32 v16, v4, v0 op_sel:[0,0,1]
	v_mul_f32_e32 v0, 0x43000000, v1
	v_mul_f32_e32 v1, 0x43000000, v5
	v_med3_f32 v0, v0, s37, v149
	v_med3_f32 v1, v1, s37, v149
	v_mov_b32_e32 v5, v129
	v_cvt_pk_fp8_f32 v5, v0, v1
	v_mul_f32_e32 v4, 0x43000000, v9
	v_mul_f32_e32 v0, 0x43000000, v13
	v_med3_f32 v1, v4, s37, v149
	v_med3_f32 v0, v0, s37, v149
	v_cvt_pk_fp8_f32 v5, v1, v0 op_sel:[0,0,1]
	v_mul_f32_e32 v0, 0x43000000, v2
	v_mul_f32_e32 v1, 0x43000000, v6
	v_med3_f32 v0, v0, s37, v149
	v_med3_f32 v1, v1, s37, v149
	v_mov_b32_e32 v4, v129
	v_cvt_pk_fp8_f32 v4, v0, v1
	v_mad_u64_u32 v[96:97], s[14:15], s6, v148, v[96:97]
	v_mul_f32_e32 v2, 0x43000000, v10
	v_mul_f32_e32 v0, 0x43000000, v14
	s_lshl_b64 s[14:15], s[6:7], 2
	v_med3_f32 v1, v2, s37, v149
	v_med3_f32 v0, v0, s37, v149
	v_lshl_add_u64 v[132:133], v[98:99], 0, v[128:129]
	v_lshl_add_u64 v[98:99], v[96:97], 0, s[14:15]
	v_cvt_pk_fp8_f32 v4, v1, v0 op_sel:[0,0,1]
	v_mul_f32_e32 v0, 0x43000000, v3
	v_mul_f32_e32 v1, 0x43000000, v7
	global_load_dwordx4 v[116:119], v[96:97], off
	global_load_dwordx4 v[120:123], v[98:99], off
	v_lshl_add_u64 v[96:97], v[98:99], 0, s[14:15]
	v_med3_f32 v0, v0, s37, v149
	v_med3_f32 v1, v1, s37, v149
	v_mov_b32_e32 v3, v129
	v_lshl_add_u64 v[98:99], v[96:97], 0, s[14:15]
	v_cvt_pk_fp8_f32 v3, v0, v1
	global_load_dwordx4 v[124:127], v[96:97], off
	global_load_dwordx4 v[112:115], v[98:99], off
	v_mad_u64_u32 v[96:97], s[48:49], s6, 52, v[98:99]
	v_lshl_add_u64 v[98:99], v[96:97], 0, s[14:15]
	v_mul_f32_e32 v2, 0x43000000, v11
	v_mul_f32_e32 v0, 0x43000000, v15
	global_load_dwordx4 v[100:103], v[96:97], off
	global_load_dwordx4 v[104:107], v[98:99], off
	v_lshl_add_u64 v[96:97], v[98:99], 0, s[14:15]
	v_med3_f32 v1, v2, s37, v149
	v_med3_f32 v0, v0, s37, v149
	v_lshl_add_u64 v[98:99], v[96:97], 0, s[14:15]
	v_cvt_pk_fp8_f32 v3, v1, v0 op_sel:[0,0,1]
	s_waitcnt vmcnt(21)
	v_mul_f32_e32 v40, 0x43000000, v40
	s_waitcnt vmcnt(20)
	v_mul_f32_e32 v48, 0x43000000, v48
	global_load_dwordx4 v[108:111], v[96:97], off
	s_nop 0
	global_load_dwordx4 v[96:99], v[98:99], off
	ds_write2_b32 v145, v150, v16 offset1:4
	ds_write2_b32 v145, v21, v5 offset0:33 offset1:37
	ds_write2_b32 v145, v20, v4 offset0:66 offset1:70
	ds_write2_b32 v145, v19, v3 offset0:99 offset1:103
	v_med3_f32 v40, v40, s37, v149
	v_med3_f32 v48, v48, s37, v149
	v_mov_b32_e32 v150, v129
	v_cvt_pk_fp8_f32 v150, v40, v48
	s_waitcnt vmcnt(21)
	v_mul_f32_e32 v60, 0x43000000, v60
	s_waitcnt vmcnt(20)
	v_mul_f32_e32 v40, 0x43000000, v56
	v_med3_f32 v48, v60, s37, v149
	v_med3_f32 v40, v40, s37, v149
	v_cvt_pk_fp8_f32 v150, v48, v40 op_sel:[0,0,1]
	v_mul_f32_e32 v40, 0x43000000, v41
	v_mul_f32_e32 v41, 0x43000000, v49
	v_med3_f32 v40, v40, s37, v149
	v_med3_f32 v41, v41, s37, v149
	v_mov_b32_e32 v49, v129
	v_cvt_pk_fp8_f32 v49, v40, v41
	v_mul_f32_e32 v48, 0x43000000, v61
	v_mul_f32_e32 v40, 0x43000000, v57
	v_med3_f32 v41, v48, s37, v149
	v_med3_f32 v40, v40, s37, v149
	v_cvt_pk_fp8_f32 v49, v41, v40 op_sel:[0,0,1]
	v_mul_f32_e32 v40, 0x43000000, v42
	v_mul_f32_e32 v41, 0x43000000, v50
	v_med3_f32 v40, v40, s37, v149
	v_med3_f32 v41, v41, s37, v149
	v_mov_b32_e32 v48, v129
	v_cvt_pk_fp8_f32 v48, v40, v41
	v_mul_f32_e32 v42, 0x43000000, v62
	v_mul_f32_e32 v40, 0x43000000, v58
	v_med3_f32 v41, v42, s37, v149
	v_med3_f32 v40, v40, s37, v149
	v_cvt_pk_fp8_f32 v48, v41, v40 op_sel:[0,0,1]
	v_mul_f32_e32 v40, 0x43000000, v43
	v_mul_f32_e32 v41, 0x43000000, v51
	v_med3_f32 v40, v40, s37, v149
	v_med3_f32 v41, v41, s37, v149
	v_mov_b32_e32 v43, v129
	v_cvt_pk_fp8_f32 v43, v40, v41
	v_mul_f32_e32 v42, 0x43000000, v63
	v_mul_f32_e32 v40, 0x43000000, v59
	v_med3_f32 v41, v42, s37, v149
	v_med3_f32 v40, v40, s37, v149
	s_waitcnt vmcnt(19)
	v_mul_f32_e32 v32, 0x43000000, v32
	s_waitcnt vmcnt(18)
; #define CV_LOAD(qi, Q, D) do { _Pragma("unroll") for (int s_ = 0; s_ < 2; ++s_) _Pragma("unroll") for (int r_ = 0; r_ < 4; ++r_) Q.v[s_][r_] = *(const f32x4*)(D.src + (size_t)(16 * (2 * (qi) + s_) + r_) * D.N); asm volatile("" ::: "memory"); } while (0)
; #define CV_PROC(qi, Q) do { _Pragma("unroll") for (int s_ = 0; s_ < 2; ++s_) _Pragma("unroll") for (int c_ = 0; c_ < 4; ++c_) \
;         *(LAS unsigned*)(scr + (4 * nl + c_) * 132 + 16 * (2 * (qi) + s_) + 4 * kg) = pg8::pk4_fp8c(Q.v[s_][0][c_] * FP8_WSC, Q.v[s_][1][c_] * FP8_WSC, Q.v[s_][2][c_] * FP8_WSC, Q.v[s_][3][c_] * FP8_WSC); asm volatile("" ::: "memory"); } while (0)
; __device__ __forceinline__ void moe_conv_stream(const Args& a, ARGAS unsigned char* ws, LAS unsigned char* scr, int first, int cnt, int lane) {
;     ...
;     Qt A, B, C, D4;
;     ConvItem cur = moe_conv_desc(a, ws, first, lane);
;     CV_LOAD(0, A, cur); CV_LOAD(1, B, cur); CV_LOAD(2, C, cur);
; #pragma unroll 1
;     for (int i = 0; i < cnt; ++i) {
;         const ConvItem nxt = moe_conv_desc(a, ws, first + 8 * ((i + 1 < cnt) ? i + 1 : i), lane);
;         CV_LOAD(3, D4, cur); CV_PROC(0, A);
;         CV_LOAD(0, A, nxt);  CV_PROC(1, B);
;         CV_LOAD(1, B, nxt);  CV_PROC(2, C);
;         CV_LOAD(2, C, nxt);  CV_PROC(3, D4);
	v_mul_f32_e32 v36, 0x43000000, v36
	v_cvt_pk_fp8_f32 v43, v41, v40 op_sel:[0,0,1]
	v_med3_f32 v32, v32, s37, v149
	v_med3_f32 v36, v36, s37, v149
	v_mov_b32_e32 v41, v129
	v_cvt_pk_fp8_f32 v41, v32, v36
	s_waitcnt vmcnt(17)
	v_mul_f32_e32 v40, 0x43000000, v52
	s_waitcnt vmcnt(16)
	v_mul_f32_e32 v32, 0x43000000, v44
	v_med3_f32 v36, v40, s37, v149
	v_med3_f32 v32, v32, s37, v149
	v_cvt_pk_fp8_f32 v41, v36, v32 op_sel:[0,0,1]
	v_mul_f32_e32 v32, 0x43000000, v33
	v_mul_f32_e32 v33, 0x43000000, v37
	v_med3_f32 v32, v32, s37, v149
	v_med3_f32 v33, v33, s37, v149
	v_mov_b32_e32 v37, v129
	v_cvt_pk_fp8_f32 v37, v32, v33
	v_mul_f32_e32 v36, 0x43000000, v53
	v_mul_f32_e32 v32, 0x43000000, v45
	v_med3_f32 v33, v36, s37, v149
	v_med3_f32 v32, v32, s37, v149
	v_cvt_pk_fp8_f32 v37, v33, v32 op_sel:[0,0,1]
	v_mul_f32_e32 v32, 0x43000000, v34
	v_mul_f32_e32 v33, 0x43000000, v38
	v_med3_f32 v32, v32, s37, v149
	v_med3_f32 v33, v33, s37, v149
	v_mov_b32_e32 v36, v129
	v_cvt_pk_fp8_f32 v36, v32, v33
	v_mul_f32_e32 v34, 0x43000000, v54
	v_mul_f32_e32 v32, 0x43000000, v46
	s_lshl_b32 s6, s13, 2
	v_med3_f32 v33, v34, s37, v149
	v_med3_f32 v32, v32, s37, v149
	v_lshl_add_u64 v[0:1], v[132:133], 0, s[6:7]
	s_lshl_b32 s6, s13, 3
	v_cvt_pk_fp8_f32 v36, v33, v32 op_sel:[0,0,1]
	v_mul_f32_e32 v32, 0x43000000, v35
	v_mul_f32_e32 v33, 0x43000000, v39
	global_load_dwordx4 v[28:31], v[132:133], off
	global_load_dwordx4 v[16:19], v[0:1], off
	v_lshl_add_u64 v[0:1], v[132:133], 0, s[6:7]
	s_mul_i32 s6, s13, 12
	v_med3_f32 v32, v32, s37, v149
	v_med3_f32 v33, v33, s37, v149
	v_mov_b32_e32 v35, v129
	v_lshl_add_u64 v[2:3], v[132:133], 0, s[6:7]
	s_lshl_b32 s6, s13, 6
	v_cvt_pk_fp8_f32 v35, v32, v33
	global_load_dwordx4 v[20:23], v[0:1], off
	global_load_dwordx4 v[24:27], v[2:3], off
	v_lshl_add_u64 v[0:1], v[132:133], 0, s[6:7]
	s_mul_i32 s6, s13, 0x44
	v_lshl_add_u64 v[4:5], v[132:133], 0, s[6:7]
	s_mul_i32 s6, s13, 0x48
	v_mul_f32_e32 v34, 0x43000000, v55
	v_mul_f32_e32 v32, 0x43000000, v47
	v_lshl_add_u64 v[8:9], v[132:133], 0, s[6:7]
	s_mul_i32 s6, s13, 0x4c
	v_med3_f32 v33, v34, s37, v149
	v_med3_f32 v32, v32, s37, v149
	v_lshl_add_u64 v[12:13], v[132:133], 0, s[6:7]
	v_cvt_pk_fp8_f32 v35, v33, v32 op_sel:[0,0,1]
	s_waitcnt vmcnt(19)
	v_mul_f32_e32 v72, 0x43000000, v72
	s_waitcnt vmcnt(18)
	v_mul_f32_e32 v80, 0x43000000, v80
	global_load_dwordx4 v[0:3], v[0:1], off
	s_nop 0
	global_load_dwordx4 v[4:7], v[4:5], off
	s_nop 0
	global_load_dwordx4 v[8:11], v[8:9], off
	s_nop 0
	global_load_dwordx4 v[12:15], v[12:13], off
	ds_write2_b32 v146, v150, v41 offset0:8 offset1:12
	ds_write2_b32 v146, v49, v37 offset0:41 offset1:45
	ds_write2_b32 v146, v48, v36 offset0:74 offset1:78
	ds_write2_b32 v146, v43, v35 offset0:107 offset1:111
	v_med3_f32 v72, v72, s37, v149
	v_med3_f32 v80, v80, s37, v149
	v_mov_b32_e32 v150, v129
	v_cvt_pk_fp8_f32 v150, v72, v80
	s_waitcnt vmcnt(21)
	v_mul_f32_e32 v92, 0x43000000, v92
	s_waitcnt vmcnt(20)
	v_mul_f32_e32 v72, 0x43000000, v88
	v_med3_f32 v80, v92, s37, v149
	v_med3_f32 v72, v72, s37, v149
	v_cvt_pk_fp8_f32 v150, v80, v72 op_sel:[0,0,1]
	v_mul_f32_e32 v72, 0x43000000, v73
	v_mul_f32_e32 v73, 0x43000000, v81
	v_med3_f32 v72, v72, s37, v149
	v_med3_f32 v73, v73, s37, v149
	v_mov_b32_e32 v81, v129
	v_cvt_pk_fp8_f32 v81, v72, v73
	v_mul_f32_e32 v80, 0x43000000, v93
	v_mul_f32_e32 v72, 0x43000000, v89
	v_med3_f32 v73, v80, s37, v149
	v_med3_f32 v72, v72, s37, v149
	v_cvt_pk_fp8_f32 v81, v73, v72 op_sel:[0,0,1]
	v_mul_f32_e32 v72, 0x43000000, v74
	v_mul_f32_e32 v73, 0x43000000, v82
	v_med3_f32 v72, v72, s37, v149
	v_med3_f32 v73, v73, s37, v149
	v_mov_b32_e32 v80, v129
	v_cvt_pk_fp8_f32 v80, v72, v73
	v_mul_f32_e32 v74, 0x43000000, v94
	v_mul_f32_e32 v72, 0x43000000, v90
	v_med3_f32 v73, v74, s37, v149
	v_med3_f32 v72, v72, s37, v149
	v_cvt_pk_fp8_f32 v80, v73, v72 op_sel:[0,0,1]
	v_mul_f32_e32 v72, 0x43000000, v75
	v_mul_f32_e32 v73, 0x43000000, v83
	v_med3_f32 v72, v72, s37, v149
	v_med3_f32 v73, v73, s37, v149
	v_mov_b32_e32 v75, v129
	v_cvt_pk_fp8_f32 v75, v72, v73
	v_mul_f32_e32 v74, 0x43000000, v95
	v_mul_f32_e32 v72, 0x43000000, v91
	v_med3_f32 v73, v74, s37, v149
	v_med3_f32 v72, v72, s37, v149
	s_waitcnt vmcnt(19)
	v_mul_f32_e32 v64, 0x43000000, v64
	s_waitcnt vmcnt(18)
	v_mul_f32_e32 v68, 0x43000000, v68
	v_cvt_pk_fp8_f32 v75, v73, v72 op_sel:[0,0,1]
	v_med3_f32 v64, v64, s37, v149
	v_med3_f32 v68, v68, s37, v149
	v_mov_b32_e32 v73, v129
	v_cvt_pk_fp8_f32 v73, v64, v68
	s_waitcnt vmcnt(17)
	v_mul_f32_e32 v72, 0x43000000, v84
	s_waitcnt vmcnt(16)
	v_mul_f32_e32 v64, 0x43000000, v76
	v_med3_f32 v68, v72, s37, v149
	v_med3_f32 v64, v64, s37, v149
	v_cvt_pk_fp8_f32 v73, v68, v64 op_sel:[0,0,1]
	v_mul_f32_e32 v64, 0x43000000, v65
	v_mul_f32_e32 v65, 0x43000000, v69
	v_med3_f32 v64, v64, s37, v149
	v_med3_f32 v65, v65, s37, v149
	v_mov_b32_e32 v69, v129
	v_cvt_pk_fp8_f32 v69, v64, v65
	v_mul_f32_e32 v68, 0x43000000, v85
	v_mul_f32_e32 v64, 0x43000000, v77
	v_med3_f32 v65, v68, s37, v149
	v_med3_f32 v64, v64, s37, v149
	v_cvt_pk_fp8_f32 v69, v65, v64 op_sel:[0,0,1]
	v_mul_f32_e32 v64, 0x43000000, v66
	v_mul_f32_e32 v65, 0x43000000, v70
	v_med3_f32 v64, v64, s37, v149
	v_med3_f32 v65, v65, s37, v149
	v_mov_b32_e32 v68, v129
	v_cvt_pk_fp8_f32 v68, v64, v65
	s_lshl_b32 s6, s13, 7
	v_mul_f32_e32 v66, 0x43000000, v86
	v_mul_f32_e32 v64, 0x43000000, v78
	v_lshl_add_u64 v[32:33], v[132:133], 0, s[6:7]
	s_mul_i32 s6, s13, 0x84
	v_med3_f32 v65, v66, s37, v149
	v_med3_f32 v64, v64, s37, v149
	v_lshl_add_u64 v[34:35], v[132:133], 0, s[6:7]
	s_mul_i32 s6, s13, 0x88
	v_cvt_pk_fp8_f32 v68, v65, v64 op_sel:[0,0,1]
	v_mul_f32_e32 v64, 0x43000000, v67
	v_mul_f32_e32 v65, 0x43000000, v71
	global_load_dwordx4 v[40:43], v[32:33], off
	global_load_dwordx4 v[48:51], v[34:35], off
	v_lshl_add_u64 v[32:33], v[132:133], 0, s[6:7]
	s_mul_i32 s6, s13, 0x8c
	v_med3_f32 v64, v64, s37, v149
	v_med3_f32 v65, v65, s37, v149
	v_mov_b32_e32 v67, v129
	v_lshl_add_u64 v[34:35], v[132:133], 0, s[6:7]
	s_mul_i32 s6, s13, 0xc0
	v_cvt_pk_fp8_f32 v67, v64, v65
	global_load_dwordx4 v[60:63], v[32:33], off
	global_load_dwordx4 v[56:59], v[34:35], off
	v_lshl_add_u64 v[32:33], v[132:133], 0, s[6:7]
	s_mul_i32 s6, s13, 0xc4
	v_lshl_add_u64 v[36:37], v[132:133], 0, s[6:7]
	s_mul_i32 s6, s13, 0xc8
	v_mul_f32_e32 v66, 0x43000000, v87
	v_mul_f32_e32 v64, 0x43000000, v79
	v_lshl_add_u64 v[44:45], v[132:133], 0, s[6:7]
	s_mul_i32 s6, s13, 0xcc
	v_med3_f32 v65, v66, s37, v149
	v_med3_f32 v64, v64, s37, v149
	v_lshl_add_u64 v[46:47], v[132:133], 0, s[6:7]
	v_cvt_pk_fp8_f32 v67, v65, v64 op_sel:[0,0,1]
	s_waitcnt vmcnt(19)
; #define LAS __attribute__((address_space(3)))
; #define LDS_WAIT() asm volatile("s_waitcnt lgkmcnt(0)" ::: "memory")
; #define CV_LOAD(qi, Q, D) do { _Pragma("unroll") for (int s_ = 0; s_ < 2; ++s_) _Pragma("unroll") for (int r_ = 0; r_ < 4; ++r_) Q.v[s_][r_] = *(const f32x4*)(D.src + (size_t)(16 * (2 * (qi) + s_) + r_) * D.N); asm volatile("" ::: "memory"); } while (0)
; #define CV_PROC(qi, Q) do { _Pragma("unroll") for (int s_ = 0; s_ < 2; ++s_) _Pragma("unroll") for (int c_ = 0; c_ < 4; ++c_) \
;         *(LAS unsigned*)(scr + (4 * nl + c_) * 132 + 16 * (2 * (qi) + s_) + 4 * kg) = pg8::pk4_fp8c(Q.v[s_][0][c_] * FP8_WSC, Q.v[s_][1][c_] * FP8_WSC, Q.v[s_][2][c_] * FP8_WSC, Q.v[s_][3][c_] * FP8_WSC); asm volatile("" ::: "memory"); } while (0)
; __device__ __forceinline__ void moe_conv_stream(const Args& a, ARGAS unsigned char* ws, LAS unsigned char* scr, int first, int cnt, int lane) {
;     ...
;     Qt A, B, C, D4;
;     ConvItem cur = moe_conv_desc(a, ws, first, lane);
;     CV_LOAD(0, A, cur); CV_LOAD(1, B, cur); CV_LOAD(2, C, cur);
; #pragma unroll 1
;     for (int i = 0; i < cnt; ++i) {
;         const ConvItem nxt = moe_conv_desc(a, ws, first + 8 * ((i + 1 < cnt) ? i + 1 : i), lane);
;         CV_LOAD(3, D4, cur); CV_PROC(0, A);
;         CV_LOAD(0, A, nxt);  CV_PROC(1, B);
;         CV_LOAD(1, B, nxt);  CV_PROC(2, C);
;         CV_LOAD(2, C, nxt);  CV_PROC(3, D4);
;         LDS_WAIT(); asm volatile("" ::: "memory");
;         const int n0 = cur.gu > 0 ? cur.gu - 1 : -cur.gu - 1;
; #pragma unroll
;         for (int j = 0; j < 8; ++j) { const int row = (lane >> 3) + 8 * j; const LAS unsigned* s = (const LAS unsigned*)(scr + row * 132 + 16 * c8);
;             u32x4 o; o.x = s[0]; o.y = s[1]; o.z = s[2]; o.w = s[3];
;             const int n = n0 + row, wr_ = cur.gu > 0 ? RmGu()(n) : n;
;             *(u32x4*)(cur.dst + (size_t)wr_ * cur.ldk + 16 * c8) = o; }
	v_mul_f32_e32 v116, 0x43000000, v116
	s_waitcnt vmcnt(18)
	v_mul_f32_e32 v120, 0x43000000, v120
	global_load_dwordx4 v[32:35], v[32:33], off
	s_nop 0
	global_load_dwordx4 v[36:39], v[36:37], off
	s_nop 0
	global_load_dwordx4 v[52:55], v[44:45], off
	s_nop 0
	global_load_dwordx4 v[44:47], v[46:47], off
	ds_write2_b32 v146, v150, v73 offset0:16 offset1:20
	ds_write2_b32 v146, v81, v69 offset0:49 offset1:53
	ds_write2_b32 v146, v80, v68 offset0:82 offset1:86
	ds_write2_b32 v146, v75, v67 offset0:115 offset1:119
	v_med3_f32 v116, v116, s37, v149
	v_med3_f32 v120, v120, s37, v149
	v_mov_b32_e32 v150, v129
	v_cvt_pk_fp8_f32 v150, v116, v120
	s_waitcnt vmcnt(21)
	v_mul_f32_e32 v124, 0x43000000, v124
	s_waitcnt vmcnt(20)
	v_mul_f32_e32 v112, 0x43000000, v112
	v_med3_f32 v116, v124, s37, v149
	v_med3_f32 v112, v112, s37, v149
	v_cvt_pk_fp8_f32 v150, v116, v112 op_sel:[0,0,1]
	v_mul_f32_e32 v112, 0x43000000, v117
	v_mul_f32_e32 v116, 0x43000000, v121
	v_med3_f32 v112, v112, s37, v149
	v_med3_f32 v116, v116, s37, v149
	v_mov_b32_e32 v120, v129
	v_cvt_pk_fp8_f32 v120, v112, v116
	v_mul_f32_e32 v117, 0x43000000, v125
	v_mul_f32_e32 v112, 0x43000000, v113
	v_med3_f32 v113, v117, s37, v149
	v_med3_f32 v112, v112, s37, v149
	v_cvt_pk_fp8_f32 v120, v113, v112 op_sel:[0,0,1]
	v_mul_f32_e32 v112, 0x43000000, v118
	v_mul_f32_e32 v113, 0x43000000, v122
	v_med3_f32 v112, v112, s37, v149
	v_med3_f32 v113, v113, s37, v149
	v_mov_b32_e32 v117, v129
	v_cvt_pk_fp8_f32 v117, v112, v113
	v_mul_f32_e32 v116, 0x43000000, v126
	v_mul_f32_e32 v112, 0x43000000, v114
	v_med3_f32 v113, v116, s37, v149
	v_med3_f32 v112, v112, s37, v149
	v_cvt_pk_fp8_f32 v117, v113, v112 op_sel:[0,0,1]
	v_mul_f32_e32 v112, 0x43000000, v119
	v_mul_f32_e32 v113, 0x43000000, v123
	v_med3_f32 v112, v112, s37, v149
	v_med3_f32 v113, v113, s37, v149
	v_mov_b32_e32 v116, v129
	v_cvt_pk_fp8_f32 v116, v112, v113
	v_mul_f32_e32 v114, 0x43000000, v127
	v_mul_f32_e32 v112, 0x43000000, v115
	v_med3_f32 v113, v114, s37, v149
	v_med3_f32 v112, v112, s37, v149
	s_waitcnt vmcnt(19)
	v_mul_f32_e32 v100, 0x43000000, v100
	s_waitcnt vmcnt(18)
	v_mul_f32_e32 v104, 0x43000000, v104
	v_cvt_pk_fp8_f32 v116, v113, v112 op_sel:[0,0,1]
	v_med3_f32 v100, v100, s37, v149
	v_med3_f32 v104, v104, s37, v149
	v_mov_b32_e32 v112, v129
	v_cvt_pk_fp8_f32 v112, v100, v104
	s_waitcnt vmcnt(17)
	v_mul_f32_e32 v108, 0x43000000, v108
	s_waitcnt vmcnt(16)
	v_mul_f32_e32 v96, 0x43000000, v96
	v_med3_f32 v100, v108, s37, v149
	v_med3_f32 v96, v96, s37, v149
	v_cvt_pk_fp8_f32 v112, v100, v96 op_sel:[0,0,1]
	v_mul_f32_e32 v96, 0x43000000, v101
	v_mul_f32_e32 v100, 0x43000000, v105
	v_med3_f32 v96, v96, s37, v149
	v_med3_f32 v100, v100, s37, v149
	v_mov_b32_e32 v104, v129
	v_cvt_pk_fp8_f32 v104, v96, v100
	v_mul_f32_e32 v101, 0x43000000, v109
	v_mul_f32_e32 v96, 0x43000000, v97
	v_med3_f32 v97, v101, s37, v149
	v_med3_f32 v96, v96, s37, v149
	s_lshl_b32 s6, s13, 8
	v_cvt_pk_fp8_f32 v104, v97, v96 op_sel:[0,0,1]
	v_mul_f32_e32 v96, 0x43000000, v102
	v_mul_f32_e32 v97, 0x43000000, v106
	v_lshl_add_u64 v[64:65], v[132:133], 0, s[6:7]
	s_mul_i32 s6, s13, 0x104
	v_med3_f32 v96, v96, s37, v149
	v_med3_f32 v97, v97, s37, v149
	v_mov_b32_e32 v101, v129
	v_lshl_add_u64 v[66:67], v[132:133], 0, s[6:7]
	s_mul_i32 s6, s13, 0x108
	v_cvt_pk_fp8_f32 v101, v96, v97
	global_load_dwordx4 v[72:75], v[64:65], off
	global_load_dwordx4 v[80:83], v[66:67], off
	v_lshl_add_u64 v[64:65], v[132:133], 0, s[6:7]
	s_mul_i32 s6, s13, 0x10c
	v_lshl_add_u64 v[66:67], v[132:133], 0, s[6:7]
	s_mul_i32 s6, s13, 0x140
	v_mul_f32_e32 v100, 0x43000000, v110
	v_mul_f32_e32 v96, 0x43000000, v98
	global_load_dwordx4 v[92:95], v[64:65], off
	global_load_dwordx4 v[88:91], v[66:67], off
	v_lshl_add_u64 v[64:65], v[132:133], 0, s[6:7]
	s_mul_i32 s6, s13, 0x144
	v_med3_f32 v97, v100, s37, v149
	v_med3_f32 v96, v96, s37, v149
	v_lshl_add_u64 v[68:69], v[132:133], 0, s[6:7]
	s_mul_i32 s6, s13, 0x148
	v_cvt_pk_fp8_f32 v101, v97, v96 op_sel:[0,0,1]
	v_mul_f32_e32 v96, 0x43000000, v103
	v_mul_f32_e32 v97, 0x43000000, v107
	v_lshl_add_u64 v[76:77], v[132:133], 0, s[6:7]
	s_mul_i32 s6, s13, 0x14c
	v_med3_f32 v96, v96, s37, v149
	v_med3_f32 v97, v97, s37, v149
	v_mov_b32_e32 v100, v129
	v_lshl_add_u64 v[78:79], v[132:133], 0, s[6:7]
	v_cvt_pk_fp8_f32 v100, v96, v97
	s_add_i32 s6, s40, -1
	s_not_b32 s12, s40
	s_cmp_gt_i32 s40, 0
	global_load_dwordx4 v[64:67], v[64:65], off
	s_nop 0
	global_load_dwordx4 v[68:71], v[68:69], off
	s_nop 0
	global_load_dwordx4 v[84:87], v[76:77], off
	s_nop 0
	global_load_dwordx4 v[76:79], v[78:79], off
	v_mul_f32_e32 v98, 0x43000000, v111
	v_mul_f32_e32 v96, 0x43000000, v99
	s_cselect_b64 vcc, -1, 0
	v_med3_f32 v97, v98, s37, v149
	v_med3_f32 v96, v96, s37, v149
	s_and_b64 s[14:15], vcc, exec
	v_cvt_pk_fp8_f32 v100, v97, v96 op_sel:[0,0,1]
	s_cselect_b32 s6, s6, s12
	ds_write2_b32 v146, v150, v112 offset0:24 offset1:28
	ds_write2_b32 v146, v120, v104 offset0:57 offset1:61
	ds_write2_b32 v146, v117, v101 offset0:90 offset1:94
	ds_write2_b32 v146, v116, v100 offset0:123 offset1:127
	v_add_u32_e32 v100, s6, v194
	v_lshlrev_b32_e32 v101, 1, v100
	v_ashrrev_i32_e32 v102, 3, v100
	s_waitcnt lgkmcnt(0)
	v_and_b32_e32 v101, 0x700, v101
	v_and_b32_e32 v102, 0xffffff80, v102
	v_add_u32_e32 v101, v101, v102
	ds_read2_b32 v[96:97], v147 offset1:1
	ds_read2_b32 v[98:99], v147 offset0:2 offset1:3
	v_and_or_b32 v101, v100, s38, v101
	v_cndmask_b32_e32 v100, v100, v101, vcc
	v_ashrrev_i32_e32 v101, 31, v100
	v_lshl_add_u64 v[104:105], s[8:9], 0, v[130:131]
	v_lshlrev_b64 v[100:101], 10, v[100:101]
	v_lshl_add_u64 v[106:107], v[104:105], 0, v[100:101]
	v_add_u32_e32 v100, 0x420, v147
	v_add_u32_e32 v102, 0x428, v147
	ds_read2_b32 v[100:101], v100 offset1:1
	ds_read2_b32 v[102:103], v102 offset1:1
	s_waitcnt lgkmcnt(2)
; #define LAS __attribute__((address_space(3)))
; #define LDS_WAIT() asm volatile("s_waitcnt lgkmcnt(0)" ::: "memory")
; __device__ __forceinline__ ConvItem moe_conv_desc(const Args& a, ARGAS unsigned char* ws, int it, int lane) {
;     const int m = it / MOE_CONV_PER_M, r = it % MOE_CONV_PER_M, nl = lane & 15, kg = lane >> 4; ConvItem d;
;     if (r < 256) { const int kb = r / 32, nb = r % 32; d.N = 2048; d.ldk = DM; d.gu = 64 * nb + 1; d.src = a.moe_w_gu + (size_t)m * DM * 2048 + (size_t)(128 * kb + 4 * kg) * 2048 + 64 * nb + 4 * nl; d.dst = (unsigned char*)(ws + WS_WGU) + (size_t)m * 2048 * DM + 128 * kb; }
;     else { const int r2 = r - 256, kb = r2 / 16, nb = r2 % 16; d.N = DM; d.ldk = EFF; d.gu = -(64 * nb) - 1; d.src = a.moe_w_down + (size_t)m * EFF * DM + (size_t)(128 * kb + 4 * kg) * DM + 64 * nb + 4 * nl; d.dst = (unsigned char*)(ws + WS_WDN) + (size_t)m * DM * EFF + 128 * kb; }
; __device__ __forceinline__ void moe_conv_stream(const Args& a, ARGAS unsigned char* ws, LAS unsigned char* scr, int first, int cnt, int lane) {
;     ...
;         const int n0 = cur.gu > 0 ? cur.gu - 1 : -cur.gu - 1;
; #pragma unroll
;         for (int j = 0; j < 8; ++j) { const int row = (lane >> 3) + 8 * j; const LAS unsigned* s = (const LAS unsigned*)(scr + row * 132 + 16 * c8);
;             u32x4 o; o.x = s[0]; o.y = s[1]; o.z = s[2]; o.w = s[3];
;             const int n = n0 + row, wr_ = cur.gu > 0 ? RmGu()(n) : n;
;             *(u32x4*)(cur.dst + (size_t)wr_ * cur.ldk + 16 * c8) = o; }
;         LDS_WAIT(); asm volatile("" ::: "memory");
;         cur = nxt;
	global_store_dwordx4 v[106:107], v[96:99], off
	s_add_i32 s41, s41, 8
	s_cmpk_eq_i32 s41, 0x28
	v_add_u32_e32 v96, s6, v137
	v_lshlrev_b32_e32 v97, 1, v96
	v_ashrrev_i32_e32 v98, 3, v96
	v_and_b32_e32 v97, 0x700, v97
	v_and_b32_e32 v98, 0xffffff80, v98
	v_add_u32_e32 v97, v97, v98
	v_and_or_b32 v97, v96, s38, v97
	v_cndmask_b32_e32 v96, v96, v97, vcc
	v_ashrrev_i32_e32 v97, 31, v96
	v_lshlrev_b64 v[96:97], 10, v[96:97]
	v_lshl_add_u64 v[96:97], v[104:105], 0, v[96:97]
	s_waitcnt lgkmcnt(0)
	global_store_dwordx4 v[96:97], v[100:103], off
	v_add_u32_e32 v96, 0x840, v147
	v_add_u32_e32 v98, 0x848, v147
	v_add_u32_e32 v100, s6, v138
	v_lshlrev_b32_e32 v101, 1, v100
	v_ashrrev_i32_e32 v102, 3, v100
	v_and_b32_e32 v101, 0x700, v101
	v_and_b32_e32 v102, 0xffffff80, v102
	v_add_u32_e32 v101, v101, v102
	ds_read2_b32 v[96:97], v96 offset1:1
	ds_read2_b32 v[98:99], v98 offset1:1
	v_and_or_b32 v101, v100, s38, v101
	v_cndmask_b32_e32 v100, v100, v101, vcc
	v_ashrrev_i32_e32 v101, 31, v100
	v_lshlrev_b64 v[100:101], 10, v[100:101]
	v_lshl_add_u64 v[106:107], v[104:105], 0, v[100:101]
	v_add_u32_e32 v100, 0xc60, v147
	v_add_u32_e32 v102, 0xc68, v147
	ds_read2_b32 v[100:101], v100 offset1:1
	ds_read2_b32 v[102:103], v102 offset1:1
	s_waitcnt lgkmcnt(2)
	global_store_dwordx4 v[106:107], v[96:99], off
	s_mov_b32 s40, s42
	s_mov_b64 s[8:9], s[10:11]
	v_add_u32_e32 v96, s6, v139
	v_lshlrev_b32_e32 v97, 1, v96
	v_ashrrev_i32_e32 v98, 3, v96
	v_and_b32_e32 v97, 0x700, v97
	v_and_b32_e32 v98, 0xffffff80, v98
	v_add_u32_e32 v97, v97, v98
	v_and_or_b32 v97, v96, s38, v97
	v_cndmask_b32_e32 v96, v96, v97, vcc
	v_ashrrev_i32_e32 v97, 31, v96
	v_lshlrev_b64 v[96:97], 10, v[96:97]
	v_lshl_add_u64 v[96:97], v[104:105], 0, v[96:97]
	s_waitcnt lgkmcnt(0)
	global_store_dwordx4 v[96:97], v[100:103], off
	v_add_u32_e32 v96, 0x1080, v147
	v_add_u32_e32 v98, 0x1088, v147
	v_add_u32_e32 v100, s6, v140
	v_lshlrev_b32_e32 v101, 1, v100
	v_ashrrev_i32_e32 v102, 3, v100
	v_and_b32_e32 v101, 0x700, v101
	v_and_b32_e32 v102, 0xffffff80, v102
	v_add_u32_e32 v101, v101, v102
	ds_read2_b32 v[96:97], v96 offset1:1
	ds_read2_b32 v[98:99], v98 offset1:1
	v_and_or_b32 v101, v100, s38, v101
	v_cndmask_b32_e32 v100, v100, v101, vcc
	v_ashrrev_i32_e32 v101, 31, v100
	v_lshlrev_b64 v[100:101], 10, v[100:101]
	v_lshl_add_u64 v[106:107], v[104:105], 0, v[100:101]
	v_add_u32_e32 v100, 0x14a0, v147
	v_add_u32_e32 v102, 0x14a8, v147
	ds_read2_b32 v[100:101], v100 offset1:1
	ds_read2_b32 v[102:103], v102 offset1:1
	s_waitcnt lgkmcnt(2)
	global_store_dwordx4 v[106:107], v[96:99], off
	s_nop 1
	v_add_u32_e32 v96, s6, v141
	v_lshlrev_b32_e32 v97, 1, v96
	v_ashrrev_i32_e32 v98, 3, v96
	v_and_b32_e32 v97, 0x700, v97
	v_and_b32_e32 v98, 0xffffff80, v98
	v_add_u32_e32 v97, v97, v98
	v_and_or_b32 v97, v96, s38, v97
	v_cndmask_b32_e32 v96, v96, v97, vcc
	v_ashrrev_i32_e32 v97, 31, v96
	v_lshlrev_b64 v[96:97], 10, v[96:97]
	v_lshl_add_u64 v[96:97], v[104:105], 0, v[96:97]
	s_waitcnt lgkmcnt(0)
	global_store_dwordx4 v[96:97], v[100:103], off
	v_add_u32_e32 v96, 0x18c0, v147
	v_add_u32_e32 v98, 0x18c8, v147
	v_add_u32_e32 v100, s6, v142
	v_lshlrev_b32_e32 v101, 1, v100
	v_ashrrev_i32_e32 v102, 3, v100
	v_and_b32_e32 v101, 0x700, v101
	v_and_b32_e32 v102, 0xffffff80, v102
	v_add_u32_e32 v101, v101, v102
	ds_read2_b32 v[96:97], v96 offset1:1
	ds_read2_b32 v[98:99], v98 offset1:1
	v_and_or_b32 v101, v100, s38, v101
	v_cndmask_b32_e32 v100, v100, v101, vcc
	v_ashrrev_i32_e32 v101, 31, v100
	v_lshlrev_b64 v[100:101], 10, v[100:101]
	v_lshl_add_u64 v[106:107], v[104:105], 0, v[100:101]
	v_add_u32_e32 v100, 0x1ce0, v147
	v_add_u32_e32 v102, 0x1ce8, v147
	ds_read2_b32 v[100:101], v100 offset1:1
	ds_read2_b32 v[102:103], v102 offset1:1
	s_waitcnt lgkmcnt(2)
	global_store_dwordx4 v[106:107], v[96:99], off
	s_nop 1
	v_add_u32_e32 v96, s6, v143
	v_lshlrev_b32_e32 v97, 1, v96
	v_ashrrev_i32_e32 v98, 3, v96
	v_and_b32_e32 v97, 0x700, v97
	v_and_b32_e32 v98, 0xffffff80, v98
	v_add_u32_e32 v97, v97, v98
	v_and_or_b32 v97, v96, s38, v97
	v_cndmask_b32_e32 v96, v96, v97, vcc
	v_ashrrev_i32_e32 v97, 31, v96
	v_lshlrev_b64 v[96:97], 10, v[96:97]
	v_lshl_add_u64 v[96:97], v[104:105], 0, v[96:97]
	s_waitcnt lgkmcnt(0)
	global_store_dwordx4 v[96:97], v[100:103], off
	s_waitcnt lgkmcnt(0)
	s_mov_b32 s6, s13
	v_mov_b64_e32 v[96:97], v[132:133]
	s_cbranch_scc1 .LBB0_3115
.LBB0_3128:
	s_cmpk_lg_i32 s41, 0x20
	s_cselect_b32 s10, s41, 0x18
	s_add_i32 s10, s10, s39
	s_mul_hi_i32 s11, s10, 0x2aaaaaab
	s_lshr_b32 s12, s11, 31
	s_ashr_i32 s11, s11, 6
	s_add_i32 s12, s11, s12
	s_mul_i32 s11, s12, 0x180
	s_sub_i32 s43, s10, s11
	s_cmpk_gt_i32 s43, 0xff
	s_cbranch_scc0 .LBB0_3130
	s_load_dwordx2 s[10:11], s[20:21], 0xe0
	s_lshl_b32 s13, s43, 6
	s_and_b32 s44, s13, 0x3c0
	s_ashr_i32 s13, s12, 31
	s_not_b32 s42, s44
	s_lshl_b64 s[14:15], s[12:13], 20
	s_lshl_b64 s[48:49], s[12:13], 22
	s_waitcnt lgkmcnt(0)
	s_add_u32 s10, s10, s48
	s_addc_u32 s11, s11, s49
	s_lshl_b32 s13, s43, 3
	s_and_b32 s13, s13, 0x7fffff80
	s_addk_i32 s13, 0xf800
	v_or_b32_e32 v98, s13, v136
	v_mov_b32_e32 v99, v129
	v_lshlrev_b64 v[98:99], 12, v[98:99]
	v_lshl_add_u64 v[98:99], s[10:11], 0, v[98:99]
	s_lshl_b32 s10, s44, 2
	s_mov_b32 s11, s7
	v_lshl_add_u64 v[98:99], v[98:99], 0, s[10:11]
	s_add_u32 s10, s16, s14
	s_addc_u32 s11, s17, s15
	s_add_u32 s10, s10, s13
	s_addc_u32 s11, s11, 0
	s_movk_i32 s13, 0x400
	s_cbranch_execnz .LBB0_3127
	s_branch .LBB0_3131

; __device__ __forceinline__ unsigned xb_add(gbar_t p, unsigned v) { return __hip_atomic_fetch_add(p, v, __ATOMIC_RELAXED, __HIP_MEMORY_SCOPE_AGENT); }
; __device__ __forceinline__ ConvItem moe_conv_desc(const Args& a, ARGAS unsigned char* ws, int it, int lane) {
;     const int m = it / MOE_CONV_PER_M, r = it % MOE_CONV_PER_M, nl = lane & 15, kg = lane >> 4; ConvItem d;
;     if (r < 256) { const int kb = r / 32, nb = r % 32; d.N = 2048; d.ldk = DM; d.gu = 64 * nb + 1; d.src = a.moe_w_gu + (size_t)m * DM * 2048 + (size_t)(128 * kb + 4 * kg) * 2048 + 64 * nb + 4 * nl; d.dst = (unsigned char*)(ws + WS_WGU) + (size_t)m * 2048 * DM + 128 * kb; }
;     else { const int r2 = r - 256, kb = r2 / 16, nb = r2 % 16; d.N = DM; d.ldk = EFF; d.gu = -(64 * nb) - 1; d.src = a.moe_w_down + (size_t)m * EFF * DM + (size_t)(128 * kb + 4 * kg) * DM + 64 * nb + 4 * nl; d.dst = (unsigned char*)(ws + WS_WDN) + (size_t)m * DM * EFF + 128 * kb; }
; __device__ __forceinline__ void moe_conv_drain(const Frame& F, const Args& a, ARGAS unsigned char* ws, gbar_t head, LAS unsigned* qslot, const int first_chunk, const int nchunks) {
;     ...
;     for (;;) {
;         __syncthreads();
;         if (F.tid == 0) *qslot = xb_add(head, 1u);
;         __syncthreads();
;         const unsigned ch = *qslot;
;         if (ch >= (unsigned)nchunks) break;
;         moe_conv_stream(a, ws, scr, (first_chunk + (int)ch) * MOE_CONV_CHUNK + F.wave, MOE_CONV_CHUNK / 8, F.lane);
.LBB0_3201:
	s_or_b64 exec, exec, s[8:9]
	s_waitcnt lgkmcnt(0)
	s_barrier
	s_waitcnt vmcnt(27)
	ds_read_b32 v0, v142
	s_mov_b64 s[8:9], -1
	s_waitcnt lgkmcnt(0)
	s_movk_i32 s98, 0x2ff
	v_cmp_lt_u32_e32 vcc, s98, v0
	v_readfirstlane_b32 s6, v0
	s_cbranch_vccnz .LBB0_3196
	s_lshl_b32 s6, s6, 5
	s_add_i32 s37, s24, s6
	s_mul_hi_i32 s6, s37, 0x2aaaaaab
	s_lshr_b32 s8, s6, 31
	s_ashr_i32 s6, s6, 6
	s_add_i32 s10, s6, s8
	s_mul_i32 s6, s10, 0x180
	s_sub_i32 s14, s37, s6
	s_cmpk_gt_i32 s14, 0xff
	s_cbranch_scc0 .LBB0_3204
	s_load_dwordx2 s[8:9], s[20:21], 0xe0
	s_lshl_b32 s6, s14, 6
	s_and_b32 s6, s6, 0x3c0
	s_ashr_i32 s11, s10, 31
	s_not_b32 s38, s6
	s_lshl_b64 s[12:13], s[10:11], 20
	s_lshl_b64 s[40:41], s[10:11], 22
	s_waitcnt lgkmcnt(0)
	s_add_u32 s8, s8, s40
	s_addc_u32 s9, s9, s41
	s_lshl_b32 s11, s14, 3
	s_and_b32 s11, s11, 0x7fffff80
	s_addk_i32 s11, 0xf800
	v_or_b32_e32 v0, s11, v134
	v_mov_b32_e32 v1, v129
	v_lshlrev_b64 v[0:1], 12, v[0:1]
	v_lshl_add_u64 v[0:1], s[8:9], 0, v[0:1]
	s_lshl_b32 s6, s6, 2
	v_lshl_add_u64 v[0:1], v[0:1], 0, s[6:7]
	s_add_u32 s6, s16, s12
	s_addc_u32 s9, s17, s13
	s_add_u32 s8, s6, s11
	s_addc_u32 s9, s9, 0
	s_movk_i32 s11, 0x400
	s_cbranch_execz .LBB0_3205
	s_branch .LBB0_3206

; #define CV_LOAD(qi, Q, D) do { _Pragma("unroll") for (int s_ = 0; s_ < 2; ++s_) _Pragma("unroll") for (int r_ = 0; r_ < 4; ++r_) Q.v[s_][r_] = *(const f32x4*)(D.src + (size_t)(16 * (2 * (qi) + s_) + r_) * D.N); asm volatile("" ::: "memory"); } while (0)
; #define CV_PROC(qi, Q) do { _Pragma("unroll") for (int s_ = 0; s_ < 2; ++s_) _Pragma("unroll") for (int c_ = 0; c_ < 4; ++c_) \
;         *(LAS unsigned*)(scr + (4 * nl + c_) * 132 + 16 * (2 * (qi) + s_) + 4 * kg) = pg8::pk4_fp8c(Q.v[s_][0][c_] * FP8_WSC, Q.v[s_][1][c_] * FP8_WSC, Q.v[s_][2][c_] * FP8_WSC, Q.v[s_][3][c_] * FP8_WSC); asm volatile("" ::: "memory"); } while (0)
; __device__ __forceinline__ void moe_conv_stream(const Args& a, ARGAS unsigned char* ws, LAS unsigned char* scr, int first, int cnt, int lane) {
;     ...
;     Qt A, B, C, D4;
;     ConvItem cur = moe_conv_desc(a, ws, first, lane);
;     CV_LOAD(0, A, cur); CV_LOAD(1, B, cur); CV_LOAD(2, C, cur);
; #pragma unroll 1
;     for (int i = 0; i < cnt; ++i) {
;         const ConvItem nxt = moe_conv_desc(a, ws, first + 8 * ((i + 1 < cnt) ? i + 1 : i), lane);
;         CV_LOAD(3, D4, cur); CV_PROC(0, A);
;         CV_LOAD(0, A, nxt);  CV_PROC(1, B);
;         CV_LOAD(1, B, nxt);  CV_PROC(2, C);
;         CV_LOAD(2, C, nxt);  CV_PROC(3, D4);
.LBB0_3207:
	s_waitcnt vmcnt(17)
	v_mul_f32_e32 v28, 0x43000000, v28
	v_mul_f32_e32 v16, 0x43000000, v16
	v_med3_f32 v28, v28, s27, v147
	v_med3_f32 v16, v16, s27, v147
	v_mov_b32_e32 v148, v129
	v_cvt_pk_fp8_f32 v148, v28, v16
	v_mul_f32_e32 v20, 0x43000000, v20
	v_mul_f32_e32 v16, 0x43000000, v24
	v_med3_f32 v20, v20, s27, v147
	v_med3_f32 v16, v16, s27, v147
	v_cvt_pk_fp8_f32 v148, v20, v16 op_sel:[0,0,1]
	v_mul_f32_e32 v16, 0x43000000, v29
	v_mul_f32_e32 v17, 0x43000000, v17
	v_mul_f32_e32 v20, 0x43000000, v21
	v_med3_f32 v16, v16, s27, v147
	v_med3_f32 v17, v17, s27, v147
	v_mov_b32_e32 v21, v129
	v_cvt_pk_fp8_f32 v21, v16, v17
	v_mul_f32_e32 v16, 0x43000000, v25
	v_med3_f32 v17, v20, s27, v147
	v_med3_f32 v16, v16, s27, v147
	v_cvt_pk_fp8_f32 v21, v17, v16 op_sel:[0,0,1]
	v_mul_f32_e32 v16, 0x43000000, v30
	v_mul_f32_e32 v17, 0x43000000, v18
	v_med3_f32 v16, v16, s27, v147
	v_med3_f32 v17, v17, s27, v147
	v_mov_b32_e32 v20, v129
	v_cvt_pk_fp8_f32 v20, v16, v17
	v_mul_f32_e32 v18, 0x43000000, v22
	v_mul_f32_e32 v16, 0x43000000, v26
	v_med3_f32 v17, v18, s27, v147
	v_med3_f32 v16, v16, s27, v147
	v_cvt_pk_fp8_f32 v20, v17, v16 op_sel:[0,0,1]
	v_mul_f32_e32 v16, 0x43000000, v31
	v_mul_f32_e32 v17, 0x43000000, v19
	v_med3_f32 v16, v16, s27, v147
	v_med3_f32 v17, v17, s27, v147
	v_mov_b32_e32 v19, v129
	v_cvt_pk_fp8_f32 v19, v16, v17
	v_mul_f32_e32 v18, 0x43000000, v23
	v_mul_f32_e32 v16, 0x43000000, v27
	v_med3_f32 v17, v18, s27, v147
	v_med3_f32 v16, v16, s27, v147
	v_mul_f32_e32 v0, 0x43000000, v0
	v_mul_f32_e32 v4, 0x43000000, v4
	v_cvt_pk_fp8_f32 v19, v17, v16 op_sel:[0,0,1]
	v_med3_f32 v0, v0, s27, v147
	v_med3_f32 v4, v4, s27, v147
	v_mov_b32_e32 v16, v129
	v_cvt_pk_fp8_f32 v16, v0, v4
	v_mul_f32_e32 v8, 0x43000000, v8
	s_waitcnt vmcnt(16)
	v_mul_f32_e32 v0, 0x43000000, v12
	v_med3_f32 v4, v8, s27, v147
	v_med3_f32 v0, v0, s27, v147
	v_cvt_pk_fp8_f32 v16, v4, v0 op_sel:[0,0,1]
	v_mul_f32_e32 v0, 0x43000000, v1
	v_mul_f32_e32 v1, 0x43000000, v5
	v_med3_f32 v0, v0, s27, v147
	v_med3_f32 v1, v1, s27, v147
	v_mov_b32_e32 v5, v129
	v_cvt_pk_fp8_f32 v5, v0, v1
	v_mul_f32_e32 v4, 0x43000000, v9
	v_mul_f32_e32 v0, 0x43000000, v13
	v_med3_f32 v1, v4, s27, v147
	v_med3_f32 v0, v0, s27, v147
	v_cvt_pk_fp8_f32 v5, v1, v0 op_sel:[0,0,1]
	v_mul_f32_e32 v0, 0x43000000, v2
	v_mul_f32_e32 v1, 0x43000000, v6
	v_med3_f32 v0, v0, s27, v147
	v_med3_f32 v1, v1, s27, v147
	v_mov_b32_e32 v4, v129
	v_cvt_pk_fp8_f32 v4, v0, v1
	v_mad_u64_u32 v[96:97], s[14:15], s6, v146, v[96:97]
	v_mul_f32_e32 v2, 0x43000000, v10
	v_mul_f32_e32 v0, 0x43000000, v14
	s_lshl_b64 s[14:15], s[6:7], 2
	v_med3_f32 v1, v2, s27, v147
	v_med3_f32 v0, v0, s27, v147
	v_lshl_add_u64 v[132:133], v[98:99], 0, v[128:129]
	v_lshl_add_u64 v[98:99], v[96:97], 0, s[14:15]
	v_cvt_pk_fp8_f32 v4, v1, v0 op_sel:[0,0,1]
	v_mul_f32_e32 v0, 0x43000000, v3
	v_mul_f32_e32 v1, 0x43000000, v7
	global_load_dwordx4 v[116:119], v[96:97], off
	global_load_dwordx4 v[120:123], v[98:99], off
	v_lshl_add_u64 v[96:97], v[98:99], 0, s[14:15]
	v_med3_f32 v0, v0, s27, v147
	v_med3_f32 v1, v1, s27, v147
	v_mov_b32_e32 v3, v129
	v_lshl_add_u64 v[98:99], v[96:97], 0, s[14:15]
	v_cvt_pk_fp8_f32 v3, v0, v1
	global_load_dwordx4 v[124:127], v[96:97], off
	global_load_dwordx4 v[112:115], v[98:99], off
	v_mad_u64_u32 v[96:97], s[42:43], s6, 52, v[98:99]
	v_lshl_add_u64 v[98:99], v[96:97], 0, s[14:15]
	v_mul_f32_e32 v2, 0x43000000, v11
	v_mul_f32_e32 v0, 0x43000000, v15
	global_load_dwordx4 v[100:103], v[96:97], off
	global_load_dwordx4 v[104:107], v[98:99], off
	v_lshl_add_u64 v[96:97], v[98:99], 0, s[14:15]
	v_med3_f32 v1, v2, s27, v147
	v_med3_f32 v0, v0, s27, v147
	v_lshl_add_u64 v[98:99], v[96:97], 0, s[14:15]
	v_cvt_pk_fp8_f32 v3, v1, v0 op_sel:[0,0,1]
	s_waitcnt vmcnt(21)
	v_mul_f32_e32 v40, 0x43000000, v40
	s_waitcnt vmcnt(20)
	v_mul_f32_e32 v48, 0x43000000, v48
	global_load_dwordx4 v[108:111], v[96:97], off
	s_nop 0
	global_load_dwordx4 v[96:99], v[98:99], off
	ds_write2_b32 v143, v148, v16 offset1:4
	ds_write2_b32 v143, v21, v5 offset0:33 offset1:37
	ds_write2_b32 v143, v20, v4 offset0:66 offset1:70
	ds_write2_b32 v143, v19, v3 offset0:99 offset1:103
	v_med3_f32 v40, v40, s27, v147
	v_med3_f32 v48, v48, s27, v147
	v_mov_b32_e32 v148, v129
	v_cvt_pk_fp8_f32 v148, v40, v48
	s_waitcnt vmcnt(21)
	v_mul_f32_e32 v60, 0x43000000, v60
	s_waitcnt vmcnt(20)
	v_mul_f32_e32 v40, 0x43000000, v56
	v_med3_f32 v48, v60, s27, v147
	v_med3_f32 v40, v40, s27, v147
	v_cvt_pk_fp8_f32 v148, v48, v40 op_sel:[0,0,1]
	v_mul_f32_e32 v40, 0x43000000, v41
	v_mul_f32_e32 v41, 0x43000000, v49
	v_med3_f32 v40, v40, s27, v147
	v_med3_f32 v41, v41, s27, v147
	v_mov_b32_e32 v49, v129
	v_cvt_pk_fp8_f32 v49, v40, v41
	v_mul_f32_e32 v48, 0x43000000, v61
	v_mul_f32_e32 v40, 0x43000000, v57
	v_med3_f32 v41, v48, s27, v147
	v_med3_f32 v40, v40, s27, v147
	v_cvt_pk_fp8_f32 v49, v41, v40 op_sel:[0,0,1]
	v_mul_f32_e32 v40, 0x43000000, v42
	v_mul_f32_e32 v41, 0x43000000, v50
	v_med3_f32 v40, v40, s27, v147
	v_med3_f32 v41, v41, s27, v147
	v_mov_b32_e32 v48, v129
	v_cvt_pk_fp8_f32 v48, v40, v41
	v_mul_f32_e32 v42, 0x43000000, v62
	v_mul_f32_e32 v40, 0x43000000, v58
	v_med3_f32 v41, v42, s27, v147
	v_med3_f32 v40, v40, s27, v147
	v_cvt_pk_fp8_f32 v48, v41, v40 op_sel:[0,0,1]
	v_mul_f32_e32 v40, 0x43000000, v43
	v_mul_f32_e32 v41, 0x43000000, v51
	v_med3_f32 v40, v40, s27, v147
	v_med3_f32 v41, v41, s27, v147
	v_mov_b32_e32 v43, v129
	v_cvt_pk_fp8_f32 v43, v40, v41
	v_mul_f32_e32 v42, 0x43000000, v63
	v_mul_f32_e32 v40, 0x43000000, v59
	v_med3_f32 v41, v42, s27, v147
	v_med3_f32 v40, v40, s27, v147
	s_waitcnt vmcnt(19)
	v_mul_f32_e32 v32, 0x43000000, v32
	s_waitcnt vmcnt(18)
; #define CV_LOAD(qi, Q, D) do { _Pragma("unroll") for (int s_ = 0; s_ < 2; ++s_) _Pragma("unroll") for (int r_ = 0; r_ < 4; ++r_) Q.v[s_][r_] = *(const f32x4*)(D.src + (size_t)(16 * (2 * (qi) + s_) + r_) * D.N); asm volatile("" ::: "memory"); } while (0)
; #define CV_PROC(qi, Q) do { _Pragma("unroll") for (int s_ = 0; s_ < 2; ++s_) _Pragma("unroll") for (int c_ = 0; c_ < 4; ++c_) \
;         *(LAS unsigned*)(scr + (4 * nl + c_) * 132 + 16 * (2 * (qi) + s_) + 4 * kg) = pg8::pk4_fp8c(Q.v[s_][0][c_] * FP8_WSC, Q.v[s_][1][c_] * FP8_WSC, Q.v[s_][2][c_] * FP8_WSC, Q.v[s_][3][c_] * FP8_WSC); asm volatile("" ::: "memory"); } while (0)
; __device__ __forceinline__ void moe_conv_stream(const Args& a, ARGAS unsigned char* ws, LAS unsigned char* scr, int first, int cnt, int lane) {
;     ...
;     Qt A, B, C, D4;
;     ConvItem cur = moe_conv_desc(a, ws, first, lane);
;     CV_LOAD(0, A, cur); CV_LOAD(1, B, cur); CV_LOAD(2, C, cur);
; #pragma unroll 1
;     for (int i = 0; i < cnt; ++i) {
;         const ConvItem nxt = moe_conv_desc(a, ws, first + 8 * ((i + 1 < cnt) ? i + 1 : i), lane);
;         CV_LOAD(3, D4, cur); CV_PROC(0, A);
;         CV_LOAD(0, A, nxt);  CV_PROC(1, B);
;         CV_LOAD(1, B, nxt);  CV_PROC(2, C);
;         CV_LOAD(2, C, nxt);  CV_PROC(3, D4);
	v_mul_f32_e32 v36, 0x43000000, v36
	v_cvt_pk_fp8_f32 v43, v41, v40 op_sel:[0,0,1]
	v_med3_f32 v32, v32, s27, v147
	v_med3_f32 v36, v36, s27, v147
	v_mov_b32_e32 v41, v129
	v_cvt_pk_fp8_f32 v41, v32, v36
	s_waitcnt vmcnt(17)
	v_mul_f32_e32 v40, 0x43000000, v52
	s_waitcnt vmcnt(16)
	v_mul_f32_e32 v32, 0x43000000, v44
	v_med3_f32 v36, v40, s27, v147
	v_med3_f32 v32, v32, s27, v147
	v_cvt_pk_fp8_f32 v41, v36, v32 op_sel:[0,0,1]
	v_mul_f32_e32 v32, 0x43000000, v33
	v_mul_f32_e32 v33, 0x43000000, v37
	v_med3_f32 v32, v32, s27, v147
	v_med3_f32 v33, v33, s27, v147
	v_mov_b32_e32 v37, v129
	v_cvt_pk_fp8_f32 v37, v32, v33
	v_mul_f32_e32 v36, 0x43000000, v53
	v_mul_f32_e32 v32, 0x43000000, v45
	v_med3_f32 v33, v36, s27, v147
	v_med3_f32 v32, v32, s27, v147
	v_cvt_pk_fp8_f32 v37, v33, v32 op_sel:[0,0,1]
	v_mul_f32_e32 v32, 0x43000000, v34
	v_mul_f32_e32 v33, 0x43000000, v38
	v_med3_f32 v32, v32, s27, v147
	v_med3_f32 v33, v33, s27, v147
	v_mov_b32_e32 v36, v129
	v_cvt_pk_fp8_f32 v36, v32, v33
	v_mul_f32_e32 v34, 0x43000000, v54
	v_mul_f32_e32 v32, 0x43000000, v46
	s_lshl_b32 s6, s13, 2
	v_med3_f32 v33, v34, s27, v147
	v_med3_f32 v32, v32, s27, v147
	v_lshl_add_u64 v[0:1], v[132:133], 0, s[6:7]
	s_lshl_b32 s6, s13, 3
	v_cvt_pk_fp8_f32 v36, v33, v32 op_sel:[0,0,1]
	v_mul_f32_e32 v32, 0x43000000, v35
	v_mul_f32_e32 v33, 0x43000000, v39
	global_load_dwordx4 v[28:31], v[132:133], off
	global_load_dwordx4 v[16:19], v[0:1], off
	v_lshl_add_u64 v[0:1], v[132:133], 0, s[6:7]
	s_mul_i32 s6, s13, 12
	v_med3_f32 v32, v32, s27, v147
	v_med3_f32 v33, v33, s27, v147
	v_mov_b32_e32 v35, v129
	v_lshl_add_u64 v[2:3], v[132:133], 0, s[6:7]
	s_lshl_b32 s6, s13, 6
	v_cvt_pk_fp8_f32 v35, v32, v33
	global_load_dwordx4 v[20:23], v[0:1], off
	global_load_dwordx4 v[24:27], v[2:3], off
	v_lshl_add_u64 v[0:1], v[132:133], 0, s[6:7]
	s_mul_i32 s6, s13, 0x44
	v_lshl_add_u64 v[4:5], v[132:133], 0, s[6:7]
	s_mul_i32 s6, s13, 0x48
	v_mul_f32_e32 v34, 0x43000000, v55
	v_mul_f32_e32 v32, 0x43000000, v47
	v_lshl_add_u64 v[8:9], v[132:133], 0, s[6:7]
	s_mul_i32 s6, s13, 0x4c
	v_med3_f32 v33, v34, s27, v147
	v_med3_f32 v32, v32, s27, v147
	v_lshl_add_u64 v[12:13], v[132:133], 0, s[6:7]
	v_cvt_pk_fp8_f32 v35, v33, v32 op_sel:[0,0,1]
	s_waitcnt vmcnt(19)
	v_mul_f32_e32 v72, 0x43000000, v72
	s_waitcnt vmcnt(18)
	v_mul_f32_e32 v80, 0x43000000, v80
	global_load_dwordx4 v[0:3], v[0:1], off
	s_nop 0
	global_load_dwordx4 v[4:7], v[4:5], off
	s_nop 0
	global_load_dwordx4 v[8:11], v[8:9], off
	s_nop 0
	global_load_dwordx4 v[12:15], v[12:13], off
	ds_write2_b32 v144, v148, v41 offset0:8 offset1:12
	ds_write2_b32 v144, v49, v37 offset0:41 offset1:45
	ds_write2_b32 v144, v48, v36 offset0:74 offset1:78
	ds_write2_b32 v144, v43, v35 offset0:107 offset1:111
	v_med3_f32 v72, v72, s27, v147
	v_med3_f32 v80, v80, s27, v147
	v_mov_b32_e32 v148, v129
	v_cvt_pk_fp8_f32 v148, v72, v80
	s_waitcnt vmcnt(21)
	v_mul_f32_e32 v92, 0x43000000, v92
	s_waitcnt vmcnt(20)
	v_mul_f32_e32 v72, 0x43000000, v88
	v_med3_f32 v80, v92, s27, v147
	v_med3_f32 v72, v72, s27, v147
	v_cvt_pk_fp8_f32 v148, v80, v72 op_sel:[0,0,1]
	v_mul_f32_e32 v72, 0x43000000, v73
	v_mul_f32_e32 v73, 0x43000000, v81
	v_med3_f32 v72, v72, s27, v147
	v_med3_f32 v73, v73, s27, v147
	v_mov_b32_e32 v81, v129
	v_cvt_pk_fp8_f32 v81, v72, v73
	v_mul_f32_e32 v80, 0x43000000, v93
	v_mul_f32_e32 v72, 0x43000000, v89
	v_med3_f32 v73, v80, s27, v147
	v_med3_f32 v72, v72, s27, v147
	v_cvt_pk_fp8_f32 v81, v73, v72 op_sel:[0,0,1]
	v_mul_f32_e32 v72, 0x43000000, v74
	v_mul_f32_e32 v73, 0x43000000, v82
	v_med3_f32 v72, v72, s27, v147
	v_med3_f32 v73, v73, s27, v147
	v_mov_b32_e32 v80, v129
	v_cvt_pk_fp8_f32 v80, v72, v73
	v_mul_f32_e32 v74, 0x43000000, v94
	v_mul_f32_e32 v72, 0x43000000, v90
	v_med3_f32 v73, v74, s27, v147
	v_med3_f32 v72, v72, s27, v147
	v_cvt_pk_fp8_f32 v80, v73, v72 op_sel:[0,0,1]
	v_mul_f32_e32 v72, 0x43000000, v75
	v_mul_f32_e32 v73, 0x43000000, v83
	v_med3_f32 v72, v72, s27, v147
	v_med3_f32 v73, v73, s27, v147
	v_mov_b32_e32 v75, v129
	v_cvt_pk_fp8_f32 v75, v72, v73
	v_mul_f32_e32 v74, 0x43000000, v95
	v_mul_f32_e32 v72, 0x43000000, v91
	v_med3_f32 v73, v74, s27, v147
	v_med3_f32 v72, v72, s27, v147
	s_waitcnt vmcnt(19)
	v_mul_f32_e32 v64, 0x43000000, v64
	s_waitcnt vmcnt(18)
	v_mul_f32_e32 v68, 0x43000000, v68
	v_cvt_pk_fp8_f32 v75, v73, v72 op_sel:[0,0,1]
	v_med3_f32 v64, v64, s27, v147
	v_med3_f32 v68, v68, s27, v147
	v_mov_b32_e32 v73, v129
	v_cvt_pk_fp8_f32 v73, v64, v68
	s_waitcnt vmcnt(17)
	v_mul_f32_e32 v72, 0x43000000, v84
	s_waitcnt vmcnt(16)
	v_mul_f32_e32 v64, 0x43000000, v76
	v_med3_f32 v68, v72, s27, v147
	v_med3_f32 v64, v64, s27, v147
	v_cvt_pk_fp8_f32 v73, v68, v64 op_sel:[0,0,1]
	v_mul_f32_e32 v64, 0x43000000, v65
	v_mul_f32_e32 v65, 0x43000000, v69
	v_med3_f32 v64, v64, s27, v147
	v_med3_f32 v65, v65, s27, v147
	v_mov_b32_e32 v69, v129
	v_cvt_pk_fp8_f32 v69, v64, v65
	v_mul_f32_e32 v68, 0x43000000, v85
	v_mul_f32_e32 v64, 0x43000000, v77
	v_med3_f32 v65, v68, s27, v147
	v_med3_f32 v64, v64, s27, v147
	v_cvt_pk_fp8_f32 v69, v65, v64 op_sel:[0,0,1]
	v_mul_f32_e32 v64, 0x43000000, v66
	v_mul_f32_e32 v65, 0x43000000, v70
	v_med3_f32 v64, v64, s27, v147
	v_med3_f32 v65, v65, s27, v147
	v_mov_b32_e32 v68, v129
	v_cvt_pk_fp8_f32 v68, v64, v65
	s_lshl_b32 s6, s13, 7
	v_mul_f32_e32 v66, 0x43000000, v86
	v_mul_f32_e32 v64, 0x43000000, v78
	v_lshl_add_u64 v[32:33], v[132:133], 0, s[6:7]
	s_mul_i32 s6, s13, 0x84
	v_med3_f32 v65, v66, s27, v147
	v_med3_f32 v64, v64, s27, v147
	v_lshl_add_u64 v[34:35], v[132:133], 0, s[6:7]
	s_mul_i32 s6, s13, 0x88
	v_cvt_pk_fp8_f32 v68, v65, v64 op_sel:[0,0,1]
	v_mul_f32_e32 v64, 0x43000000, v67
	v_mul_f32_e32 v65, 0x43000000, v71
	global_load_dwordx4 v[40:43], v[32:33], off
	global_load_dwordx4 v[48:51], v[34:35], off
	v_lshl_add_u64 v[32:33], v[132:133], 0, s[6:7]
	s_mul_i32 s6, s13, 0x8c
	v_med3_f32 v64, v64, s27, v147
	v_med3_f32 v65, v65, s27, v147
	v_mov_b32_e32 v67, v129
	v_lshl_add_u64 v[34:35], v[132:133], 0, s[6:7]
	s_mul_i32 s6, s13, 0xc0
	v_cvt_pk_fp8_f32 v67, v64, v65
	global_load_dwordx4 v[60:63], v[32:33], off
	global_load_dwordx4 v[56:59], v[34:35], off
	v_lshl_add_u64 v[32:33], v[132:133], 0, s[6:7]
	s_mul_i32 s6, s13, 0xc4
	v_lshl_add_u64 v[36:37], v[132:133], 0, s[6:7]
	s_mul_i32 s6, s13, 0xc8
	v_mul_f32_e32 v66, 0x43000000, v87
	v_mul_f32_e32 v64, 0x43000000, v79
	v_lshl_add_u64 v[44:45], v[132:133], 0, s[6:7]
	s_mul_i32 s6, s13, 0xcc
	v_med3_f32 v65, v66, s27, v147
	v_med3_f32 v64, v64, s27, v147
	v_lshl_add_u64 v[46:47], v[132:133], 0, s[6:7]
	v_cvt_pk_fp8_f32 v67, v65, v64 op_sel:[0,0,1]
	s_waitcnt vmcnt(19)
; #define LAS __attribute__((address_space(3)))
; #define LDS_WAIT() asm volatile("s_waitcnt lgkmcnt(0)" ::: "memory")
; #define CV_LOAD(qi, Q, D) do { _Pragma("unroll") for (int s_ = 0; s_ < 2; ++s_) _Pragma("unroll") for (int r_ = 0; r_ < 4; ++r_) Q.v[s_][r_] = *(const f32x4*)(D.src + (size_t)(16 * (2 * (qi) + s_) + r_) * D.N); asm volatile("" ::: "memory"); } while (0)
; #define CV_PROC(qi, Q) do { _Pragma("unroll") for (int s_ = 0; s_ < 2; ++s_) _Pragma("unroll") for (int c_ = 0; c_ < 4; ++c_) \
;         *(LAS unsigned*)(scr + (4 * nl + c_) * 132 + 16 * (2 * (qi) + s_) + 4 * kg) = pg8::pk4_fp8c(Q.v[s_][0][c_] * FP8_WSC, Q.v[s_][1][c_] * FP8_WSC, Q.v[s_][2][c_] * FP8_WSC, Q.v[s_][3][c_] * FP8_WSC); asm volatile("" ::: "memory"); } while (0)
; __device__ __forceinline__ void moe_conv_stream(const Args& a, ARGAS unsigned char* ws, LAS unsigned char* scr, int first, int cnt, int lane) {
;     ...
;         CV_LOAD(3, D4, cur); CV_PROC(0, A);
;         CV_LOAD(0, A, nxt);  CV_PROC(1, B);
;         CV_LOAD(1, B, nxt);  CV_PROC(2, C);
;         CV_LOAD(2, C, nxt);  CV_PROC(3, D4);
;         LDS_WAIT(); asm volatile("" ::: "memory");
;         const int n0 = cur.gu > 0 ? cur.gu - 1 : -cur.gu - 1;
; #pragma unroll
;         for (int j = 0; j < 8; ++j) { const int row = (lane >> 3) + 8 * j; const LAS unsigned* s = (const LAS unsigned*)(scr + row * 132 + 16 * c8);
;             u32x4 o; o.x = s[0]; o.y = s[1]; o.z = s[2]; o.w = s[3];
;             const int n = n0 + row, wr_ = cur.gu > 0 ? RmGu()(n) : n;
;             *(u32x4*)(cur.dst + (size_t)wr_ * cur.ldk + 16 * c8) = o; }
	v_mul_f32_e32 v116, 0x43000000, v116
	s_waitcnt vmcnt(18)
	v_mul_f32_e32 v120, 0x43000000, v120
	global_load_dwordx4 v[32:35], v[32:33], off
	s_nop 0
	global_load_dwordx4 v[36:39], v[36:37], off
	s_nop 0
	global_load_dwordx4 v[52:55], v[44:45], off
	s_nop 0
	global_load_dwordx4 v[44:47], v[46:47], off
	ds_write2_b32 v144, v148, v73 offset0:16 offset1:20
	ds_write2_b32 v144, v81, v69 offset0:49 offset1:53
	ds_write2_b32 v144, v80, v68 offset0:82 offset1:86
	ds_write2_b32 v144, v75, v67 offset0:115 offset1:119
	v_med3_f32 v116, v116, s27, v147
	v_med3_f32 v120, v120, s27, v147
	v_mov_b32_e32 v148, v129
	v_cvt_pk_fp8_f32 v148, v116, v120
	s_waitcnt vmcnt(21)
	v_mul_f32_e32 v124, 0x43000000, v124
	s_waitcnt vmcnt(20)
	v_mul_f32_e32 v112, 0x43000000, v112
	v_med3_f32 v116, v124, s27, v147
	v_med3_f32 v112, v112, s27, v147
	v_cvt_pk_fp8_f32 v148, v116, v112 op_sel:[0,0,1]
	v_mul_f32_e32 v112, 0x43000000, v117
	v_mul_f32_e32 v116, 0x43000000, v121
	v_med3_f32 v112, v112, s27, v147
	v_med3_f32 v116, v116, s27, v147
	v_mov_b32_e32 v120, v129
	v_cvt_pk_fp8_f32 v120, v112, v116
	v_mul_f32_e32 v117, 0x43000000, v125
	v_mul_f32_e32 v112, 0x43000000, v113
	v_med3_f32 v113, v117, s27, v147
	v_med3_f32 v112, v112, s27, v147
	v_cvt_pk_fp8_f32 v120, v113, v112 op_sel:[0,0,1]
	v_mul_f32_e32 v112, 0x43000000, v118
	v_mul_f32_e32 v113, 0x43000000, v122
	v_med3_f32 v112, v112, s27, v147
	v_med3_f32 v113, v113, s27, v147
	v_mov_b32_e32 v117, v129
	v_cvt_pk_fp8_f32 v117, v112, v113
	v_mul_f32_e32 v116, 0x43000000, v126
	v_mul_f32_e32 v112, 0x43000000, v114
	v_med3_f32 v113, v116, s27, v147
	v_med3_f32 v112, v112, s27, v147
	v_cvt_pk_fp8_f32 v117, v113, v112 op_sel:[0,0,1]
	v_mul_f32_e32 v112, 0x43000000, v119
	v_mul_f32_e32 v113, 0x43000000, v123
	v_med3_f32 v112, v112, s27, v147
	v_med3_f32 v113, v113, s27, v147
	v_mov_b32_e32 v116, v129
	v_cvt_pk_fp8_f32 v116, v112, v113
	v_mul_f32_e32 v114, 0x43000000, v127
	v_mul_f32_e32 v112, 0x43000000, v115
	v_med3_f32 v113, v114, s27, v147
	v_med3_f32 v112, v112, s27, v147
	s_waitcnt vmcnt(19)
	v_mul_f32_e32 v100, 0x43000000, v100
	s_waitcnt vmcnt(18)
	v_mul_f32_e32 v104, 0x43000000, v104
	v_cvt_pk_fp8_f32 v116, v113, v112 op_sel:[0,0,1]
	v_med3_f32 v100, v100, s27, v147
	v_med3_f32 v104, v104, s27, v147
	v_mov_b32_e32 v112, v129
	v_cvt_pk_fp8_f32 v112, v100, v104
	s_waitcnt vmcnt(17)
	v_mul_f32_e32 v108, 0x43000000, v108
	s_waitcnt vmcnt(16)
	v_mul_f32_e32 v96, 0x43000000, v96
	v_med3_f32 v100, v108, s27, v147
	v_med3_f32 v96, v96, s27, v147
	v_cvt_pk_fp8_f32 v112, v100, v96 op_sel:[0,0,1]
	v_mul_f32_e32 v96, 0x43000000, v101
	v_mul_f32_e32 v100, 0x43000000, v105
	v_med3_f32 v96, v96, s27, v147
	v_med3_f32 v100, v100, s27, v147
	v_mov_b32_e32 v104, v129
	v_cvt_pk_fp8_f32 v104, v96, v100
	v_mul_f32_e32 v101, 0x43000000, v109
	v_mul_f32_e32 v96, 0x43000000, v97
	v_med3_f32 v97, v101, s27, v147
	v_med3_f32 v96, v96, s27, v147
	s_lshl_b32 s6, s13, 8
	v_cvt_pk_fp8_f32 v104, v97, v96 op_sel:[0,0,1]
	v_mul_f32_e32 v96, 0x43000000, v102
	v_mul_f32_e32 v97, 0x43000000, v106
	v_lshl_add_u64 v[64:65], v[132:133], 0, s[6:7]
	s_mul_i32 s6, s13, 0x104
	v_med3_f32 v96, v96, s27, v147
	v_med3_f32 v97, v97, s27, v147
	v_mov_b32_e32 v101, v129
	v_lshl_add_u64 v[66:67], v[132:133], 0, s[6:7]
	s_mul_i32 s6, s13, 0x108
	v_cvt_pk_fp8_f32 v101, v96, v97
	global_load_dwordx4 v[72:75], v[64:65], off
	global_load_dwordx4 v[80:83], v[66:67], off
	v_lshl_add_u64 v[64:65], v[132:133], 0, s[6:7]
	s_mul_i32 s6, s13, 0x10c
	v_lshl_add_u64 v[66:67], v[132:133], 0, s[6:7]
	s_mul_i32 s6, s13, 0x140
	v_mul_f32_e32 v100, 0x43000000, v110
	v_mul_f32_e32 v96, 0x43000000, v98
	global_load_dwordx4 v[92:95], v[64:65], off
	global_load_dwordx4 v[88:91], v[66:67], off
	v_lshl_add_u64 v[64:65], v[132:133], 0, s[6:7]
	s_mul_i32 s6, s13, 0x144
	v_med3_f32 v97, v100, s27, v147
	v_med3_f32 v96, v96, s27, v147
	v_lshl_add_u64 v[68:69], v[132:133], 0, s[6:7]
	s_mul_i32 s6, s13, 0x148
	v_cvt_pk_fp8_f32 v101, v97, v96 op_sel:[0,0,1]
	v_mul_f32_e32 v96, 0x43000000, v103
	v_mul_f32_e32 v97, 0x43000000, v107
	v_lshl_add_u64 v[76:77], v[132:133], 0, s[6:7]
	s_mul_i32 s6, s13, 0x14c
	v_med3_f32 v96, v96, s27, v147
	v_med3_f32 v97, v97, s27, v147
	v_mov_b32_e32 v100, v129
	v_lshl_add_u64 v[78:79], v[132:133], 0, s[6:7]
	v_cvt_pk_fp8_f32 v100, v96, v97
	s_add_i32 s6, s38, -1
	s_not_b32 s12, s38
	s_cmp_gt_i32 s38, 0
	global_load_dwordx4 v[64:67], v[64:65], off
	s_nop 0
	global_load_dwordx4 v[68:71], v[68:69], off
	s_nop 0
	global_load_dwordx4 v[84:87], v[76:77], off
	s_nop 0
	global_load_dwordx4 v[76:79], v[78:79], off
	v_mul_f32_e32 v98, 0x43000000, v111
	v_mul_f32_e32 v96, 0x43000000, v99
	s_cselect_b64 vcc, -1, 0
	v_med3_f32 v97, v98, s27, v147
	v_med3_f32 v96, v96, s27, v147
	s_and_b64 s[14:15], vcc, exec
	v_cvt_pk_fp8_f32 v100, v97, v96 op_sel:[0,0,1]
	s_cselect_b32 s6, s6, s12
	ds_write2_b32 v144, v148, v112 offset0:24 offset1:28
	ds_write2_b32 v144, v120, v104 offset0:57 offset1:61
	ds_write2_b32 v144, v117, v101 offset0:90 offset1:94
	ds_write2_b32 v144, v116, v100 offset0:123 offset1:127
	v_add_u32_e32 v100, s6, v194
	v_lshlrev_b32_e32 v101, 1, v100
	v_ashrrev_i32_e32 v102, 3, v100
	s_waitcnt lgkmcnt(0)
	v_and_b32_e32 v101, 0x700, v101
	v_and_b32_e32 v102, 0xffffff80, v102
	v_add_u32_e32 v101, v101, v102
	ds_read2_b32 v[96:97], v145 offset1:1
	ds_read2_b32 v[98:99], v145 offset0:2 offset1:3
	v_and_or_b32 v101, v100, s36, v101
	v_cndmask_b32_e32 v100, v100, v101, vcc
	v_ashrrev_i32_e32 v101, 31, v100
	v_lshl_add_u64 v[104:105], s[8:9], 0, v[130:131]
	v_lshlrev_b64 v[100:101], 10, v[100:101]
	v_lshl_add_u64 v[106:107], v[104:105], 0, v[100:101]
	v_add_u32_e32 v100, 0x420, v145
	v_add_u32_e32 v102, 0x428, v145
	ds_read2_b32 v[100:101], v100 offset1:1
	ds_read2_b32 v[102:103], v102 offset1:1
	s_waitcnt lgkmcnt(2)
; #define LAS __attribute__((address_space(3)))
; #define LDS_WAIT() asm volatile("s_waitcnt lgkmcnt(0)" ::: "memory")
; __device__ __forceinline__ ConvItem moe_conv_desc(const Args& a, ARGAS unsigned char* ws, int it, int lane) {
;     const int m = it / MOE_CONV_PER_M, r = it % MOE_CONV_PER_M, nl = lane & 15, kg = lane >> 4; ConvItem d;
;     if (r < 256) { const int kb = r / 32, nb = r % 32; d.N = 2048; d.ldk = DM; d.gu = 64 * nb + 1; d.src = a.moe_w_gu + (size_t)m * DM * 2048 + (size_t)(128 * kb + 4 * kg) * 2048 + 64 * nb + 4 * nl; d.dst = (unsigned char*)(ws + WS_WGU) + (size_t)m * 2048 * DM + 128 * kb; }
;     else { const int r2 = r - 256, kb = r2 / 16, nb = r2 % 16; d.N = DM; d.ldk = EFF; d.gu = -(64 * nb) - 1; d.src = a.moe_w_down + (size_t)m * EFF * DM + (size_t)(128 * kb + 4 * kg) * DM + 64 * nb + 4 * nl; d.dst = (unsigned char*)(ws + WS_WDN) + (size_t)m * DM * EFF + 128 * kb; }
; __device__ __forceinline__ void moe_conv_stream(const Args& a, ARGAS unsigned char* ws, LAS unsigned char* scr, int first, int cnt, int lane) {
;     ...
;         const int n0 = cur.gu > 0 ? cur.gu - 1 : -cur.gu - 1;
; #pragma unroll
;         for (int j = 0; j < 8; ++j) { const int row = (lane >> 3) + 8 * j; const LAS unsigned* s = (const LAS unsigned*)(scr + row * 132 + 16 * c8);
;             u32x4 o; o.x = s[0]; o.y = s[1]; o.z = s[2]; o.w = s[3];
;             const int n = n0 + row, wr_ = cur.gu > 0 ? RmGu()(n) : n;
;             *(u32x4*)(cur.dst + (size_t)wr_ * cur.ldk + 16 * c8) = o; }
;         LDS_WAIT(); asm volatile("" ::: "memory");
;         cur = nxt;
	global_store_dwordx4 v[106:107], v[96:99], off
	s_add_i32 s39, s39, 8
	s_cmpk_eq_i32 s39, 0x28
	v_add_u32_e32 v96, s6, v135
	v_lshlrev_b32_e32 v97, 1, v96
	v_ashrrev_i32_e32 v98, 3, v96
	v_and_b32_e32 v97, 0x700, v97
	v_and_b32_e32 v98, 0xffffff80, v98
	v_add_u32_e32 v97, v97, v98
	v_and_or_b32 v97, v96, s36, v97
	v_cndmask_b32_e32 v96, v96, v97, vcc
	v_ashrrev_i32_e32 v97, 31, v96
	v_lshlrev_b64 v[96:97], 10, v[96:97]
	v_lshl_add_u64 v[96:97], v[104:105], 0, v[96:97]
	s_waitcnt lgkmcnt(0)
	global_store_dwordx4 v[96:97], v[100:103], off
	v_add_u32_e32 v96, 0x840, v145
	v_add_u32_e32 v98, 0x848, v145
	v_add_u32_e32 v100, s6, v136
	v_lshlrev_b32_e32 v101, 1, v100
	v_ashrrev_i32_e32 v102, 3, v100
	v_and_b32_e32 v101, 0x700, v101
	v_and_b32_e32 v102, 0xffffff80, v102
	v_add_u32_e32 v101, v101, v102
	ds_read2_b32 v[96:97], v96 offset1:1
	ds_read2_b32 v[98:99], v98 offset1:1
	v_and_or_b32 v101, v100, s36, v101
	v_cndmask_b32_e32 v100, v100, v101, vcc
	v_ashrrev_i32_e32 v101, 31, v100
	v_lshlrev_b64 v[100:101], 10, v[100:101]
	v_lshl_add_u64 v[106:107], v[104:105], 0, v[100:101]
	v_add_u32_e32 v100, 0xc60, v145
	v_add_u32_e32 v102, 0xc68, v145
	ds_read2_b32 v[100:101], v100 offset1:1
	ds_read2_b32 v[102:103], v102 offset1:1
	s_waitcnt lgkmcnt(2)
	global_store_dwordx4 v[106:107], v[96:99], off
	s_mov_b32 s38, s40
	s_mov_b64 s[8:9], s[10:11]
	v_add_u32_e32 v96, s6, v137
	v_lshlrev_b32_e32 v97, 1, v96
	v_ashrrev_i32_e32 v98, 3, v96
	v_and_b32_e32 v97, 0x700, v97
	v_and_b32_e32 v98, 0xffffff80, v98
	v_add_u32_e32 v97, v97, v98
	v_and_or_b32 v97, v96, s36, v97
	v_cndmask_b32_e32 v96, v96, v97, vcc
	v_ashrrev_i32_e32 v97, 31, v96
	v_lshlrev_b64 v[96:97], 10, v[96:97]
	v_lshl_add_u64 v[96:97], v[104:105], 0, v[96:97]
	s_waitcnt lgkmcnt(0)
	global_store_dwordx4 v[96:97], v[100:103], off
	v_add_u32_e32 v96, 0x1080, v145
	v_add_u32_e32 v98, 0x1088, v145
	v_add_u32_e32 v100, s6, v138
	v_lshlrev_b32_e32 v101, 1, v100
	v_ashrrev_i32_e32 v102, 3, v100
	v_and_b32_e32 v101, 0x700, v101
	v_and_b32_e32 v102, 0xffffff80, v102
	v_add_u32_e32 v101, v101, v102
	ds_read2_b32 v[96:97], v96 offset1:1
	ds_read2_b32 v[98:99], v98 offset1:1
	v_and_or_b32 v101, v100, s36, v101
	v_cndmask_b32_e32 v100, v100, v101, vcc
	v_ashrrev_i32_e32 v101, 31, v100
	v_lshlrev_b64 v[100:101], 10, v[100:101]
	v_lshl_add_u64 v[106:107], v[104:105], 0, v[100:101]
	v_add_u32_e32 v100, 0x14a0, v145
	v_add_u32_e32 v102, 0x14a8, v145
	ds_read2_b32 v[100:101], v100 offset1:1
	ds_read2_b32 v[102:103], v102 offset1:1
	s_waitcnt lgkmcnt(2)
	global_store_dwordx4 v[106:107], v[96:99], off
	s_nop 1
	v_add_u32_e32 v96, s6, v139
	v_lshlrev_b32_e32 v97, 1, v96
	v_ashrrev_i32_e32 v98, 3, v96
	v_and_b32_e32 v97, 0x700, v97
	v_and_b32_e32 v98, 0xffffff80, v98
	v_add_u32_e32 v97, v97, v98
	v_and_or_b32 v97, v96, s36, v97
	v_cndmask_b32_e32 v96, v96, v97, vcc
	v_ashrrev_i32_e32 v97, 31, v96
	v_lshlrev_b64 v[96:97], 10, v[96:97]
	v_lshl_add_u64 v[96:97], v[104:105], 0, v[96:97]
	s_waitcnt lgkmcnt(0)
	global_store_dwordx4 v[96:97], v[100:103], off
	v_add_u32_e32 v96, 0x18c0, v145
	v_add_u32_e32 v98, 0x18c8, v145
	v_add_u32_e32 v100, s6, v140
	v_lshlrev_b32_e32 v101, 1, v100
	v_ashrrev_i32_e32 v102, 3, v100
	v_and_b32_e32 v101, 0x700, v101
	v_and_b32_e32 v102, 0xffffff80, v102
	v_add_u32_e32 v101, v101, v102
	ds_read2_b32 v[96:97], v96 offset1:1
	ds_read2_b32 v[98:99], v98 offset1:1
	v_and_or_b32 v101, v100, s36, v101
	v_cndmask_b32_e32 v100, v100, v101, vcc
	v_ashrrev_i32_e32 v101, 31, v100
	v_lshlrev_b64 v[100:101], 10, v[100:101]
	v_lshl_add_u64 v[106:107], v[104:105], 0, v[100:101]
	v_add_u32_e32 v100, 0x1ce0, v145
	v_add_u32_e32 v102, 0x1ce8, v145
	ds_read2_b32 v[100:101], v100 offset1:1
	ds_read2_b32 v[102:103], v102 offset1:1
	s_waitcnt lgkmcnt(2)
	global_store_dwordx4 v[106:107], v[96:99], off
	s_nop 1
	v_add_u32_e32 v96, s6, v141
	v_lshlrev_b32_e32 v97, 1, v96
	v_ashrrev_i32_e32 v98, 3, v96
	v_and_b32_e32 v97, 0x700, v97
	v_and_b32_e32 v98, 0xffffff80, v98
	v_add_u32_e32 v97, v97, v98
	v_and_or_b32 v97, v96, s36, v97
	v_cndmask_b32_e32 v96, v96, v97, vcc
	v_ashrrev_i32_e32 v97, 31, v96
	v_lshlrev_b64 v[96:97], 10, v[96:97]
	v_lshl_add_u64 v[96:97], v[104:105], 0, v[96:97]
	s_waitcnt lgkmcnt(0)
	global_store_dwordx4 v[96:97], v[100:103], off
	s_waitcnt lgkmcnt(0)
	s_mov_b32 s6, s13
	v_mov_b64_e32 v[96:97], v[132:133]
	s_cbranch_scc1 .LBB0_3195
.LBB0_3208:
	s_cmpk_lg_i32 s39, 0x20
	s_cselect_b32 s10, s39, 0x18
	s_add_i32 s10, s10, s37
	s_mul_hi_i32 s11, s10, 0x2aaaaaab
	s_lshr_b32 s12, s11, 31
	s_ashr_i32 s11, s11, 6
	s_add_i32 s12, s11, s12
	s_mul_i32 s11, s12, 0x180
	s_sub_i32 s41, s10, s11
	s_cmpk_gt_i32 s41, 0xff
	s_cbranch_scc0 .LBB0_3210
	s_load_dwordx2 s[10:11], s[20:21], 0xe0
	s_lshl_b32 s13, s41, 6
	s_and_b32 s44, s13, 0x3c0
	s_ashr_i32 s13, s12, 31
	s_not_b32 s40, s44
	s_lshl_b64 s[14:15], s[12:13], 20
	s_lshl_b64 s[42:43], s[12:13], 22
	s_waitcnt lgkmcnt(0)
	s_add_u32 s10, s10, s42
	s_addc_u32 s11, s11, s43
	s_lshl_b32 s13, s41, 3
	s_and_b32 s13, s13, 0x7fffff80
	s_addk_i32 s13, 0xf800
	v_or_b32_e32 v98, s13, v134
	v_mov_b32_e32 v99, v129
	v_lshlrev_b64 v[98:99], 12, v[98:99]
	v_lshl_add_u64 v[98:99], s[10:11], 0, v[98:99]
	s_lshl_b32 s10, s44, 2
	s_mov_b32 s11, s7
	v_lshl_add_u64 v[98:99], v[98:99], 0, s[10:11]
	s_add_u32 s10, s16, s14
	s_addc_u32 s11, s17, s15
	s_add_u32 s10, s10, s13
	s_addc_u32 s11, s11, 0
	s_movk_i32 s13, 0x400
	s_cbranch_execnz .LBB0_3207
	s_branch .LBB0_3211
